# K-loops: the s_setprio 0 / s_setprio 1 pair in the middle of each 32-MFMA block removed (priority stays raised through the block)
# speedup vs baseline: 1.0041x; 1.0041x over previous
; #define LAS __attribute__((address_space(3)))
; #define PG8_STAGE(bufoff, gbase, voff) do { _Pragma("unroll") for (int _i = 0; _i < 2; ++_i) \
;         __builtin_amdgcn_global_load_lds((const unsigned*)((const char*)(gbase) + (voff)[_i]), (LAS unsigned*)(lds + (bufoff) + ldsw + _i * 8192), 16, 0, 0); } while (0)
; #define PG8_LDA(dst, b, h) do { _Pragma("unroll") for (int m = 0; m < 4; ++m) PG8_LD2(dst[m], PG8_SA(b, h) + aoff + m * 2048); } while (0)
; #define PG8_LDB(dst, b, h) do { _Pragma("unroll") for (int n = 0; n < 2; ++n) PG8_LD2(dst[n], PG8_SB(b, h) + boff + n * 2048); } while (0)
; #define PG8_BAR __builtin_amdgcn_s_barrier()
; template <int DT  , class Epi, class Sched, class Hook = NoHook>
; __device__ __forceinline__ void gemm_phase(LAS unsigned char* lds, const Sched& S, const Epi& E, int wave_s, LAS unsigned char* aux  ,
;                                            const Hook& H = Hook()  ) {
;     ...
;         const bool has_next = S.next(ui + 1, nxt);
;         const char* nA = has_next ? S.aptr(nxt) : cA; const char* nB = has_next ? S.bptr(nxt) : cB;
;         {
;             if constexpr (GATHER) { if (has_next && wid == 0) __builtin_amdgcn_global_load_lds((const unsigned*)(S.list_src(nxt) + 4 * lane), (LAS unsigned*)(aux + ((ui + 1) & 1) * 1024), 16, 0, 0); }
;             if constexpr (Epi::PREFETCH) E.prefetch(cur, aux + 2048 + (ui & 1) * 3072, wid, lane);
;         }
;         for (int t = 0; t < nt; t += 2) {
;             const bool last = (t == nt - 2);
;             const char* a1 = cA + (size_t)(t + 1) * kstep;
;             const char* a2 = last ? nA : cA + (size_t)(t + 2) * kstep; const char* b2 = last ? nB : cB + (size_t)(t + 2) * kstep;
;             const char* a3 = a2 + kstep; const char* b3 = b2 + kstep;
;             PG8_LDB(B0, 0, 0); PG8_LDB(B1, 0, 1); PG8_SCHED; PG8_LDA(At, 0, 0); PG8_STAGE_A(PG8_SA(1, 1), 1, a1);
;             if (GATHER) { if (last && has_next) S.gather_lds(nxt, gA, tid, aux + ((ui + 1) & 1) * 1024); }
;             PG8_WAIT_V(8); PG8_WAIT_L(0); PG8_BAR; PG8_MMA(0, 0, At, B0); PG8_MMA(0, 1, At, B1); PG8_BAR; PG8_SCHED;
;             PG8_LDA(At, 0, 1); PG8_STAGE(PG8_SB(0, 0), b2, voffB); PG8_STAGE(PG8_SB(0, 1), b2 + hstep, voffB); PG8_STAGE_A(PG8_SA(0, 0), 0, a2);
;             PG8_WAIT_V(8); PG8_WAIT_L(0); PG8_BAR; PG8_MMA(1, 0, At, B0); PG8_MMA(1, 1, At, B1); PG8_BAR; PG8_SCHED;
.LBB0_118:
	s_ashr_i32 s29, s28, 31
	s_lshl_b64 s[30:31], s[28:29], 18
	s_add_u32 s30, s36, s30
	s_addc_u32 s31, s37, s31
	s_and_b64 s[34:35], s[2:3], exec
	s_cselect_b32 s29, s31, s47
	s_cselect_b32 s41, s30, s46
	s_ashr_i32 s27, s26, 31
	s_lshl_b64 s[34:35], s[26:27], 18
	s_add_u32 s34, s67, s34
	s_addc_u32 s35, s20, s35
	s_and_b64 s[72:73], s[2:3], exec
	s_cselect_b32 s27, s35, s19
	s_cselect_b32 s68, s34, s18
	s_add_u32 s46, s46, 0x20080
	s_addc_u32 s47, s47, 0
	s_add_u32 s76, s18, 0x100
	s_addc_u32 s77, s19, 0
	s_mov_b32 vcc_lo, -2
	ds_read_b128 v[130:133], v168
	ds_read_b128 v[134:137], v169
	ds_read_b128 v[138:141], v164
	ds_read_b128 v[142:145], v165
	ds_read_b128 v[158:161], v170
	ds_read_b128 v[182:185], v171
	ds_read_b128 v[186:189], v172
	ds_read_b128 v[190:193], v173
	s_add_u32 s18, s46, 0xfffe0080
	s_addc_u32 s19, s47, -1
	s_cmp_eq_u32 vcc_lo, 4
	s_cselect_b32 s73, s29, s19
	s_cselect_b32 s72, s41, s18
	s_cselect_b32 s19, s27, s77
	s_cselect_b32 s18, s68, s76
	v_lshl_add_u64 v[162:163], s[46:47], 0, v[154:155]
	s_add_i32 m0, s11, 0xc000
	ds_read_b128 v[196:199], v181
	ds_read_b128 v[204:207], v181 offset:1024
	ds_read_b128 v[208:211], v181 offset:2048
	ds_read_b128 v[212:215], v181 offset:3072
	ds_read_b128 v[216:219], v181 offset:4096
	ds_read_b128 v[226:229], v181 offset:5120
	ds_read_b128 v[230:233], v181 offset:6144
	ds_read_b128 v[234:237], v181 offset:7168
	global_load_lds_dwordx4 v[162:163], off
	v_lshl_add_u64 v[162:163], s[46:47], 0, v[156:157]
	s_add_i32 m0, s11, 0xe000
	s_nop 0
	global_load_lds_dwordx4 v[162:163], off
	s_waitcnt vmcnt(8)
	s_waitcnt lgkmcnt(0)
	s_barrier
	s_setprio 1
	s_waitcnt lgkmcnt(0)
	v_mfma_i32_16x16x64_i8 v[126:129], v[138:141], v[196:199], 0
	v_mfma_i32_16x16x64_i8 v[122:125], v[134:137], v[196:199], 0
	v_mfma_i32_16x16x64_i8 v[110:113], v[138:141], v[208:211], 0
	v_mfma_i32_16x16x64_i8 v[106:109], v[134:137], v[208:211], 0
	v_mfma_i32_16x16x64_i8 v[94:97], v[138:141], v[216:219], 0
	v_mfma_i32_16x16x64_i8 v[90:93], v[134:137], v[216:219], 0
	v_mfma_i32_16x16x64_i8 v[78:81], v[138:141], v[230:233], 0
	v_mfma_i32_16x16x64_i8 v[74:77], v[134:137], v[230:233], 0
	v_mfma_i32_16x16x64_i8 v[126:129], v[130:133], v[204:207], v[126:129]
	v_mfma_i32_16x16x64_i8 v[122:125], v[158:161], v[204:207], v[122:125]
	v_mfma_i32_16x16x64_i8 v[110:113], v[130:133], v[212:215], v[110:113]
	v_mfma_i32_16x16x64_i8 v[106:109], v[158:161], v[212:215], v[106:109]
	v_mfma_i32_16x16x64_i8 v[94:97], v[130:133], v[226:229], v[94:97]
	v_mfma_i32_16x16x64_i8 v[90:93], v[158:161], v[226:229], v[90:93]
	v_mfma_i32_16x16x64_i8 v[78:81], v[130:133], v[234:237], v[78:81]
	v_mfma_i32_16x16x64_i8 v[74:77], v[158:161], v[234:237], v[74:77]
	v_mfma_i32_16x16x64_i8 v[118:121], v[142:145], v[196:199], 0
	v_mfma_i32_16x16x64_i8 v[114:117], v[186:189], v[196:199], 0
	v_mfma_i32_16x16x64_i8 v[102:105], v[142:145], v[208:211], 0
	v_mfma_i32_16x16x64_i8 v[98:101], v[186:189], v[208:211], 0
	v_mfma_i32_16x16x64_i8 v[86:89], v[142:145], v[216:219], 0
	v_mfma_i32_16x16x64_i8 v[82:85], v[186:189], v[216:219], 0
	v_mfma_i32_16x16x64_i8 v[70:73], v[142:145], v[230:233], 0
	v_mfma_i32_16x16x64_i8 v[66:69], v[186:189], v[230:233], 0
	v_mfma_i32_16x16x64_i8 v[118:121], v[182:185], v[204:207], v[118:121]
	v_mfma_i32_16x16x64_i8 v[114:117], v[190:193], v[204:207], v[114:117]
	v_mfma_i32_16x16x64_i8 v[102:105], v[182:185], v[212:215], v[102:105]
	v_mfma_i32_16x16x64_i8 v[98:101], v[190:193], v[212:215], v[98:101]
	v_mfma_i32_16x16x64_i8 v[86:89], v[182:185], v[226:229], v[86:89]
	v_mfma_i32_16x16x64_i8 v[82:85], v[190:193], v[226:229], v[82:85]
	v_mfma_i32_16x16x64_i8 v[70:73], v[182:185], v[234:237], v[70:73]
	v_mfma_i32_16x16x64_i8 v[66:69], v[190:193], v[234:237], v[66:69]
	s_setprio 0
	s_barrier
	s_mov_b32 m0, s12
	v_lshl_add_u64 v[162:163], s[18:19], 0, v[150:151]
	s_add_u32 s42, s18, 0x20000
	ds_read_b128 v[196:199], v181 offset:16384
	ds_read_b128 v[204:207], v181 offset:17408
	ds_read_b128 v[208:211], v181 offset:18432
	ds_read_b128 v[212:215], v181 offset:19456
	ds_read_b128 v[216:219], v181 offset:20480
	ds_read_b128 v[226:229], v181 offset:21504
	ds_read_b128 v[230:233], v181 offset:22528
	ds_read_b128 v[234:237], v181 offset:23552
	global_load_lds_dwordx4 v[162:163], off
	v_lshl_add_u64 v[200:201], s[18:19], 0, v[146:147]
	s_mov_b32 m0, s13
	s_addc_u32 s43, s19, 0
	global_load_lds_dwordx4 v[200:201], off
	v_lshl_add_u64 v[238:239], s[42:43], 0, v[150:151]
	s_mov_b32 m0, s38
	v_lshl_add_u64 v[240:241], s[72:73], 0, v[148:149]
	global_load_lds_dwordx4 v[238:239], off
	v_lshl_add_u64 v[238:239], s[42:43], 0, v[146:147]
	s_mov_b32 m0, s51
	s_nop 0
	global_load_lds_dwordx4 v[238:239], off
	v_lshl_add_u64 v[238:239], s[72:73], 0, v[152:153]
	s_mov_b32 m0, s11
	s_nop 0
	global_load_lds_dwordx4 v[238:239], off
	s_mov_b32 m0, s89
	s_nop 0
	global_load_lds_dwordx4 v[240:241], off
	s_waitcnt vmcnt(8)
	s_waitcnt lgkmcnt(0)
	s_barrier
; #define PG8_STAGE_A(bufoff, h, abase) do { _Pragma("unroll") for (int _i = 0; _i < 2; ++_i) { \
;         const char* _src = GATHER ? ((const char*)(abase) + gA[h][_i]) : ((const char*)(abase) + (size_t)(h) * hstep + voffA[_i]); \
;         __builtin_amdgcn_global_load_lds((const unsigned*)_src, (LAS unsigned*)(lds + (bufoff) + ldsw + _i * 8192), 16, 0, 0); } } while (0)
; #define PG8_LDA(dst, b, h) do { _Pragma("unroll") for (int m = 0; m < 4; ++m) PG8_LD2(dst[m], PG8_SA(b, h) + aoff + m * 2048); } while (0)
; #define PG8_LDB(dst, b, h) do { _Pragma("unroll") for (int n = 0; n < 2; ++n) PG8_LD2(dst[n], PG8_SB(b, h) + boff + n * 2048); } while (0)
; #define PG8_WAIT_V(n) asm volatile("s_waitcnt vmcnt(" #n ")" ::: "memory")
; #define PG8_WAIT_L(n) asm volatile("s_waitcnt lgkmcnt(" #n ")" ::: "memory")
; #define PG8_BAR __builtin_amdgcn_s_barrier()
; #define PG8_SCHED __builtin_amdgcn_sched_barrier(0)
; template <int DT  , class Epi, class Sched, class Hook = NoHook>
; __device__ __forceinline__ void gemm_phase(LAS unsigned char* lds, const Sched& S, const Epi& E, int wave_s, LAS unsigned char* aux  ,
;                                            const Hook& H = Hook()  ) {
;     ...
;             PG8_WAIT_V(8); PG8_WAIT_L(0); PG8_BAR; PG8_MMA(1, 0, At, B0); PG8_MMA(1, 1, At, B1); PG8_BAR; PG8_SCHED;
;             PG8_LDB(B0, 1, 0); PG8_LDB(B1, 1, 1); PG8_SCHED; PG8_LDA(At, 1, 0); PG8_STAGE_A(PG8_SA(0, 1), 1, a2);
;             PG8_WAIT_V(8); PG8_WAIT_L(0); PG8_BAR; PG8_MMA(0, 0, At, B0); PG8_MMA(0, 1, At, B1); PG8_BAR; PG8_SCHED;
	s_setprio 1
	s_waitcnt lgkmcnt(0)
	v_mfma_i32_16x16x64_i8 v[54:57], v[138:141], v[196:199], 0
	v_mfma_i32_16x16x64_i8 v[50:53], v[134:137], v[196:199], 0
	v_mfma_i32_16x16x64_i8 v[38:41], v[138:141], v[208:211], 0
	v_mfma_i32_16x16x64_i8 v[34:37], v[134:137], v[208:211], 0
	v_mfma_i32_16x16x64_i8 v[20:23], v[138:141], v[216:219], 0
	v_mfma_i32_16x16x64_i8 v[16:19], v[134:137], v[216:219], 0
	v_mfma_i32_16x16x64_i8 v[4:7], v[138:141], v[230:233], 0
	v_mfma_i32_16x16x64_i8 v[0:3], v[134:137], v[230:233], 0
	v_mfma_i32_16x16x64_i8 v[54:57], v[130:133], v[204:207], v[54:57]
	v_mfma_i32_16x16x64_i8 v[50:53], v[158:161], v[204:207], v[50:53]
	v_mfma_i32_16x16x64_i8 v[38:41], v[130:133], v[212:215], v[38:41]
	v_mfma_i32_16x16x64_i8 v[34:37], v[158:161], v[212:215], v[34:37]
	v_mfma_i32_16x16x64_i8 v[20:23], v[130:133], v[226:229], v[20:23]
	v_mfma_i32_16x16x64_i8 v[16:19], v[158:161], v[226:229], v[16:19]
	v_mfma_i32_16x16x64_i8 v[4:7], v[130:133], v[234:237], v[4:7]
	v_mfma_i32_16x16x64_i8 v[0:3], v[158:161], v[234:237], v[0:3]
	v_mfma_i32_16x16x64_i8 v[62:65], v[142:145], v[196:199], 0
	v_mfma_i32_16x16x64_i8 v[58:61], v[186:189], v[196:199], 0
	v_mfma_i32_16x16x64_i8 v[46:49], v[142:145], v[208:211], 0
	v_mfma_i32_16x16x64_i8 v[42:45], v[186:189], v[208:211], 0
	v_mfma_i32_16x16x64_i8 v[28:31], v[142:145], v[216:219], 0
	v_mfma_i32_16x16x64_i8 v[24:27], v[186:189], v[216:219], 0
	v_mfma_i32_16x16x64_i8 v[12:15], v[142:145], v[230:233], 0
	v_mfma_i32_16x16x64_i8 v[8:11], v[186:189], v[230:233], 0
	v_mfma_i32_16x16x64_i8 v[62:65], v[182:185], v[204:207], v[62:65]
	v_mfma_i32_16x16x64_i8 v[58:61], v[190:193], v[204:207], v[58:61]
	v_mfma_i32_16x16x64_i8 v[46:49], v[182:185], v[212:215], v[46:49]
	v_mfma_i32_16x16x64_i8 v[42:45], v[190:193], v[212:215], v[42:45]
	v_mfma_i32_16x16x64_i8 v[28:31], v[182:185], v[226:229], v[28:31]
	v_mfma_i32_16x16x64_i8 v[24:27], v[190:193], v[226:229], v[24:27]
	v_mfma_i32_16x16x64_i8 v[12:15], v[182:185], v[234:237], v[12:15]
	v_mfma_i32_16x16x64_i8 v[8:11], v[190:193], v[234:237], v[8:11]
	s_setprio 0
	s_barrier
	ds_read_b128 v[130:133], v174
	ds_read_b128 v[134:137], v175
	ds_read_b128 v[138:141], v166
	ds_read_b128 v[142:145], v167
	ds_read_b128 v[158:161], v176
	ds_read_b128 v[182:185], v177
	ds_read_b128 v[186:189], v178
	ds_read_b128 v[190:193], v179
	s_add_u32 s42, s72, 0x20000
	s_addc_u32 s43, s73, 0
	s_mov_b32 m0, s65
	v_lshl_add_u64 v[242:243], s[42:43], 0, v[152:153]
	ds_read_b128 v[196:199], v181 offset:32768
	ds_read_b128 v[204:207], v181 offset:33792
	ds_read_b128 v[208:211], v181 offset:34816
	ds_read_b128 v[212:215], v181 offset:35840
	ds_read_b128 v[216:219], v181 offset:36864
	ds_read_b128 v[226:229], v181 offset:37888
	ds_read_b128 v[230:233], v181 offset:38912
	ds_read_b128 v[234:237], v181 offset:39936
	global_load_lds_dwordx4 v[242:243], off
	v_lshl_add_u64 v[242:243], s[42:43], 0, v[148:149]
	s_mov_b32 m0, s97
	s_nop 0
	global_load_lds_dwordx4 v[242:243], off
	s_waitcnt vmcnt(8)
	s_waitcnt lgkmcnt(0)
	s_barrier
	s_setprio 1
	s_waitcnt lgkmcnt(0)
	v_mfma_i32_16x16x64_i8 v[126:129], v[138:141], v[196:199], v[126:129]
	v_mfma_i32_16x16x64_i8 v[122:125], v[134:137], v[196:199], v[122:125]
	v_mfma_i32_16x16x64_i8 v[110:113], v[138:141], v[208:211], v[110:113]
	v_mfma_i32_16x16x64_i8 v[106:109], v[134:137], v[208:211], v[106:109]
	v_mfma_i32_16x16x64_i8 v[94:97], v[138:141], v[216:219], v[94:97]
	v_mfma_i32_16x16x64_i8 v[90:93], v[134:137], v[216:219], v[90:93]
	v_mfma_i32_16x16x64_i8 v[78:81], v[138:141], v[230:233], v[78:81]
	v_mfma_i32_16x16x64_i8 v[74:77], v[134:137], v[230:233], v[74:77]
	v_mfma_i32_16x16x64_i8 v[126:129], v[130:133], v[204:207], v[126:129]
	v_mfma_i32_16x16x64_i8 v[122:125], v[158:161], v[204:207], v[122:125]
	v_mfma_i32_16x16x64_i8 v[110:113], v[130:133], v[212:215], v[110:113]
	v_mfma_i32_16x16x64_i8 v[106:109], v[158:161], v[212:215], v[106:109]
	v_mfma_i32_16x16x64_i8 v[94:97], v[130:133], v[226:229], v[94:97]
	v_mfma_i32_16x16x64_i8 v[90:93], v[158:161], v[226:229], v[90:93]
	v_mfma_i32_16x16x64_i8 v[78:81], v[130:133], v[234:237], v[78:81]
	v_mfma_i32_16x16x64_i8 v[74:77], v[158:161], v[234:237], v[74:77]
	v_mfma_i32_16x16x64_i8 v[118:121], v[142:145], v[196:199], v[118:121]
	v_mfma_i32_16x16x64_i8 v[114:117], v[186:189], v[196:199], v[114:117]
	v_mfma_i32_16x16x64_i8 v[102:105], v[142:145], v[208:211], v[102:105]
	v_mfma_i32_16x16x64_i8 v[98:101], v[186:189], v[208:211], v[98:101]
	v_mfma_i32_16x16x64_i8 v[86:89], v[142:145], v[216:219], v[86:89]
	v_mfma_i32_16x16x64_i8 v[82:85], v[186:189], v[216:219], v[82:85]
	v_mfma_i32_16x16x64_i8 v[70:73], v[142:145], v[230:233], v[70:73]
	v_mfma_i32_16x16x64_i8 v[66:69], v[186:189], v[230:233], v[66:69]
	v_mfma_i32_16x16x64_i8 v[118:121], v[182:185], v[204:207], v[118:121]
	v_mfma_i32_16x16x64_i8 v[114:117], v[190:193], v[204:207], v[114:117]
	v_mfma_i32_16x16x64_i8 v[102:105], v[182:185], v[212:215], v[102:105]
	v_mfma_i32_16x16x64_i8 v[98:101], v[190:193], v[212:215], v[98:101]
	v_mfma_i32_16x16x64_i8 v[86:89], v[182:185], v[226:229], v[86:89]
	v_mfma_i32_16x16x64_i8 v[82:85], v[190:193], v[226:229], v[82:85]
	v_mfma_i32_16x16x64_i8 v[70:73], v[182:185], v[234:237], v[70:73]
	v_mfma_i32_16x16x64_i8 v[66:69], v[190:193], v[234:237], v[66:69]
	s_setprio 0
	s_barrier
; #define PG8_STAGE(bufoff, gbase, voff) do { _Pragma("unroll") for (int _i = 0; _i < 2; ++_i) \
;         __builtin_amdgcn_global_load_lds((const unsigned*)((const char*)(gbase) + (voff)[_i]), (LAS unsigned*)(lds + (bufoff) + ldsw + _i * 8192), 16, 0, 0); } while (0)
; #define PG8_STAGE_A(bufoff, h, abase) do { _Pragma("unroll") for (int _i = 0; _i < 2; ++_i) { \
;         const char* _src = GATHER ? ((const char*)(abase) + gA[h][_i]) : ((const char*)(abase) + (size_t)(h) * hstep + voffA[_i]); \
;         __builtin_amdgcn_global_load_lds((const unsigned*)_src, (LAS unsigned*)(lds + (bufoff) + ldsw + _i * 8192), 16, 0, 0); } } while (0)
; template <int DT  , class Epi, class Sched, class Hook = NoHook>
; __device__ __forceinline__ void gemm_phase(LAS unsigned char* lds, const Sched& S, const Epi& E, int wave_s, LAS unsigned char* aux  ,
;                                            const Hook& H = Hook()  ) {
;     ...
;         for (int t = 0; t < nt; t += 2) {
;             const bool last = (t == nt - 2);
;             const char* a1 = cA + (size_t)(t + 1) * kstep;
;             const char* a2 = last ? nA : cA + (size_t)(t + 2) * kstep; const char* b2 = last ? nB : cB + (size_t)(t + 2) * kstep;
;             const char* a3 = a2 + kstep; const char* b3 = b2 + kstep;
;             PG8_LDB(B0, 0, 0); PG8_LDB(B1, 0, 1); PG8_SCHED; PG8_LDA(At, 0, 0); PG8_STAGE_A(PG8_SA(1, 1), 1, a1);
;             if (GATHER) { if (last && has_next) S.gather_lds(nxt, gA, tid, aux + ((ui + 1) & 1) * 1024); }
;             PG8_WAIT_V(8); PG8_WAIT_L(0); PG8_BAR; PG8_MMA(0, 0, At, B0); PG8_MMA(0, 1, At, B1); PG8_BAR; PG8_SCHED;
;             PG8_LDA(At, 0, 1); PG8_STAGE(PG8_SB(0, 0), b2, voffB); PG8_STAGE(PG8_SB(0, 1), b2 + hstep, voffB); PG8_STAGE_A(PG8_SA(0, 0), 0, a2);
;             PG8_WAIT_V(8); PG8_WAIT_L(0); PG8_BAR; PG8_MMA(1, 0, At, B0); PG8_MMA(1, 1, At, B1); PG8_BAR; PG8_SCHED;
;             PG8_LDB(B0, 1, 0); PG8_LDB(B1, 1, 1); PG8_SCHED; PG8_LDA(At, 1, 0); PG8_STAGE_A(PG8_SA(0, 1), 1, a2);
;             PG8_WAIT_V(8); PG8_WAIT_L(0); PG8_BAR; PG8_MMA(0, 0, At, B0); PG8_MMA(0, 1, At, B1); PG8_BAR; PG8_SCHED;
;             PG8_LDA(At, 1, 1); PG8_STAGE(PG8_SB(1, 0), b3, voffB); PG8_STAGE(PG8_SB(1, 1), b3 + hstep, voffB); PG8_STAGE_A(PG8_SA(1, 0), 0, a3);
;             PG8_WAIT_V(8); PG8_WAIT_L(0); PG8_BAR; PG8_MMA(1, 0, At, B0); PG8_MMA(1, 1, At, B1); PG8_BAR; PG8_SCHED;
	s_mov_b32 m0, s57
	v_lshl_add_u64 v[162:163], v[162:163], 0, s[58:59]
	s_add_u32 s18, s18, 0x20080
	ds_read_b128 v[196:199], v181 offset:49152
	ds_read_b128 v[204:207], v181 offset:50176
	ds_read_b128 v[208:211], v181 offset:51200
	ds_read_b128 v[212:215], v181 offset:52224
	ds_read_b128 v[216:219], v181 offset:53248
	ds_read_b128 v[226:229], v181 offset:54272
	ds_read_b128 v[230:233], v181 offset:55296
	ds_read_b128 v[234:237], v181 offset:56320
	global_load_lds_dwordx4 v[162:163], off
	v_lshl_add_u64 v[162:163], v[200:201], 0, s[58:59]
	s_mov_b32 m0, s10
	s_addc_u32 s19, s19, 0
	global_load_lds_dwordx4 v[162:163], off
	v_lshl_add_u64 v[162:163], s[18:19], 0, v[150:151]
	s_mov_b32 m0, s48
	s_nop 0
	global_load_lds_dwordx4 v[162:163], off
	v_lshl_add_u64 v[162:163], s[18:19], 0, v[146:147]
	s_mov_b32 m0, s44
	s_nop 0
	global_load_lds_dwordx4 v[162:163], off
	v_lshl_add_u64 v[162:163], v[238:239], 0, s[58:59]
	s_mov_b32 m0, s94
	s_nop 0
	global_load_lds_dwordx4 v[162:163], off
	v_lshl_add_u64 v[162:163], v[240:241], 0, s[58:59]
	s_mov_b32 m0, s95
	s_nop 0
	global_load_lds_dwordx4 v[162:163], off
	s_waitcnt vmcnt(8)
	s_waitcnt lgkmcnt(0)
	s_barrier
	s_setprio 1
	s_waitcnt lgkmcnt(0)
	v_mfma_i32_16x16x64_i8 v[54:57], v[138:141], v[196:199], v[54:57]
	v_mfma_i32_16x16x64_i8 v[50:53], v[134:137], v[196:199], v[50:53]
	v_mfma_i32_16x16x64_i8 v[38:41], v[138:141], v[208:211], v[38:41]
	v_mfma_i32_16x16x64_i8 v[34:37], v[134:137], v[208:211], v[34:37]
	v_mfma_i32_16x16x64_i8 v[20:23], v[138:141], v[216:219], v[20:23]
	v_mfma_i32_16x16x64_i8 v[16:19], v[134:137], v[216:219], v[16:19]
	v_mfma_i32_16x16x64_i8 v[4:7], v[138:141], v[230:233], v[4:7]
	v_mfma_i32_16x16x64_i8 v[0:3], v[134:137], v[230:233], v[0:3]
	v_mfma_i32_16x16x64_i8 v[54:57], v[130:133], v[204:207], v[54:57]
	v_mfma_i32_16x16x64_i8 v[50:53], v[158:161], v[204:207], v[50:53]
	v_mfma_i32_16x16x64_i8 v[38:41], v[130:133], v[212:215], v[38:41]
	v_mfma_i32_16x16x64_i8 v[34:37], v[158:161], v[212:215], v[34:37]
	v_mfma_i32_16x16x64_i8 v[20:23], v[130:133], v[226:229], v[20:23]
	v_mfma_i32_16x16x64_i8 v[16:19], v[158:161], v[226:229], v[16:19]
	v_mfma_i32_16x16x64_i8 v[4:7], v[130:133], v[234:237], v[4:7]
	v_mfma_i32_16x16x64_i8 v[0:3], v[158:161], v[234:237], v[0:3]
	v_mfma_i32_16x16x64_i8 v[62:65], v[142:145], v[196:199], v[62:65]
	v_mfma_i32_16x16x64_i8 v[58:61], v[186:189], v[196:199], v[58:61]
	v_mfma_i32_16x16x64_i8 v[46:49], v[142:145], v[208:211], v[46:49]
	v_mfma_i32_16x16x64_i8 v[42:45], v[186:189], v[208:211], v[42:45]
	v_mfma_i32_16x16x64_i8 v[28:31], v[142:145], v[216:219], v[28:31]
	v_mfma_i32_16x16x64_i8 v[24:27], v[186:189], v[216:219], v[24:27]
	v_mfma_i32_16x16x64_i8 v[12:15], v[142:145], v[230:233], v[12:15]
	v_mfma_i32_16x16x64_i8 v[8:11], v[186:189], v[230:233], v[8:11]
	v_mfma_i32_16x16x64_i8 v[62:65], v[182:185], v[204:207], v[62:65]
	v_mfma_i32_16x16x64_i8 v[58:61], v[190:193], v[204:207], v[58:61]
	v_mfma_i32_16x16x64_i8 v[46:49], v[182:185], v[212:215], v[46:49]
	v_mfma_i32_16x16x64_i8 v[42:45], v[190:193], v[212:215], v[42:45]
	v_mfma_i32_16x16x64_i8 v[28:31], v[182:185], v[226:229], v[28:31]
	v_mfma_i32_16x16x64_i8 v[24:27], v[190:193], v[226:229], v[24:27]
	v_mfma_i32_16x16x64_i8 v[12:15], v[182:185], v[234:237], v[12:15]
	v_mfma_i32_16x16x64_i8 v[8:11], v[190:193], v[234:237], v[8:11]
	s_setprio 0
	s_barrier
	s_add_i32 vcc_lo, vcc_lo, 2
	s_add_u32 s46, s46, 0x100
	s_addc_u32 s47, s47, 0
	s_add_u32 s76, s76, 0x100
	s_addc_u32 s77, s77, 0
	s_cmp_gt_u32 vcc_lo, 5
.LBB0_119:
	ds_read_b128 v[130:133], v168
	ds_read_b128 v[134:137], v169
	ds_read_b128 v[138:141], v164
	ds_read_b128 v[142:145], v165
	ds_read_b128 v[158:161], v170
	ds_read_b128 v[182:185], v171
	ds_read_b128 v[186:189], v172
	ds_read_b128 v[190:193], v173
	s_add_u32 s18, s46, 0xfffe0080
	s_addc_u32 s19, s47, -1
	s_cmp_eq_u32 vcc_lo, 4
	s_cselect_b32 s73, s29, s19
	s_cselect_b32 s72, s41, s18
	s_cselect_b32 s19, s27, s77
	s_cselect_b32 s18, s68, s76
	v_lshl_add_u64 v[162:163], s[46:47], 0, v[154:155]
	s_add_i32 m0, s11, 0xc000
	ds_read_b128 v[196:199], v181
	ds_read_b128 v[204:207], v181 offset:1024
	ds_read_b128 v[208:211], v181 offset:2048
	ds_read_b128 v[212:215], v181 offset:3072
	ds_read_b128 v[216:219], v181 offset:4096
	ds_read_b128 v[226:229], v181 offset:5120
	ds_read_b128 v[230:233], v181 offset:6144
	ds_read_b128 v[234:237], v181 offset:7168
	global_load_lds_dwordx4 v[162:163], off
	v_lshl_add_u64 v[162:163], s[46:47], 0, v[156:157]
	s_add_i32 m0, s11, 0xe000
	s_nop 0
	global_load_lds_dwordx4 v[162:163], off
	s_waitcnt vmcnt(8)
	s_waitcnt lgkmcnt(0)
	s_barrier
; #define PG8_STAGE(bufoff, gbase, voff) do { _Pragma("unroll") for (int _i = 0; _i < 2; ++_i) \
;         __builtin_amdgcn_global_load_lds((const unsigned*)((const char*)(gbase) + (voff)[_i]), (LAS unsigned*)(lds + (bufoff) + ldsw + _i * 8192), 16, 0, 0); } while (0)
; #define PG8_STAGE_A(bufoff, h, abase) do { _Pragma("unroll") for (int _i = 0; _i < 2; ++_i) { \
;         const char* _src = GATHER ? ((const char*)(abase) + gA[h][_i]) : ((const char*)(abase) + (size_t)(h) * hstep + voffA[_i]); \
;         __builtin_amdgcn_global_load_lds((const unsigned*)_src, (LAS unsigned*)(lds + (bufoff) + ldsw + _i * 8192), 16, 0, 0); } } while (0)
; #define PG8_LDA(dst, b, h) do { _Pragma("unroll") for (int m = 0; m < 4; ++m) PG8_LD2(dst[m], PG8_SA(b, h) + aoff + m * 2048); } while (0)
; #define PG8_LDB(dst, b, h) do { _Pragma("unroll") for (int n = 0; n < 2; ++n) PG8_LD2(dst[n], PG8_SB(b, h) + boff + n * 2048); } while (0)
; #define PG8_WAIT_V(n) asm volatile("s_waitcnt vmcnt(" #n ")" ::: "memory")
; #define PG8_WAIT_L(n) asm volatile("s_waitcnt lgkmcnt(" #n ")" ::: "memory")
; #define PG8_BAR __builtin_amdgcn_s_barrier()
; #define PG8_SCHED __builtin_amdgcn_sched_barrier(0)
; template <int DT  , class Epi, class Sched, class Hook = NoHook>
; __device__ __forceinline__ void gemm_phase(LAS unsigned char* lds, const Sched& S, const Epi& E, int wave_s, LAS unsigned char* aux  ,
;                                            const Hook& H = Hook()  ) {
;     ...
;             PG8_WAIT_V(8); PG8_WAIT_L(0); PG8_BAR; PG8_MMA(0, 0, At, B0); PG8_MMA(0, 1, At, B1); PG8_BAR; PG8_SCHED;
;             PG8_LDA(At, 0, 1); PG8_STAGE(PG8_SB(0, 0), b2, voffB); PG8_STAGE(PG8_SB(0, 1), b2 + hstep, voffB); PG8_STAGE_A(PG8_SA(0, 0), 0, a2);
;             PG8_WAIT_V(8); PG8_WAIT_L(0); PG8_BAR; PG8_MMA(1, 0, At, B0); PG8_MMA(1, 1, At, B1); PG8_BAR; PG8_SCHED;
;             PG8_LDB(B0, 1, 0); PG8_LDB(B1, 1, 1); PG8_SCHED; PG8_LDA(At, 1, 0); PG8_STAGE_A(PG8_SA(0, 1), 1, a2);
;             PG8_WAIT_V(8); PG8_WAIT_L(0); PG8_BAR; PG8_MMA(0, 0, At, B0); PG8_MMA(0, 1, At, B1); PG8_BAR; PG8_SCHED;
	s_setprio 1
	s_waitcnt lgkmcnt(0)
	v_mfma_i32_16x16x64_i8 v[126:129], v[138:141], v[196:199], v[126:129]
	v_mfma_i32_16x16x64_i8 v[122:125], v[134:137], v[196:199], v[122:125]
	v_mfma_i32_16x16x64_i8 v[110:113], v[138:141], v[208:211], v[110:113]
	v_mfma_i32_16x16x64_i8 v[106:109], v[134:137], v[208:211], v[106:109]
	v_mfma_i32_16x16x64_i8 v[94:97], v[138:141], v[216:219], v[94:97]
	v_mfma_i32_16x16x64_i8 v[90:93], v[134:137], v[216:219], v[90:93]
	v_mfma_i32_16x16x64_i8 v[78:81], v[138:141], v[230:233], v[78:81]
	v_mfma_i32_16x16x64_i8 v[74:77], v[134:137], v[230:233], v[74:77]
	v_mfma_i32_16x16x64_i8 v[126:129], v[130:133], v[204:207], v[126:129]
	v_mfma_i32_16x16x64_i8 v[122:125], v[158:161], v[204:207], v[122:125]
	v_mfma_i32_16x16x64_i8 v[110:113], v[130:133], v[212:215], v[110:113]
	v_mfma_i32_16x16x64_i8 v[106:109], v[158:161], v[212:215], v[106:109]
	v_mfma_i32_16x16x64_i8 v[94:97], v[130:133], v[226:229], v[94:97]
	v_mfma_i32_16x16x64_i8 v[90:93], v[158:161], v[226:229], v[90:93]
	v_mfma_i32_16x16x64_i8 v[78:81], v[130:133], v[234:237], v[78:81]
	v_mfma_i32_16x16x64_i8 v[74:77], v[158:161], v[234:237], v[74:77]
	v_mfma_i32_16x16x64_i8 v[118:121], v[142:145], v[196:199], v[118:121]
	v_mfma_i32_16x16x64_i8 v[114:117], v[186:189], v[196:199], v[114:117]
	v_mfma_i32_16x16x64_i8 v[102:105], v[142:145], v[208:211], v[102:105]
	v_mfma_i32_16x16x64_i8 v[98:101], v[186:189], v[208:211], v[98:101]
	v_mfma_i32_16x16x64_i8 v[86:89], v[142:145], v[216:219], v[86:89]
	v_mfma_i32_16x16x64_i8 v[82:85], v[186:189], v[216:219], v[82:85]
	v_mfma_i32_16x16x64_i8 v[70:73], v[142:145], v[230:233], v[70:73]
	v_mfma_i32_16x16x64_i8 v[66:69], v[186:189], v[230:233], v[66:69]
	v_mfma_i32_16x16x64_i8 v[118:121], v[182:185], v[204:207], v[118:121]
	v_mfma_i32_16x16x64_i8 v[114:117], v[190:193], v[204:207], v[114:117]
	v_mfma_i32_16x16x64_i8 v[102:105], v[182:185], v[212:215], v[102:105]
	v_mfma_i32_16x16x64_i8 v[98:101], v[190:193], v[212:215], v[98:101]
	v_mfma_i32_16x16x64_i8 v[86:89], v[182:185], v[226:229], v[86:89]
	v_mfma_i32_16x16x64_i8 v[82:85], v[190:193], v[226:229], v[82:85]
	v_mfma_i32_16x16x64_i8 v[70:73], v[182:185], v[234:237], v[70:73]
	v_mfma_i32_16x16x64_i8 v[66:69], v[190:193], v[234:237], v[66:69]
	s_setprio 0
	s_barrier
	s_mov_b32 m0, s12
	v_lshl_add_u64 v[162:163], s[18:19], 0, v[150:151]
	s_add_u32 s42, s18, 0x20000
	ds_read_b128 v[196:199], v181 offset:16384
	ds_read_b128 v[204:207], v181 offset:17408
	ds_read_b128 v[208:211], v181 offset:18432
	ds_read_b128 v[212:215], v181 offset:19456
	ds_read_b128 v[216:219], v181 offset:20480
	ds_read_b128 v[226:229], v181 offset:21504
	ds_read_b128 v[230:233], v181 offset:22528
	ds_read_b128 v[234:237], v181 offset:23552
	global_load_lds_dwordx4 v[162:163], off
	v_lshl_add_u64 v[200:201], s[18:19], 0, v[146:147]
	s_mov_b32 m0, s13
	s_addc_u32 s43, s19, 0
	global_load_lds_dwordx4 v[200:201], off
	v_lshl_add_u64 v[238:239], s[42:43], 0, v[150:151]
	s_mov_b32 m0, s38
	v_lshl_add_u64 v[240:241], s[72:73], 0, v[148:149]
	global_load_lds_dwordx4 v[238:239], off
	v_lshl_add_u64 v[238:239], s[42:43], 0, v[146:147]
	s_mov_b32 m0, s51
	s_nop 0
	global_load_lds_dwordx4 v[238:239], off
	v_lshl_add_u64 v[238:239], s[72:73], 0, v[152:153]
	s_mov_b32 m0, s11
	s_nop 0
	global_load_lds_dwordx4 v[238:239], off
	s_mov_b32 m0, s89
	s_nop 0
	global_load_lds_dwordx4 v[240:241], off
	s_waitcnt vmcnt(8)
	s_waitcnt lgkmcnt(0)
	s_barrier
	s_setprio 1
	s_waitcnt lgkmcnt(0)
	v_mfma_i32_16x16x64_i8 v[54:57], v[138:141], v[196:199], v[54:57]
	v_mfma_i32_16x16x64_i8 v[50:53], v[134:137], v[196:199], v[50:53]
	v_mfma_i32_16x16x64_i8 v[38:41], v[138:141], v[208:211], v[38:41]
	v_mfma_i32_16x16x64_i8 v[34:37], v[134:137], v[208:211], v[34:37]
	v_mfma_i32_16x16x64_i8 v[20:23], v[138:141], v[216:219], v[20:23]
	v_mfma_i32_16x16x64_i8 v[16:19], v[134:137], v[216:219], v[16:19]
	v_mfma_i32_16x16x64_i8 v[4:7], v[138:141], v[230:233], v[4:7]
	v_mfma_i32_16x16x64_i8 v[0:3], v[134:137], v[230:233], v[0:3]
	v_mfma_i32_16x16x64_i8 v[54:57], v[130:133], v[204:207], v[54:57]
	v_mfma_i32_16x16x64_i8 v[50:53], v[158:161], v[204:207], v[50:53]
	v_mfma_i32_16x16x64_i8 v[38:41], v[130:133], v[212:215], v[38:41]
	v_mfma_i32_16x16x64_i8 v[34:37], v[158:161], v[212:215], v[34:37]
	v_mfma_i32_16x16x64_i8 v[20:23], v[130:133], v[226:229], v[20:23]
	v_mfma_i32_16x16x64_i8 v[16:19], v[158:161], v[226:229], v[16:19]
	v_mfma_i32_16x16x64_i8 v[4:7], v[130:133], v[234:237], v[4:7]
	v_mfma_i32_16x16x64_i8 v[0:3], v[158:161], v[234:237], v[0:3]
	v_mfma_i32_16x16x64_i8 v[62:65], v[142:145], v[196:199], v[62:65]
	v_mfma_i32_16x16x64_i8 v[58:61], v[186:189], v[196:199], v[58:61]
	v_mfma_i32_16x16x64_i8 v[46:49], v[142:145], v[208:211], v[46:49]
	v_mfma_i32_16x16x64_i8 v[42:45], v[186:189], v[208:211], v[42:45]
	v_mfma_i32_16x16x64_i8 v[28:31], v[142:145], v[216:219], v[28:31]
	v_mfma_i32_16x16x64_i8 v[24:27], v[186:189], v[216:219], v[24:27]
	v_mfma_i32_16x16x64_i8 v[12:15], v[142:145], v[230:233], v[12:15]
	v_mfma_i32_16x16x64_i8 v[8:11], v[186:189], v[230:233], v[8:11]
	v_mfma_i32_16x16x64_i8 v[62:65], v[182:185], v[204:207], v[62:65]
	v_mfma_i32_16x16x64_i8 v[58:61], v[190:193], v[204:207], v[58:61]
	v_mfma_i32_16x16x64_i8 v[46:49], v[182:185], v[212:215], v[46:49]
	v_mfma_i32_16x16x64_i8 v[42:45], v[190:193], v[212:215], v[42:45]
	v_mfma_i32_16x16x64_i8 v[28:31], v[182:185], v[226:229], v[28:31]
	v_mfma_i32_16x16x64_i8 v[24:27], v[190:193], v[226:229], v[24:27]
	v_mfma_i32_16x16x64_i8 v[12:15], v[182:185], v[234:237], v[12:15]
	v_mfma_i32_16x16x64_i8 v[8:11], v[190:193], v[234:237], v[8:11]
	s_setprio 0
	s_barrier
; #define PG8_STAGE(bufoff, gbase, voff) do { _Pragma("unroll") for (int _i = 0; _i < 2; ++_i) \
;         __builtin_amdgcn_global_load_lds((const unsigned*)((const char*)(gbase) + (voff)[_i]), (LAS unsigned*)(lds + (bufoff) + ldsw + _i * 8192), 16, 0, 0); } while (0)
; #define PG8_STAGE_A(bufoff, h, abase) do { _Pragma("unroll") for (int _i = 0; _i < 2; ++_i) { \
;         const char* _src = GATHER ? ((const char*)(abase) + gA[h][_i]) : ((const char*)(abase) + (size_t)(h) * hstep + voffA[_i]); \
;         __builtin_amdgcn_global_load_lds((const unsigned*)_src, (LAS unsigned*)(lds + (bufoff) + ldsw + _i * 8192), 16, 0, 0); } } while (0)
; #define PG8_LDA(dst, b, h) do { _Pragma("unroll") for (int m = 0; m < 4; ++m) PG8_LD2(dst[m], PG8_SA(b, h) + aoff + m * 2048); } while (0)
; #define PG8_LDB(dst, b, h) do { _Pragma("unroll") for (int n = 0; n < 2; ++n) PG8_LD2(dst[n], PG8_SB(b, h) + boff + n * 2048); } while (0)
; #define PG8_WAIT_V(n) asm volatile("s_waitcnt vmcnt(" #n ")" ::: "memory")
; #define PG8_WAIT_L(n) asm volatile("s_waitcnt lgkmcnt(" #n ")" ::: "memory")
; #define PG8_BAR __builtin_amdgcn_s_barrier()
; #define PG8_SCHED __builtin_amdgcn_sched_barrier(0)
; template <int DT  , class Epi, class Sched, class Hook = NoHook>
; __device__ __forceinline__ void gemm_phase(LAS unsigned char* lds, const Sched& S, const Epi& E, int wave_s, LAS unsigned char* aux  ,
;                                            const Hook& H = Hook()  ) {
;     ...
;             PG8_LDB(B0, 1, 0); PG8_LDB(B1, 1, 1); PG8_SCHED; PG8_LDA(At, 1, 0); PG8_STAGE_A(PG8_SA(0, 1), 1, a2);
;             PG8_WAIT_V(8); PG8_WAIT_L(0); PG8_BAR; PG8_MMA(0, 0, At, B0); PG8_MMA(0, 1, At, B1); PG8_BAR; PG8_SCHED;
;             PG8_LDA(At, 1, 1); PG8_STAGE(PG8_SB(1, 0), b3, voffB); PG8_STAGE(PG8_SB(1, 1), b3 + hstep, voffB); PG8_STAGE_A(PG8_SA(1, 0), 0, a3);
;             PG8_WAIT_V(8); PG8_WAIT_L(0); PG8_BAR; PG8_MMA(1, 0, At, B0); PG8_MMA(1, 1, At, B1); PG8_BAR; PG8_SCHED;
;         }
;         if (wr == 0) PG8_BAR;
	ds_read_b128 v[130:133], v174
	ds_read_b128 v[134:137], v175
	ds_read_b128 v[138:141], v166
	ds_read_b128 v[142:145], v167
	ds_read_b128 v[158:161], v176
	ds_read_b128 v[182:185], v177
	ds_read_b128 v[186:189], v178
	ds_read_b128 v[190:193], v179
	s_add_u32 s42, s72, 0x20000
	s_addc_u32 s43, s73, 0
	s_mov_b32 m0, s65
	v_lshl_add_u64 v[242:243], s[42:43], 0, v[152:153]
	ds_read_b128 v[196:199], v181 offset:32768
	ds_read_b128 v[204:207], v181 offset:33792
	ds_read_b128 v[208:211], v181 offset:34816
	ds_read_b128 v[212:215], v181 offset:35840
	ds_read_b128 v[216:219], v181 offset:36864
	ds_read_b128 v[226:229], v181 offset:37888
	ds_read_b128 v[230:233], v181 offset:38912
	ds_read_b128 v[234:237], v181 offset:39936
	global_load_lds_dwordx4 v[242:243], off
	v_lshl_add_u64 v[242:243], s[42:43], 0, v[148:149]
	s_mov_b32 m0, s97
	s_nop 0
	global_load_lds_dwordx4 v[242:243], off
	s_waitcnt vmcnt(8)
	s_waitcnt lgkmcnt(0)
	s_barrier
	s_setprio 1
	s_waitcnt lgkmcnt(0)
	v_mfma_i32_16x16x64_i8 v[126:129], v[138:141], v[196:199], v[126:129]
	v_mfma_i32_16x16x64_i8 v[122:125], v[134:137], v[196:199], v[122:125]
	v_mfma_i32_16x16x64_i8 v[110:113], v[138:141], v[208:211], v[110:113]
	v_mfma_i32_16x16x64_i8 v[106:109], v[134:137], v[208:211], v[106:109]
	v_mfma_i32_16x16x64_i8 v[94:97], v[138:141], v[216:219], v[94:97]
	v_mfma_i32_16x16x64_i8 v[90:93], v[134:137], v[216:219], v[90:93]
	v_mfma_i32_16x16x64_i8 v[78:81], v[138:141], v[230:233], v[78:81]
	v_mfma_i32_16x16x64_i8 v[74:77], v[134:137], v[230:233], v[74:77]
	v_mfma_i32_16x16x64_i8 v[126:129], v[130:133], v[204:207], v[126:129]
	v_mfma_i32_16x16x64_i8 v[122:125], v[158:161], v[204:207], v[122:125]
	v_mfma_i32_16x16x64_i8 v[110:113], v[130:133], v[212:215], v[110:113]
	v_mfma_i32_16x16x64_i8 v[106:109], v[158:161], v[212:215], v[106:109]
	v_mfma_i32_16x16x64_i8 v[94:97], v[130:133], v[226:229], v[94:97]
	v_mfma_i32_16x16x64_i8 v[90:93], v[158:161], v[226:229], v[90:93]
	v_mfma_i32_16x16x64_i8 v[78:81], v[130:133], v[234:237], v[78:81]
	v_mfma_i32_16x16x64_i8 v[74:77], v[158:161], v[234:237], v[74:77]
	v_mfma_i32_16x16x64_i8 v[118:121], v[142:145], v[196:199], v[118:121]
	v_mfma_i32_16x16x64_i8 v[114:117], v[186:189], v[196:199], v[114:117]
	v_mfma_i32_16x16x64_i8 v[102:105], v[142:145], v[208:211], v[102:105]
	v_mfma_i32_16x16x64_i8 v[98:101], v[186:189], v[208:211], v[98:101]
	v_mfma_i32_16x16x64_i8 v[86:89], v[142:145], v[216:219], v[86:89]
	v_mfma_i32_16x16x64_i8 v[82:85], v[186:189], v[216:219], v[82:85]
	v_mfma_i32_16x16x64_i8 v[70:73], v[142:145], v[230:233], v[70:73]
	v_mfma_i32_16x16x64_i8 v[66:69], v[186:189], v[230:233], v[66:69]
	v_mfma_i32_16x16x64_i8 v[118:121], v[182:185], v[204:207], v[118:121]
	v_mfma_i32_16x16x64_i8 v[114:117], v[190:193], v[204:207], v[114:117]
	v_mfma_i32_16x16x64_i8 v[102:105], v[182:185], v[212:215], v[102:105]
	v_mfma_i32_16x16x64_i8 v[98:101], v[190:193], v[212:215], v[98:101]
	v_mfma_i32_16x16x64_i8 v[86:89], v[182:185], v[226:229], v[86:89]
	v_mfma_i32_16x16x64_i8 v[82:85], v[190:193], v[226:229], v[82:85]
	v_mfma_i32_16x16x64_i8 v[70:73], v[182:185], v[234:237], v[70:73]
	v_mfma_i32_16x16x64_i8 v[66:69], v[190:193], v[234:237], v[66:69]
	s_setprio 0
	s_barrier
	s_mov_b32 m0, s57
	v_lshl_add_u64 v[162:163], v[162:163], 0, s[58:59]
	s_add_u32 s18, s18, 0x20080
	ds_read_b128 v[196:199], v181 offset:49152
	ds_read_b128 v[204:207], v181 offset:50176
	ds_read_b128 v[208:211], v181 offset:51200
	ds_read_b128 v[212:215], v181 offset:52224
	ds_read_b128 v[216:219], v181 offset:53248
	ds_read_b128 v[226:229], v181 offset:54272
	ds_read_b128 v[230:233], v181 offset:55296
	ds_read_b128 v[234:237], v181 offset:56320
	global_load_lds_dwordx4 v[162:163], off
	v_lshl_add_u64 v[162:163], v[200:201], 0, s[58:59]
	s_mov_b32 m0, s10
	s_addc_u32 s19, s19, 0
	global_load_lds_dwordx4 v[162:163], off
	v_lshl_add_u64 v[162:163], s[18:19], 0, v[150:151]
	s_mov_b32 m0, s48
	s_nop 0
	global_load_lds_dwordx4 v[162:163], off
	v_lshl_add_u64 v[162:163], s[18:19], 0, v[146:147]
	s_mov_b32 m0, s44
	s_nop 0
	global_load_lds_dwordx4 v[162:163], off
	v_lshl_add_u64 v[162:163], v[238:239], 0, s[58:59]
	s_mov_b32 m0, s94
	s_nop 0
	global_load_lds_dwordx4 v[162:163], off
	v_lshl_add_u64 v[162:163], v[240:241], 0, s[58:59]
	s_mov_b32 m0, s95
	s_nop 0
	global_load_lds_dwordx4 v[162:163], off
	s_waitcnt vmcnt(8)
	s_waitcnt lgkmcnt(0)
	s_barrier
	s_setprio 1
	s_waitcnt lgkmcnt(0)
	v_mfma_i32_16x16x64_i8 v[54:57], v[138:141], v[196:199], v[54:57]
	v_mfma_i32_16x16x64_i8 v[50:53], v[134:137], v[196:199], v[50:53]
	v_mfma_i32_16x16x64_i8 v[38:41], v[138:141], v[208:211], v[38:41]
	v_mfma_i32_16x16x64_i8 v[34:37], v[134:137], v[208:211], v[34:37]
	v_mfma_i32_16x16x64_i8 v[20:23], v[138:141], v[216:219], v[20:23]
	v_mfma_i32_16x16x64_i8 v[16:19], v[134:137], v[216:219], v[16:19]
	v_mfma_i32_16x16x64_i8 v[4:7], v[138:141], v[230:233], v[4:7]
	v_mfma_i32_16x16x64_i8 v[0:3], v[134:137], v[230:233], v[0:3]
	v_mfma_i32_16x16x64_i8 v[54:57], v[130:133], v[204:207], v[54:57]
	v_mfma_i32_16x16x64_i8 v[50:53], v[158:161], v[204:207], v[50:53]
	v_mfma_i32_16x16x64_i8 v[38:41], v[130:133], v[212:215], v[38:41]
	v_mfma_i32_16x16x64_i8 v[34:37], v[158:161], v[212:215], v[34:37]
	v_mfma_i32_16x16x64_i8 v[20:23], v[130:133], v[226:229], v[20:23]
	v_mfma_i32_16x16x64_i8 v[16:19], v[158:161], v[226:229], v[16:19]
	v_mfma_i32_16x16x64_i8 v[4:7], v[130:133], v[234:237], v[4:7]
	v_mfma_i32_16x16x64_i8 v[0:3], v[158:161], v[234:237], v[0:3]
	v_mfma_i32_16x16x64_i8 v[62:65], v[142:145], v[196:199], v[62:65]
	v_mfma_i32_16x16x64_i8 v[58:61], v[186:189], v[196:199], v[58:61]
	v_mfma_i32_16x16x64_i8 v[46:49], v[142:145], v[208:211], v[46:49]
	v_mfma_i32_16x16x64_i8 v[42:45], v[186:189], v[208:211], v[42:45]
	v_mfma_i32_16x16x64_i8 v[28:31], v[142:145], v[216:219], v[28:31]
	v_mfma_i32_16x16x64_i8 v[24:27], v[186:189], v[216:219], v[24:27]
	v_mfma_i32_16x16x64_i8 v[12:15], v[142:145], v[230:233], v[12:15]
	v_mfma_i32_16x16x64_i8 v[8:11], v[186:189], v[230:233], v[8:11]
	v_mfma_i32_16x16x64_i8 v[62:65], v[182:185], v[204:207], v[62:65]
	v_mfma_i32_16x16x64_i8 v[58:61], v[190:193], v[204:207], v[58:61]
	v_mfma_i32_16x16x64_i8 v[46:49], v[182:185], v[212:215], v[46:49]
	v_mfma_i32_16x16x64_i8 v[42:45], v[190:193], v[212:215], v[42:45]
	v_mfma_i32_16x16x64_i8 v[28:31], v[182:185], v[226:229], v[28:31]
	v_mfma_i32_16x16x64_i8 v[24:27], v[190:193], v[226:229], v[24:27]
	v_mfma_i32_16x16x64_i8 v[12:15], v[182:185], v[234:237], v[12:15]
	v_mfma_i32_16x16x64_i8 v[8:11], v[190:193], v[234:237], v[8:11]
	s_setprio 0
	s_barrier
	s_add_i32 vcc_lo, vcc_lo, 2
	s_add_u32 s46, s46, 0x100
	s_addc_u32 s47, s47, 0
	s_add_u32 s76, s76, 0x100
	s_addc_u32 s77, s77, 0
	s_cmp_gt_u32 vcc_lo, 5
	s_cbranch_scc0 .LBB0_119
	s_and_b64 vcc, exec, s[22:23]
	s_cbranch_vccz .LBB0_122
	s_barrier

; #define LAS __attribute__((address_space(3)))
; #define PG8_STAGE(bufoff, gbase, voff) do { _Pragma("unroll") for (int _i = 0; _i < 2; ++_i) \
;         __builtin_amdgcn_global_load_lds((const unsigned*)((const char*)(gbase) + (voff)[_i]), (LAS unsigned*)(lds + (bufoff) + ldsw + _i * 8192), 16, 0, 0); } while (0)
; #define PG8_LDA(dst, b, h) do { _Pragma("unroll") for (int m = 0; m < 4; ++m) PG8_LD2(dst[m], PG8_SA(b, h) + aoff + m * 2048); } while (0)
; #define PG8_LDB(dst, b, h) do { _Pragma("unroll") for (int n = 0; n < 2; ++n) PG8_LD2(dst[n], PG8_SB(b, h) + boff + n * 2048); } while (0)
; #define PG8_BAR __builtin_amdgcn_s_barrier()
; template <int DT  , class Epi, class Sched, class Hook = NoHook>
; __device__ __forceinline__ void gemm_phase(LAS unsigned char* lds, const Sched& S, const Epi& E, int wave_s, LAS unsigned char* aux  ,
;                                            const Hook& H = Hook()  ) {
;     ...
;         const bool has_next = S.next(ui + 1, nxt);
;         const char* nA = has_next ? S.aptr(nxt) : cA; const char* nB = has_next ? S.bptr(nxt) : cB;
;         {
;             if constexpr (GATHER) { if (has_next && wid == 0) __builtin_amdgcn_global_load_lds((const unsigned*)(S.list_src(nxt) + 4 * lane), (LAS unsigned*)(aux + ((ui + 1) & 1) * 1024), 16, 0, 0); }
;             if constexpr (Epi::PREFETCH) E.prefetch(cur, aux + 2048 + (ui & 1) * 3072, wid, lane);
;         }
;         for (int t = 0; t < nt; t += 2) {
;             const bool last = (t == nt - 2);
;             const char* a1 = cA + (size_t)(t + 1) * kstep;
;             const char* a2 = last ? nA : cA + (size_t)(t + 2) * kstep; const char* b2 = last ? nB : cB + (size_t)(t + 2) * kstep;
;             const char* a3 = a2 + kstep; const char* b3 = b2 + kstep;
;             PG8_LDB(B0, 0, 0); PG8_LDB(B1, 0, 1); PG8_SCHED; PG8_LDA(At, 0, 0); PG8_STAGE_A(PG8_SA(1, 1), 1, a1);
;             if (GATHER) { if (last && has_next) S.gather_lds(nxt, gA, tid, aux + ((ui + 1) & 1) * 1024); }
;             PG8_WAIT_V(8); PG8_WAIT_L(0); PG8_BAR; PG8_MMA(0, 0, At, B0); PG8_MMA(0, 1, At, B1); PG8_BAR; PG8_SCHED;
;             PG8_LDA(At, 0, 1); PG8_STAGE(PG8_SB(0, 0), b2, voffB); PG8_STAGE(PG8_SB(0, 1), b2 + hstep, voffB); PG8_STAGE_A(PG8_SA(0, 0), 0, a2);
;             PG8_WAIT_V(8); PG8_WAIT_L(0); PG8_BAR; PG8_MMA(1, 0, At, B0); PG8_MMA(1, 1, At, B1); PG8_BAR; PG8_SCHED;
.LBB0_427:
	s_ashr_i32 s11, s10, 31
	s_lshl_b64 s[12:13], s[10:11], 19
	s_add_u32 s12, s80, s12
	s_addc_u32 s13, s81, s13
	s_and_b64 s[14:15], s[2:3], exec
	s_cselect_b32 s11, s13, s17
	s_cselect_b32 s51, s12, s16
	s_ashr_i32 s9, s8, 31
	s_lshl_b64 s[14:15], s[8:9], 19
	s_add_u32 s14, s22, s14
	s_addc_u32 s15, s23, s15
	s_and_b64 s[20:21], s[2:3], exec
	s_cselect_b32 s9, s15, s19
	s_cselect_b32 s57, s14, s18
	s_add_u32 s16, s16, 0x40080
	s_addc_u32 s17, s17, 0
	s_add_u32 s65, s18, 0x100
	s_addc_u32 s67, s19, 0
	s_mov_b32 s68, -2
	ds_read_b128 v[130:133], v180
	ds_read_b128 v[134:137], v181
	ds_read_b128 v[138:141], v176
	ds_read_b128 v[142:145], v177
	ds_read_b128 v[146:149], v182
	ds_read_b128 v[150:153], v183
	ds_read_b128 v[164:167], v184
	ds_read_b128 v[168:171], v185
	s_add_u32 s18, s16, 0xfffc0080
	s_addc_u32 s19, s17, -1
	s_cmp_eq_u32 s68, 12
	s_cselect_b32 s21, s11, s19
	s_cselect_b32 s20, s51, s18
	s_cselect_b32 s19, s9, s67
	s_cselect_b32 s18, s57, s65
	v_lshl_add_u64 v[200:201], s[16:17], 0, v[160:161]
	s_add_i32 m0, s24, 0xc000
	ds_read_b128 v[172:175], v192
	ds_read_b128 v[196:199], v192 offset:1024
	ds_read_b128 v[204:207], v192 offset:2048
	ds_read_b128 v[208:211], v192 offset:3072
	ds_read_b128 v[212:215], v192 offset:4096
	ds_read_b128 v[216:219], v192 offset:5120
	ds_read_b128 v[226:229], v192 offset:6144
	ds_read_b128 v[230:233], v192 offset:7168
	global_load_lds_dwordx4 v[200:201], off
	v_lshl_add_u64 v[200:201], s[16:17], 0, v[162:163]
	s_add_i32 m0, s24, 0xe000
	s_nop 0
	global_load_lds_dwordx4 v[200:201], off
	s_waitcnt vmcnt(8)
	s_waitcnt lgkmcnt(0)
	s_barrier
	s_setprio 1
	s_waitcnt lgkmcnt(0)
	v_mfma_f32_16x16x32_bf16 v[126:129], v[138:141], v[172:175], 0
	v_mfma_f32_16x16x32_bf16 v[122:125], v[134:137], v[172:175], 0
	v_mfma_f32_16x16x32_bf16 v[110:113], v[138:141], v[204:207], 0
	v_mfma_f32_16x16x32_bf16 v[106:109], v[134:137], v[204:207], 0
	v_mfma_f32_16x16x32_bf16 v[94:97], v[138:141], v[212:215], 0
	v_mfma_f32_16x16x32_bf16 v[90:93], v[134:137], v[212:215], 0
	v_mfma_f32_16x16x32_bf16 v[86:89], v[138:141], v[226:229], 0
	v_mfma_f32_16x16x32_bf16 v[78:81], v[134:137], v[226:229], 0
	v_mfma_f32_16x16x32_bf16 v[126:129], v[130:133], v[196:199], v[126:129]
	v_mfma_f32_16x16x32_bf16 v[122:125], v[146:149], v[196:199], v[122:125]
	v_mfma_f32_16x16x32_bf16 v[110:113], v[130:133], v[208:211], v[110:113]
	v_mfma_f32_16x16x32_bf16 v[106:109], v[146:149], v[208:211], v[106:109]
	v_mfma_f32_16x16x32_bf16 v[94:97], v[130:133], v[216:219], v[94:97]
	v_mfma_f32_16x16x32_bf16 v[90:93], v[146:149], v[216:219], v[90:93]
	v_mfma_f32_16x16x32_bf16 v[86:89], v[130:133], v[230:233], v[86:89]
	v_mfma_f32_16x16x32_bf16 v[78:81], v[146:149], v[230:233], v[78:81]
	v_mfma_f32_16x16x32_bf16 v[118:121], v[142:145], v[172:175], 0
	v_mfma_f32_16x16x32_bf16 v[114:117], v[164:167], v[172:175], 0
	v_mfma_f32_16x16x32_bf16 v[102:105], v[142:145], v[204:207], 0
	v_mfma_f32_16x16x32_bf16 v[98:101], v[164:167], v[204:207], 0
	v_mfma_f32_16x16x32_bf16 v[82:85], v[142:145], v[212:215], 0
	v_mfma_f32_16x16x32_bf16 v[74:77], v[164:167], v[212:215], 0
	v_mfma_f32_16x16x32_bf16 v[70:73], v[142:145], v[226:229], 0
	v_mfma_f32_16x16x32_bf16 v[66:69], v[164:167], v[226:229], 0
	v_mfma_f32_16x16x32_bf16 v[118:121], v[150:153], v[196:199], v[118:121]
	v_mfma_f32_16x16x32_bf16 v[114:117], v[168:171], v[196:199], v[114:117]
	v_mfma_f32_16x16x32_bf16 v[102:105], v[150:153], v[208:211], v[102:105]
	v_mfma_f32_16x16x32_bf16 v[98:101], v[168:171], v[208:211], v[98:101]
	v_mfma_f32_16x16x32_bf16 v[82:85], v[150:153], v[216:219], v[82:85]
	v_mfma_f32_16x16x32_bf16 v[74:77], v[168:171], v[216:219], v[74:77]
	v_mfma_f32_16x16x32_bf16 v[70:73], v[150:153], v[230:233], v[70:73]
	v_mfma_f32_16x16x32_bf16 v[66:69], v[168:171], v[230:233], v[66:69]
	s_setprio 0
	s_barrier
	s_mov_b32 m0, s25
	v_lshl_add_u64 v[200:201], s[18:19], 0, v[32:33]
	s_add_u32 s42, s18, 0x40000
	ds_read_b128 v[172:175], v192 offset:16384
	ds_read_b128 v[196:199], v192 offset:17408
	ds_read_b128 v[204:207], v192 offset:18432
	ds_read_b128 v[208:211], v192 offset:19456
	ds_read_b128 v[212:215], v192 offset:20480
	ds_read_b128 v[216:219], v192 offset:21504
	ds_read_b128 v[226:229], v192 offset:22528
	ds_read_b128 v[230:233], v192 offset:23552
	global_load_lds_dwordx4 v[200:201], off
	v_lshl_add_u64 v[234:235], s[18:19], 0, v[154:155]
	s_mov_b32 m0, s26
	s_addc_u32 s43, s19, 0
	global_load_lds_dwordx4 v[234:235], off
	v_lshl_add_u64 v[236:237], s[42:43], 0, v[32:33]
	s_mov_b32 m0, s27
	v_lshl_add_u64 v[238:239], s[20:21], 0, v[156:157]
	global_load_lds_dwordx4 v[236:237], off
	v_lshl_add_u64 v[236:237], s[42:43], 0, v[154:155]
	s_mov_b32 m0, s28
	s_nop 0
	global_load_lds_dwordx4 v[236:237], off
	v_lshl_add_u64 v[236:237], s[20:21], 0, v[158:159]
	s_mov_b32 m0, s24
	s_nop 0
	global_load_lds_dwordx4 v[236:237], off
	s_mov_b32 m0, s29
	s_nop 0
	global_load_lds_dwordx4 v[238:239], off
	s_waitcnt vmcnt(8)
	s_waitcnt lgkmcnt(0)
	s_barrier
; #define PG8_STAGE_A(bufoff, h, abase) do { _Pragma("unroll") for (int _i = 0; _i < 2; ++_i) { \
;         const char* _src = GATHER ? ((const char*)(abase) + gA[h][_i]) : ((const char*)(abase) + (size_t)(h) * hstep + voffA[_i]); \
;         __builtin_amdgcn_global_load_lds((const unsigned*)_src, (LAS unsigned*)(lds + (bufoff) + ldsw + _i * 8192), 16, 0, 0); } } while (0)
; #define PG8_LDA(dst, b, h) do { _Pragma("unroll") for (int m = 0; m < 4; ++m) PG8_LD2(dst[m], PG8_SA(b, h) + aoff + m * 2048); } while (0)
; #define PG8_LDB(dst, b, h) do { _Pragma("unroll") for (int n = 0; n < 2; ++n) PG8_LD2(dst[n], PG8_SB(b, h) + boff + n * 2048); } while (0)
; #define PG8_WAIT_V(n) asm volatile("s_waitcnt vmcnt(" #n ")" ::: "memory")
; #define PG8_WAIT_L(n) asm volatile("s_waitcnt lgkmcnt(" #n ")" ::: "memory")
; #define PG8_BAR __builtin_amdgcn_s_barrier()
; #define PG8_SCHED __builtin_amdgcn_sched_barrier(0)
; template <int DT  , class Epi, class Sched, class Hook = NoHook>
; __device__ __forceinline__ void gemm_phase(LAS unsigned char* lds, const Sched& S, const Epi& E, int wave_s, LAS unsigned char* aux  ,
;                                            const Hook& H = Hook()  ) {
;     ...
;             PG8_WAIT_V(8); PG8_WAIT_L(0); PG8_BAR; PG8_MMA(1, 0, At, B0); PG8_MMA(1, 1, At, B1); PG8_BAR; PG8_SCHED;
;             PG8_LDB(B0, 1, 0); PG8_LDB(B1, 1, 1); PG8_SCHED; PG8_LDA(At, 1, 0); PG8_STAGE_A(PG8_SA(0, 1), 1, a2);
;             PG8_WAIT_V(8); PG8_WAIT_L(0); PG8_BAR; PG8_MMA(0, 0, At, B0); PG8_MMA(0, 1, At, B1); PG8_BAR; PG8_SCHED;
	s_setprio 1
	s_waitcnt lgkmcnt(0)
	v_mfma_f32_16x16x32_bf16 v[54:57], v[138:141], v[172:175], 0
	v_mfma_f32_16x16x32_bf16 v[50:53], v[134:137], v[172:175], 0
	v_mfma_f32_16x16x32_bf16 v[38:41], v[138:141], v[204:207], 0
	v_mfma_f32_16x16x32_bf16 v[34:37], v[134:137], v[204:207], 0
	v_mfma_f32_16x16x32_bf16 v[20:23], v[138:141], v[212:215], 0
	v_mfma_f32_16x16x32_bf16 v[8:11], v[134:137], v[212:215], 0
	v_mfma_f32_16x16x32_bf16 v[4:7], v[138:141], v[226:229], 0
	v_mfma_f32_16x16x32_bf16 v[0:3], v[134:137], v[226:229], 0
	v_mfma_f32_16x16x32_bf16 v[54:57], v[130:133], v[196:199], v[54:57]
	v_mfma_f32_16x16x32_bf16 v[50:53], v[146:149], v[196:199], v[50:53]
	v_mfma_f32_16x16x32_bf16 v[38:41], v[130:133], v[208:211], v[38:41]
	v_mfma_f32_16x16x32_bf16 v[34:37], v[146:149], v[208:211], v[34:37]
	v_mfma_f32_16x16x32_bf16 v[20:23], v[130:133], v[216:219], v[20:23]
	v_mfma_f32_16x16x32_bf16 v[8:11], v[146:149], v[216:219], v[8:11]
	v_mfma_f32_16x16x32_bf16 v[4:7], v[130:133], v[230:233], v[4:7]
	v_mfma_f32_16x16x32_bf16 v[0:3], v[146:149], v[230:233], v[0:3]
	v_mfma_f32_16x16x32_bf16 v[58:61], v[142:145], v[172:175], 0
	v_mfma_f32_16x16x32_bf16 v[62:65], v[164:167], v[172:175], 0
	v_mfma_f32_16x16x32_bf16 v[42:45], v[142:145], v[204:207], 0
	v_mfma_f32_16x16x32_bf16 v[46:49], v[164:167], v[204:207], 0
	v_mfma_f32_16x16x32_bf16 v[24:27], v[142:145], v[212:215], 0
	v_mfma_f32_16x16x32_bf16 v[28:31], v[164:167], v[212:215], 0
	v_mfma_f32_16x16x32_bf16 v[12:15], v[142:145], v[226:229], 0
	v_mfma_f32_16x16x32_bf16 v[16:19], v[164:167], v[226:229], 0
	v_mfma_f32_16x16x32_bf16 v[58:61], v[150:153], v[196:199], v[58:61]
	v_mfma_f32_16x16x32_bf16 v[62:65], v[168:171], v[196:199], v[62:65]
	v_mfma_f32_16x16x32_bf16 v[42:45], v[150:153], v[208:211], v[42:45]
	v_mfma_f32_16x16x32_bf16 v[46:49], v[168:171], v[208:211], v[46:49]
	v_mfma_f32_16x16x32_bf16 v[24:27], v[150:153], v[216:219], v[24:27]
	v_mfma_f32_16x16x32_bf16 v[28:31], v[168:171], v[216:219], v[28:31]
	v_mfma_f32_16x16x32_bf16 v[12:15], v[150:153], v[230:233], v[12:15]
	v_mfma_f32_16x16x32_bf16 v[16:19], v[168:171], v[230:233], v[16:19]
	s_setprio 0
	s_barrier
	ds_read_b128 v[130:133], v186
	ds_read_b128 v[134:137], v187
	ds_read_b128 v[138:141], v178
	ds_read_b128 v[142:145], v179
	ds_read_b128 v[146:149], v188
	ds_read_b128 v[150:153], v189
	ds_read_b128 v[164:167], v190
	ds_read_b128 v[168:171], v191
	s_add_u32 s20, s20, 0x40000
	s_addc_u32 s21, s21, 0
	s_mov_b32 m0, s30
	v_lshl_add_u64 v[240:241], s[20:21], 0, v[158:159]
	ds_read_b128 v[172:175], v192 offset:32768
	ds_read_b128 v[196:199], v192 offset:33792
	ds_read_b128 v[204:207], v192 offset:34816
	ds_read_b128 v[208:211], v192 offset:35840
	ds_read_b128 v[212:215], v192 offset:36864
	ds_read_b128 v[216:219], v192 offset:37888
	ds_read_b128 v[226:229], v192 offset:38912
	ds_read_b128 v[230:233], v192 offset:39936
	global_load_lds_dwordx4 v[240:241], off
	v_lshl_add_u64 v[240:241], s[20:21], 0, v[156:157]
	s_mov_b32 m0, s31
	s_nop 0
	global_load_lds_dwordx4 v[240:241], off
	s_waitcnt vmcnt(8)
	s_waitcnt lgkmcnt(0)
	s_barrier
	s_setprio 1
	s_waitcnt lgkmcnt(0)
	v_mfma_f32_16x16x32_bf16 v[126:129], v[138:141], v[172:175], v[126:129]
	v_mfma_f32_16x16x32_bf16 v[122:125], v[134:137], v[172:175], v[122:125]
	v_mfma_f32_16x16x32_bf16 v[110:113], v[138:141], v[204:207], v[110:113]
	v_mfma_f32_16x16x32_bf16 v[106:109], v[134:137], v[204:207], v[106:109]
	v_mfma_f32_16x16x32_bf16 v[94:97], v[138:141], v[212:215], v[94:97]
	v_mfma_f32_16x16x32_bf16 v[90:93], v[134:137], v[212:215], v[90:93]
	v_mfma_f32_16x16x32_bf16 v[86:89], v[138:141], v[226:229], v[86:89]
	v_mfma_f32_16x16x32_bf16 v[78:81], v[134:137], v[226:229], v[78:81]
	v_mfma_f32_16x16x32_bf16 v[126:129], v[130:133], v[196:199], v[126:129]
	v_mfma_f32_16x16x32_bf16 v[122:125], v[146:149], v[196:199], v[122:125]
	v_mfma_f32_16x16x32_bf16 v[110:113], v[130:133], v[208:211], v[110:113]
	v_mfma_f32_16x16x32_bf16 v[106:109], v[146:149], v[208:211], v[106:109]
	v_mfma_f32_16x16x32_bf16 v[94:97], v[130:133], v[216:219], v[94:97]
	v_mfma_f32_16x16x32_bf16 v[90:93], v[146:149], v[216:219], v[90:93]
	v_mfma_f32_16x16x32_bf16 v[86:89], v[130:133], v[230:233], v[86:89]
	v_mfma_f32_16x16x32_bf16 v[78:81], v[146:149], v[230:233], v[78:81]
	v_mfma_f32_16x16x32_bf16 v[118:121], v[142:145], v[172:175], v[118:121]
	v_mfma_f32_16x16x32_bf16 v[114:117], v[164:167], v[172:175], v[114:117]
	v_mfma_f32_16x16x32_bf16 v[102:105], v[142:145], v[204:207], v[102:105]
	v_mfma_f32_16x16x32_bf16 v[98:101], v[164:167], v[204:207], v[98:101]
	v_mfma_f32_16x16x32_bf16 v[82:85], v[142:145], v[212:215], v[82:85]
	v_mfma_f32_16x16x32_bf16 v[74:77], v[164:167], v[212:215], v[74:77]
	v_mfma_f32_16x16x32_bf16 v[70:73], v[142:145], v[226:229], v[70:73]
	v_mfma_f32_16x16x32_bf16 v[66:69], v[164:167], v[226:229], v[66:69]
	v_mfma_f32_16x16x32_bf16 v[118:121], v[150:153], v[196:199], v[118:121]
	v_mfma_f32_16x16x32_bf16 v[114:117], v[168:171], v[196:199], v[114:117]
	v_mfma_f32_16x16x32_bf16 v[102:105], v[150:153], v[208:211], v[102:105]
	v_mfma_f32_16x16x32_bf16 v[98:101], v[168:171], v[208:211], v[98:101]
	v_mfma_f32_16x16x32_bf16 v[82:85], v[150:153], v[216:219], v[82:85]
	v_mfma_f32_16x16x32_bf16 v[74:77], v[168:171], v[216:219], v[74:77]
	v_mfma_f32_16x16x32_bf16 v[70:73], v[150:153], v[230:233], v[70:73]
	v_mfma_f32_16x16x32_bf16 v[66:69], v[168:171], v[230:233], v[66:69]
	s_setprio 0
	s_barrier
; #define PG8_STAGE(bufoff, gbase, voff) do { _Pragma("unroll") for (int _i = 0; _i < 2; ++_i) \
;         __builtin_amdgcn_global_load_lds((const unsigned*)((const char*)(gbase) + (voff)[_i]), (LAS unsigned*)(lds + (bufoff) + ldsw + _i * 8192), 16, 0, 0); } while (0)
; #define PG8_STAGE_A(bufoff, h, abase) do { _Pragma("unroll") for (int _i = 0; _i < 2; ++_i) { \
;         const char* _src = GATHER ? ((const char*)(abase) + gA[h][_i]) : ((const char*)(abase) + (size_t)(h) * hstep + voffA[_i]); \
;         __builtin_amdgcn_global_load_lds((const unsigned*)_src, (LAS unsigned*)(lds + (bufoff) + ldsw + _i * 8192), 16, 0, 0); } } while (0)
; template <int DT  , class Epi, class Sched, class Hook = NoHook>
; __device__ __forceinline__ void gemm_phase(LAS unsigned char* lds, const Sched& S, const Epi& E, int wave_s, LAS unsigned char* aux  ,
;                                            const Hook& H = Hook()  ) {
;     ...
;         for (int t = 0; t < nt; t += 2) {
;             const bool last = (t == nt - 2);
;             const char* a1 = cA + (size_t)(t + 1) * kstep;
;             const char* a2 = last ? nA : cA + (size_t)(t + 2) * kstep; const char* b2 = last ? nB : cB + (size_t)(t + 2) * kstep;
;             const char* a3 = a2 + kstep; const char* b3 = b2 + kstep;
;             PG8_LDB(B0, 0, 0); PG8_LDB(B1, 0, 1); PG8_SCHED; PG8_LDA(At, 0, 0); PG8_STAGE_A(PG8_SA(1, 1), 1, a1);
;             if (GATHER) { if (last && has_next) S.gather_lds(nxt, gA, tid, aux + ((ui + 1) & 1) * 1024); }
;             PG8_WAIT_V(8); PG8_WAIT_L(0); PG8_BAR; PG8_MMA(0, 0, At, B0); PG8_MMA(0, 1, At, B1); PG8_BAR; PG8_SCHED;
;             PG8_LDA(At, 0, 1); PG8_STAGE(PG8_SB(0, 0), b2, voffB); PG8_STAGE(PG8_SB(0, 1), b2 + hstep, voffB); PG8_STAGE_A(PG8_SA(0, 0), 0, a2);
;             PG8_WAIT_V(8); PG8_WAIT_L(0); PG8_BAR; PG8_MMA(1, 0, At, B0); PG8_MMA(1, 1, At, B1); PG8_BAR; PG8_SCHED;
;             PG8_LDB(B0, 1, 0); PG8_LDB(B1, 1, 1); PG8_SCHED; PG8_LDA(At, 1, 0); PG8_STAGE_A(PG8_SA(0, 1), 1, a2);
;             PG8_WAIT_V(8); PG8_WAIT_L(0); PG8_BAR; PG8_MMA(0, 0, At, B0); PG8_MMA(0, 1, At, B1); PG8_BAR; PG8_SCHED;
;             PG8_LDA(At, 1, 1); PG8_STAGE(PG8_SB(1, 0), b3, voffB); PG8_STAGE(PG8_SB(1, 1), b3 + hstep, voffB); PG8_STAGE_A(PG8_SA(1, 0), 0, a3);
;             PG8_WAIT_V(8); PG8_WAIT_L(0); PG8_BAR; PG8_MMA(1, 0, At, B0); PG8_MMA(1, 1, At, B1); PG8_BAR; PG8_SCHED;
	s_mov_b32 m0, s35
	v_lshl_add_u64 v[200:201], v[200:201], 0, s[58:59]
	s_add_u32 s18, s18, 0x40080
	ds_read_b128 v[172:175], v192 offset:49152
	ds_read_b128 v[196:199], v192 offset:50176
	ds_read_b128 v[204:207], v192 offset:51200
	ds_read_b128 v[208:211], v192 offset:52224
	ds_read_b128 v[212:215], v192 offset:53248
	ds_read_b128 v[216:219], v192 offset:54272
	ds_read_b128 v[226:229], v192 offset:55296
	ds_read_b128 v[230:233], v192 offset:56320
	global_load_lds_dwordx4 v[200:201], off
	v_lshl_add_u64 v[200:201], v[234:235], 0, s[58:59]
	s_mov_b32 m0, s38
	s_addc_u32 s19, s19, 0
	global_load_lds_dwordx4 v[200:201], off
	v_lshl_add_u64 v[200:201], s[18:19], 0, v[32:33]
	s_mov_b32 m0, s44
	s_nop 0
	global_load_lds_dwordx4 v[200:201], off
	v_lshl_add_u64 v[200:201], s[18:19], 0, v[154:155]
	s_mov_b32 m0, s45
	s_nop 0
	global_load_lds_dwordx4 v[200:201], off
	v_lshl_add_u64 v[200:201], v[236:237], 0, s[58:59]
	s_mov_b32 m0, s40
	s_nop 0
	global_load_lds_dwordx4 v[200:201], off
	v_lshl_add_u64 v[200:201], v[238:239], 0, s[58:59]
	s_mov_b32 m0, s41
	s_nop 0
	global_load_lds_dwordx4 v[200:201], off
	s_waitcnt vmcnt(8)
	s_waitcnt lgkmcnt(0)
	s_barrier
	s_setprio 1
	s_waitcnt lgkmcnt(0)
	v_mfma_f32_16x16x32_bf16 v[54:57], v[138:141], v[172:175], v[54:57]
	v_mfma_f32_16x16x32_bf16 v[50:53], v[134:137], v[172:175], v[50:53]
	v_mfma_f32_16x16x32_bf16 v[38:41], v[138:141], v[204:207], v[38:41]
	v_mfma_f32_16x16x32_bf16 v[34:37], v[134:137], v[204:207], v[34:37]
	v_mfma_f32_16x16x32_bf16 v[20:23], v[138:141], v[212:215], v[20:23]
	v_mfma_f32_16x16x32_bf16 v[8:11], v[134:137], v[212:215], v[8:11]
	v_mfma_f32_16x16x32_bf16 v[4:7], v[138:141], v[226:229], v[4:7]
	v_mfma_f32_16x16x32_bf16 v[0:3], v[134:137], v[226:229], v[0:3]
	v_mfma_f32_16x16x32_bf16 v[54:57], v[130:133], v[196:199], v[54:57]
	v_mfma_f32_16x16x32_bf16 v[50:53], v[146:149], v[196:199], v[50:53]
	v_mfma_f32_16x16x32_bf16 v[38:41], v[130:133], v[208:211], v[38:41]
	v_mfma_f32_16x16x32_bf16 v[34:37], v[146:149], v[208:211], v[34:37]
	v_mfma_f32_16x16x32_bf16 v[20:23], v[130:133], v[216:219], v[20:23]
	v_mfma_f32_16x16x32_bf16 v[8:11], v[146:149], v[216:219], v[8:11]
	v_mfma_f32_16x16x32_bf16 v[4:7], v[130:133], v[230:233], v[4:7]
	v_mfma_f32_16x16x32_bf16 v[0:3], v[146:149], v[230:233], v[0:3]
	v_mfma_f32_16x16x32_bf16 v[58:61], v[142:145], v[172:175], v[58:61]
	v_mfma_f32_16x16x32_bf16 v[62:65], v[164:167], v[172:175], v[62:65]
	v_mfma_f32_16x16x32_bf16 v[42:45], v[142:145], v[204:207], v[42:45]
	v_mfma_f32_16x16x32_bf16 v[46:49], v[164:167], v[204:207], v[46:49]
	v_mfma_f32_16x16x32_bf16 v[24:27], v[142:145], v[212:215], v[24:27]
	v_mfma_f32_16x16x32_bf16 v[28:31], v[164:167], v[212:215], v[28:31]
	v_mfma_f32_16x16x32_bf16 v[12:15], v[142:145], v[226:229], v[12:15]
	v_mfma_f32_16x16x32_bf16 v[16:19], v[164:167], v[226:229], v[16:19]
	v_mfma_f32_16x16x32_bf16 v[58:61], v[150:153], v[196:199], v[58:61]
	v_mfma_f32_16x16x32_bf16 v[62:65], v[168:171], v[196:199], v[62:65]
	v_mfma_f32_16x16x32_bf16 v[42:45], v[150:153], v[208:211], v[42:45]
	v_mfma_f32_16x16x32_bf16 v[46:49], v[168:171], v[208:211], v[46:49]
	v_mfma_f32_16x16x32_bf16 v[24:27], v[150:153], v[216:219], v[24:27]
	v_mfma_f32_16x16x32_bf16 v[28:31], v[168:171], v[216:219], v[28:31]
	v_mfma_f32_16x16x32_bf16 v[12:15], v[150:153], v[230:233], v[12:15]
	v_mfma_f32_16x16x32_bf16 v[16:19], v[168:171], v[230:233], v[16:19]
	s_setprio 0
	s_barrier
	s_add_i32 s68, s68, 2
	s_add_u32 s16, s16, 0x100
	s_addc_u32 s17, s17, 0
	s_add_u32 s65, s65, 0x100
	s_addc_u32 s67, s67, 0
	s_cmp_gt_u32 s68, 13
.LBB0_428:
	ds_read_b128 v[130:133], v180
	ds_read_b128 v[134:137], v181
	ds_read_b128 v[138:141], v176
	ds_read_b128 v[142:145], v177
	ds_read_b128 v[146:149], v182
	ds_read_b128 v[150:153], v183
	ds_read_b128 v[164:167], v184
	ds_read_b128 v[168:171], v185
	s_add_u32 s18, s16, 0xfffc0080
	s_addc_u32 s19, s17, -1
	s_cmp_eq_u32 s68, 12
	s_cselect_b32 s21, s11, s19
	s_cselect_b32 s20, s51, s18
	s_cselect_b32 s19, s9, s67
	s_cselect_b32 s18, s57, s65
	v_lshl_add_u64 v[200:201], s[16:17], 0, v[160:161]
	s_add_i32 m0, s24, 0xc000
	ds_read_b128 v[172:175], v192
	ds_read_b128 v[196:199], v192 offset:1024
	ds_read_b128 v[204:207], v192 offset:2048
	ds_read_b128 v[208:211], v192 offset:3072
	ds_read_b128 v[212:215], v192 offset:4096
	ds_read_b128 v[216:219], v192 offset:5120
	ds_read_b128 v[226:229], v192 offset:6144
	ds_read_b128 v[230:233], v192 offset:7168
	global_load_lds_dwordx4 v[200:201], off
	v_lshl_add_u64 v[200:201], s[16:17], 0, v[162:163]
	s_add_i32 m0, s24, 0xe000
	s_nop 0
	global_load_lds_dwordx4 v[200:201], off
	s_waitcnt vmcnt(8)
	s_waitcnt lgkmcnt(0)
	s_barrier
; #define PG8_STAGE(bufoff, gbase, voff) do { _Pragma("unroll") for (int _i = 0; _i < 2; ++_i) \
;         __builtin_amdgcn_global_load_lds((const unsigned*)((const char*)(gbase) + (voff)[_i]), (LAS unsigned*)(lds + (bufoff) + ldsw + _i * 8192), 16, 0, 0); } while (0)
; #define PG8_STAGE_A(bufoff, h, abase) do { _Pragma("unroll") for (int _i = 0; _i < 2; ++_i) { \
;         const char* _src = GATHER ? ((const char*)(abase) + gA[h][_i]) : ((const char*)(abase) + (size_t)(h) * hstep + voffA[_i]); \
;         __builtin_amdgcn_global_load_lds((const unsigned*)_src, (LAS unsigned*)(lds + (bufoff) + ldsw + _i * 8192), 16, 0, 0); } } while (0)
; #define PG8_LDA(dst, b, h) do { _Pragma("unroll") for (int m = 0; m < 4; ++m) PG8_LD2(dst[m], PG8_SA(b, h) + aoff + m * 2048); } while (0)
; #define PG8_LDB(dst, b, h) do { _Pragma("unroll") for (int n = 0; n < 2; ++n) PG8_LD2(dst[n], PG8_SB(b, h) + boff + n * 2048); } while (0)
; #define PG8_WAIT_V(n) asm volatile("s_waitcnt vmcnt(" #n ")" ::: "memory")
; #define PG8_WAIT_L(n) asm volatile("s_waitcnt lgkmcnt(" #n ")" ::: "memory")
; #define PG8_BAR __builtin_amdgcn_s_barrier()
; #define PG8_SCHED __builtin_amdgcn_sched_barrier(0)
; template <int DT  , class Epi, class Sched, class Hook = NoHook>
; __device__ __forceinline__ void gemm_phase(LAS unsigned char* lds, const Sched& S, const Epi& E, int wave_s, LAS unsigned char* aux  ,
;                                            const Hook& H = Hook()  ) {
;     ...
;             PG8_WAIT_V(8); PG8_WAIT_L(0); PG8_BAR; PG8_MMA(0, 0, At, B0); PG8_MMA(0, 1, At, B1); PG8_BAR; PG8_SCHED;
;             PG8_LDA(At, 0, 1); PG8_STAGE(PG8_SB(0, 0), b2, voffB); PG8_STAGE(PG8_SB(0, 1), b2 + hstep, voffB); PG8_STAGE_A(PG8_SA(0, 0), 0, a2);
;             PG8_WAIT_V(8); PG8_WAIT_L(0); PG8_BAR; PG8_MMA(1, 0, At, B0); PG8_MMA(1, 1, At, B1); PG8_BAR; PG8_SCHED;
;             PG8_LDB(B0, 1, 0); PG8_LDB(B1, 1, 1); PG8_SCHED; PG8_LDA(At, 1, 0); PG8_STAGE_A(PG8_SA(0, 1), 1, a2);
;             PG8_WAIT_V(8); PG8_WAIT_L(0); PG8_BAR; PG8_MMA(0, 0, At, B0); PG8_MMA(0, 1, At, B1); PG8_BAR; PG8_SCHED;
	s_setprio 1
	s_waitcnt lgkmcnt(0)
	v_mfma_f32_16x16x32_bf16 v[126:129], v[138:141], v[172:175], v[126:129]
	v_mfma_f32_16x16x32_bf16 v[122:125], v[134:137], v[172:175], v[122:125]
	v_mfma_f32_16x16x32_bf16 v[110:113], v[138:141], v[204:207], v[110:113]
	v_mfma_f32_16x16x32_bf16 v[106:109], v[134:137], v[204:207], v[106:109]
	v_mfma_f32_16x16x32_bf16 v[94:97], v[138:141], v[212:215], v[94:97]
	v_mfma_f32_16x16x32_bf16 v[90:93], v[134:137], v[212:215], v[90:93]
	v_mfma_f32_16x16x32_bf16 v[86:89], v[138:141], v[226:229], v[86:89]
	v_mfma_f32_16x16x32_bf16 v[78:81], v[134:137], v[226:229], v[78:81]
	v_mfma_f32_16x16x32_bf16 v[126:129], v[130:133], v[196:199], v[126:129]
	v_mfma_f32_16x16x32_bf16 v[122:125], v[146:149], v[196:199], v[122:125]
	v_mfma_f32_16x16x32_bf16 v[110:113], v[130:133], v[208:211], v[110:113]
	v_mfma_f32_16x16x32_bf16 v[106:109], v[146:149], v[208:211], v[106:109]
	v_mfma_f32_16x16x32_bf16 v[94:97], v[130:133], v[216:219], v[94:97]
	v_mfma_f32_16x16x32_bf16 v[90:93], v[146:149], v[216:219], v[90:93]
	v_mfma_f32_16x16x32_bf16 v[86:89], v[130:133], v[230:233], v[86:89]
	v_mfma_f32_16x16x32_bf16 v[78:81], v[146:149], v[230:233], v[78:81]
	v_mfma_f32_16x16x32_bf16 v[118:121], v[142:145], v[172:175], v[118:121]
	v_mfma_f32_16x16x32_bf16 v[114:117], v[164:167], v[172:175], v[114:117]
	v_mfma_f32_16x16x32_bf16 v[102:105], v[142:145], v[204:207], v[102:105]
	v_mfma_f32_16x16x32_bf16 v[98:101], v[164:167], v[204:207], v[98:101]
	v_mfma_f32_16x16x32_bf16 v[82:85], v[142:145], v[212:215], v[82:85]
	v_mfma_f32_16x16x32_bf16 v[74:77], v[164:167], v[212:215], v[74:77]
	v_mfma_f32_16x16x32_bf16 v[70:73], v[142:145], v[226:229], v[70:73]
	v_mfma_f32_16x16x32_bf16 v[66:69], v[164:167], v[226:229], v[66:69]
	v_mfma_f32_16x16x32_bf16 v[118:121], v[150:153], v[196:199], v[118:121]
	v_mfma_f32_16x16x32_bf16 v[114:117], v[168:171], v[196:199], v[114:117]
	v_mfma_f32_16x16x32_bf16 v[102:105], v[150:153], v[208:211], v[102:105]
	v_mfma_f32_16x16x32_bf16 v[98:101], v[168:171], v[208:211], v[98:101]
	v_mfma_f32_16x16x32_bf16 v[82:85], v[150:153], v[216:219], v[82:85]
	v_mfma_f32_16x16x32_bf16 v[74:77], v[168:171], v[216:219], v[74:77]
	v_mfma_f32_16x16x32_bf16 v[70:73], v[150:153], v[230:233], v[70:73]
	v_mfma_f32_16x16x32_bf16 v[66:69], v[168:171], v[230:233], v[66:69]
	s_setprio 0
	s_barrier
	s_mov_b32 m0, s25
	v_lshl_add_u64 v[200:201], s[18:19], 0, v[32:33]
	s_add_u32 s42, s18, 0x40000
	ds_read_b128 v[172:175], v192 offset:16384
	ds_read_b128 v[196:199], v192 offset:17408
	ds_read_b128 v[204:207], v192 offset:18432
	ds_read_b128 v[208:211], v192 offset:19456
	ds_read_b128 v[212:215], v192 offset:20480
	ds_read_b128 v[216:219], v192 offset:21504
	ds_read_b128 v[226:229], v192 offset:22528
	ds_read_b128 v[230:233], v192 offset:23552
	global_load_lds_dwordx4 v[200:201], off
	v_lshl_add_u64 v[234:235], s[18:19], 0, v[154:155]
	s_mov_b32 m0, s26
	s_addc_u32 s43, s19, 0
	global_load_lds_dwordx4 v[234:235], off
	v_lshl_add_u64 v[236:237], s[42:43], 0, v[32:33]
	s_mov_b32 m0, s27
	v_lshl_add_u64 v[238:239], s[20:21], 0, v[156:157]
	global_load_lds_dwordx4 v[236:237], off
	v_lshl_add_u64 v[236:237], s[42:43], 0, v[154:155]
	s_mov_b32 m0, s28
	s_nop 0
	global_load_lds_dwordx4 v[236:237], off
	v_lshl_add_u64 v[236:237], s[20:21], 0, v[158:159]
	s_mov_b32 m0, s24
	s_nop 0
	global_load_lds_dwordx4 v[236:237], off
	s_mov_b32 m0, s29
	s_nop 0
	global_load_lds_dwordx4 v[238:239], off
	s_waitcnt vmcnt(8)
	s_waitcnt lgkmcnt(0)
	s_barrier
	s_setprio 1
	s_waitcnt lgkmcnt(0)
	v_mfma_f32_16x16x32_bf16 v[54:57], v[138:141], v[172:175], v[54:57]
	v_mfma_f32_16x16x32_bf16 v[50:53], v[134:137], v[172:175], v[50:53]
	v_mfma_f32_16x16x32_bf16 v[38:41], v[138:141], v[204:207], v[38:41]
	v_mfma_f32_16x16x32_bf16 v[34:37], v[134:137], v[204:207], v[34:37]
	v_mfma_f32_16x16x32_bf16 v[20:23], v[138:141], v[212:215], v[20:23]
	v_mfma_f32_16x16x32_bf16 v[8:11], v[134:137], v[212:215], v[8:11]
	v_mfma_f32_16x16x32_bf16 v[4:7], v[138:141], v[226:229], v[4:7]
	v_mfma_f32_16x16x32_bf16 v[0:3], v[134:137], v[226:229], v[0:3]
	v_mfma_f32_16x16x32_bf16 v[54:57], v[130:133], v[196:199], v[54:57]
	v_mfma_f32_16x16x32_bf16 v[50:53], v[146:149], v[196:199], v[50:53]
	v_mfma_f32_16x16x32_bf16 v[38:41], v[130:133], v[208:211], v[38:41]
	v_mfma_f32_16x16x32_bf16 v[34:37], v[146:149], v[208:211], v[34:37]
	v_mfma_f32_16x16x32_bf16 v[20:23], v[130:133], v[216:219], v[20:23]
	v_mfma_f32_16x16x32_bf16 v[8:11], v[146:149], v[216:219], v[8:11]
	v_mfma_f32_16x16x32_bf16 v[4:7], v[130:133], v[230:233], v[4:7]
	v_mfma_f32_16x16x32_bf16 v[0:3], v[146:149], v[230:233], v[0:3]
	v_mfma_f32_16x16x32_bf16 v[58:61], v[142:145], v[172:175], v[58:61]
	v_mfma_f32_16x16x32_bf16 v[62:65], v[164:167], v[172:175], v[62:65]
	v_mfma_f32_16x16x32_bf16 v[42:45], v[142:145], v[204:207], v[42:45]
	v_mfma_f32_16x16x32_bf16 v[46:49], v[164:167], v[204:207], v[46:49]
	v_mfma_f32_16x16x32_bf16 v[24:27], v[142:145], v[212:215], v[24:27]
	v_mfma_f32_16x16x32_bf16 v[28:31], v[164:167], v[212:215], v[28:31]
	v_mfma_f32_16x16x32_bf16 v[12:15], v[142:145], v[226:229], v[12:15]
	v_mfma_f32_16x16x32_bf16 v[16:19], v[164:167], v[226:229], v[16:19]
	v_mfma_f32_16x16x32_bf16 v[58:61], v[150:153], v[196:199], v[58:61]
	v_mfma_f32_16x16x32_bf16 v[62:65], v[168:171], v[196:199], v[62:65]
	v_mfma_f32_16x16x32_bf16 v[42:45], v[150:153], v[208:211], v[42:45]
	v_mfma_f32_16x16x32_bf16 v[46:49], v[168:171], v[208:211], v[46:49]
	v_mfma_f32_16x16x32_bf16 v[24:27], v[150:153], v[216:219], v[24:27]
	v_mfma_f32_16x16x32_bf16 v[28:31], v[168:171], v[216:219], v[28:31]
	v_mfma_f32_16x16x32_bf16 v[12:15], v[150:153], v[230:233], v[12:15]
	v_mfma_f32_16x16x32_bf16 v[16:19], v[168:171], v[230:233], v[16:19]
	s_setprio 0
	s_barrier
; #define PG8_STAGE(bufoff, gbase, voff) do { _Pragma("unroll") for (int _i = 0; _i < 2; ++_i) \
;         __builtin_amdgcn_global_load_lds((const unsigned*)((const char*)(gbase) + (voff)[_i]), (LAS unsigned*)(lds + (bufoff) + ldsw + _i * 8192), 16, 0, 0); } while (0)
; #define PG8_STAGE_A(bufoff, h, abase) do { _Pragma("unroll") for (int _i = 0; _i < 2; ++_i) { \
;         const char* _src = GATHER ? ((const char*)(abase) + gA[h][_i]) : ((const char*)(abase) + (size_t)(h) * hstep + voffA[_i]); \
;         __builtin_amdgcn_global_load_lds((const unsigned*)_src, (LAS unsigned*)(lds + (bufoff) + ldsw + _i * 8192), 16, 0, 0); } } while (0)
; #define PG8_LDA(dst, b, h) do { _Pragma("unroll") for (int m = 0; m < 4; ++m) PG8_LD2(dst[m], PG8_SA(b, h) + aoff + m * 2048); } while (0)
; #define PG8_LDB(dst, b, h) do { _Pragma("unroll") for (int n = 0; n < 2; ++n) PG8_LD2(dst[n], PG8_SB(b, h) + boff + n * 2048); } while (0)
; #define PG8_WAIT_V(n) asm volatile("s_waitcnt vmcnt(" #n ")" ::: "memory")
; #define PG8_WAIT_L(n) asm volatile("s_waitcnt lgkmcnt(" #n ")" ::: "memory")
; #define PG8_BAR __builtin_amdgcn_s_barrier()
; #define PG8_SCHED __builtin_amdgcn_sched_barrier(0)
; template <int DT  , class Epi, class Sched, class Hook = NoHook>
; __device__ __forceinline__ void gemm_phase(LAS unsigned char* lds, const Sched& S, const Epi& E, int wave_s, LAS unsigned char* aux  ,
;                                            const Hook& H = Hook()  ) {
;     ...
;             PG8_LDB(B0, 1, 0); PG8_LDB(B1, 1, 1); PG8_SCHED; PG8_LDA(At, 1, 0); PG8_STAGE_A(PG8_SA(0, 1), 1, a2);
;             PG8_WAIT_V(8); PG8_WAIT_L(0); PG8_BAR; PG8_MMA(0, 0, At, B0); PG8_MMA(0, 1, At, B1); PG8_BAR; PG8_SCHED;
;             PG8_LDA(At, 1, 1); PG8_STAGE(PG8_SB(1, 0), b3, voffB); PG8_STAGE(PG8_SB(1, 1), b3 + hstep, voffB); PG8_STAGE_A(PG8_SA(1, 0), 0, a3);
;             PG8_WAIT_V(8); PG8_WAIT_L(0); PG8_BAR; PG8_MMA(1, 0, At, B0); PG8_MMA(1, 1, At, B1); PG8_BAR; PG8_SCHED;
;         }
;         if (wr == 0) PG8_BAR;
	ds_read_b128 v[130:133], v186
	ds_read_b128 v[134:137], v187
	ds_read_b128 v[138:141], v178
	ds_read_b128 v[142:145], v179
	ds_read_b128 v[146:149], v188
	ds_read_b128 v[150:153], v189
	ds_read_b128 v[164:167], v190
	ds_read_b128 v[168:171], v191
	s_add_u32 s20, s20, 0x40000
	s_addc_u32 s21, s21, 0
	s_mov_b32 m0, s30
	v_lshl_add_u64 v[240:241], s[20:21], 0, v[158:159]
	ds_read_b128 v[172:175], v192 offset:32768
	ds_read_b128 v[196:199], v192 offset:33792
	ds_read_b128 v[204:207], v192 offset:34816
	ds_read_b128 v[208:211], v192 offset:35840
	ds_read_b128 v[212:215], v192 offset:36864
	ds_read_b128 v[216:219], v192 offset:37888
	ds_read_b128 v[226:229], v192 offset:38912
	ds_read_b128 v[230:233], v192 offset:39936
	global_load_lds_dwordx4 v[240:241], off
	v_lshl_add_u64 v[240:241], s[20:21], 0, v[156:157]
	s_mov_b32 m0, s31
	s_nop 0
	global_load_lds_dwordx4 v[240:241], off
	s_waitcnt vmcnt(8)
	s_waitcnt lgkmcnt(0)
	s_barrier
	s_setprio 1
	s_waitcnt lgkmcnt(0)
	v_mfma_f32_16x16x32_bf16 v[126:129], v[138:141], v[172:175], v[126:129]
	v_mfma_f32_16x16x32_bf16 v[122:125], v[134:137], v[172:175], v[122:125]
	v_mfma_f32_16x16x32_bf16 v[110:113], v[138:141], v[204:207], v[110:113]
	v_mfma_f32_16x16x32_bf16 v[106:109], v[134:137], v[204:207], v[106:109]
	v_mfma_f32_16x16x32_bf16 v[94:97], v[138:141], v[212:215], v[94:97]
	v_mfma_f32_16x16x32_bf16 v[90:93], v[134:137], v[212:215], v[90:93]
	v_mfma_f32_16x16x32_bf16 v[86:89], v[138:141], v[226:229], v[86:89]
	v_mfma_f32_16x16x32_bf16 v[78:81], v[134:137], v[226:229], v[78:81]
	v_mfma_f32_16x16x32_bf16 v[126:129], v[130:133], v[196:199], v[126:129]
	v_mfma_f32_16x16x32_bf16 v[122:125], v[146:149], v[196:199], v[122:125]
	v_mfma_f32_16x16x32_bf16 v[110:113], v[130:133], v[208:211], v[110:113]
	v_mfma_f32_16x16x32_bf16 v[106:109], v[146:149], v[208:211], v[106:109]
	v_mfma_f32_16x16x32_bf16 v[94:97], v[130:133], v[216:219], v[94:97]
	v_mfma_f32_16x16x32_bf16 v[90:93], v[146:149], v[216:219], v[90:93]
	v_mfma_f32_16x16x32_bf16 v[86:89], v[130:133], v[230:233], v[86:89]
	v_mfma_f32_16x16x32_bf16 v[78:81], v[146:149], v[230:233], v[78:81]
	v_mfma_f32_16x16x32_bf16 v[118:121], v[142:145], v[172:175], v[118:121]
	v_mfma_f32_16x16x32_bf16 v[114:117], v[164:167], v[172:175], v[114:117]
	v_mfma_f32_16x16x32_bf16 v[102:105], v[142:145], v[204:207], v[102:105]
	v_mfma_f32_16x16x32_bf16 v[98:101], v[164:167], v[204:207], v[98:101]
	v_mfma_f32_16x16x32_bf16 v[82:85], v[142:145], v[212:215], v[82:85]
	v_mfma_f32_16x16x32_bf16 v[74:77], v[164:167], v[212:215], v[74:77]
	v_mfma_f32_16x16x32_bf16 v[70:73], v[142:145], v[226:229], v[70:73]
	v_mfma_f32_16x16x32_bf16 v[66:69], v[164:167], v[226:229], v[66:69]
	v_mfma_f32_16x16x32_bf16 v[118:121], v[150:153], v[196:199], v[118:121]
	v_mfma_f32_16x16x32_bf16 v[114:117], v[168:171], v[196:199], v[114:117]
	v_mfma_f32_16x16x32_bf16 v[102:105], v[150:153], v[208:211], v[102:105]
	v_mfma_f32_16x16x32_bf16 v[98:101], v[168:171], v[208:211], v[98:101]
	v_mfma_f32_16x16x32_bf16 v[82:85], v[150:153], v[216:219], v[82:85]
	v_mfma_f32_16x16x32_bf16 v[74:77], v[168:171], v[216:219], v[74:77]
	v_mfma_f32_16x16x32_bf16 v[70:73], v[150:153], v[230:233], v[70:73]
	v_mfma_f32_16x16x32_bf16 v[66:69], v[168:171], v[230:233], v[66:69]
	s_setprio 0
	s_barrier
	s_mov_b32 m0, s35
	v_lshl_add_u64 v[200:201], v[200:201], 0, s[58:59]
	s_add_u32 s18, s18, 0x40080
	ds_read_b128 v[172:175], v192 offset:49152
	ds_read_b128 v[196:199], v192 offset:50176
	ds_read_b128 v[204:207], v192 offset:51200
	ds_read_b128 v[208:211], v192 offset:52224
	ds_read_b128 v[212:215], v192 offset:53248
	ds_read_b128 v[216:219], v192 offset:54272
	ds_read_b128 v[226:229], v192 offset:55296
	ds_read_b128 v[230:233], v192 offset:56320
	global_load_lds_dwordx4 v[200:201], off
	v_lshl_add_u64 v[200:201], v[234:235], 0, s[58:59]
	s_mov_b32 m0, s38
	s_addc_u32 s19, s19, 0
	global_load_lds_dwordx4 v[200:201], off
	v_lshl_add_u64 v[200:201], s[18:19], 0, v[32:33]
	s_mov_b32 m0, s44
	s_nop 0
	global_load_lds_dwordx4 v[200:201], off
	v_lshl_add_u64 v[200:201], s[18:19], 0, v[154:155]
	s_mov_b32 m0, s45
	s_nop 0
	global_load_lds_dwordx4 v[200:201], off
	v_lshl_add_u64 v[200:201], v[236:237], 0, s[58:59]
	s_mov_b32 m0, s40
	s_nop 0
	global_load_lds_dwordx4 v[200:201], off
	v_lshl_add_u64 v[200:201], v[238:239], 0, s[58:59]
	s_mov_b32 m0, s41
	s_nop 0
	global_load_lds_dwordx4 v[200:201], off
	s_waitcnt vmcnt(8)
	s_waitcnt lgkmcnt(0)
	s_barrier
	s_setprio 1
	s_waitcnt lgkmcnt(0)
	v_mfma_f32_16x16x32_bf16 v[54:57], v[138:141], v[172:175], v[54:57]
	v_mfma_f32_16x16x32_bf16 v[50:53], v[134:137], v[172:175], v[50:53]
	v_mfma_f32_16x16x32_bf16 v[38:41], v[138:141], v[204:207], v[38:41]
	v_mfma_f32_16x16x32_bf16 v[34:37], v[134:137], v[204:207], v[34:37]
	v_mfma_f32_16x16x32_bf16 v[20:23], v[138:141], v[212:215], v[20:23]
	v_mfma_f32_16x16x32_bf16 v[8:11], v[134:137], v[212:215], v[8:11]
	v_mfma_f32_16x16x32_bf16 v[4:7], v[138:141], v[226:229], v[4:7]
	v_mfma_f32_16x16x32_bf16 v[0:3], v[134:137], v[226:229], v[0:3]
	v_mfma_f32_16x16x32_bf16 v[54:57], v[130:133], v[196:199], v[54:57]
	v_mfma_f32_16x16x32_bf16 v[50:53], v[146:149], v[196:199], v[50:53]
	v_mfma_f32_16x16x32_bf16 v[38:41], v[130:133], v[208:211], v[38:41]
	v_mfma_f32_16x16x32_bf16 v[34:37], v[146:149], v[208:211], v[34:37]
	v_mfma_f32_16x16x32_bf16 v[20:23], v[130:133], v[216:219], v[20:23]
	v_mfma_f32_16x16x32_bf16 v[8:11], v[146:149], v[216:219], v[8:11]
	v_mfma_f32_16x16x32_bf16 v[4:7], v[130:133], v[230:233], v[4:7]
	v_mfma_f32_16x16x32_bf16 v[0:3], v[146:149], v[230:233], v[0:3]
	v_mfma_f32_16x16x32_bf16 v[58:61], v[142:145], v[172:175], v[58:61]
	v_mfma_f32_16x16x32_bf16 v[62:65], v[164:167], v[172:175], v[62:65]
	v_mfma_f32_16x16x32_bf16 v[42:45], v[142:145], v[204:207], v[42:45]
	v_mfma_f32_16x16x32_bf16 v[46:49], v[164:167], v[204:207], v[46:49]
	v_mfma_f32_16x16x32_bf16 v[24:27], v[142:145], v[212:215], v[24:27]
	v_mfma_f32_16x16x32_bf16 v[28:31], v[164:167], v[212:215], v[28:31]
	v_mfma_f32_16x16x32_bf16 v[12:15], v[142:145], v[226:229], v[12:15]
	v_mfma_f32_16x16x32_bf16 v[16:19], v[164:167], v[226:229], v[16:19]
	v_mfma_f32_16x16x32_bf16 v[58:61], v[150:153], v[196:199], v[58:61]
	v_mfma_f32_16x16x32_bf16 v[62:65], v[168:171], v[196:199], v[62:65]
	v_mfma_f32_16x16x32_bf16 v[42:45], v[150:153], v[208:211], v[42:45]
	v_mfma_f32_16x16x32_bf16 v[46:49], v[168:171], v[208:211], v[46:49]
	v_mfma_f32_16x16x32_bf16 v[24:27], v[150:153], v[216:219], v[24:27]
	v_mfma_f32_16x16x32_bf16 v[28:31], v[168:171], v[216:219], v[28:31]
	v_mfma_f32_16x16x32_bf16 v[12:15], v[150:153], v[230:233], v[12:15]
	v_mfma_f32_16x16x32_bf16 v[16:19], v[168:171], v[230:233], v[16:19]
	s_setprio 0
	s_barrier
	s_add_i32 s68, s68, 2
	s_add_u32 s16, s16, 0x100
	s_addc_u32 s17, s17, 0
	s_add_u32 s65, s65, 0x100
	s_addc_u32 s67, s67, 0
	s_cmp_gt_u32 s68, 13
	s_cbranch_scc0 .LBB0_428
	s_and_b64 vcc, exec, s[6:7]
	v_readlane_b32 s51, v252, 33
	v_readlane_b32 s57, v253, 8
	v_readlane_b32 s65, v254, 26
	s_cbranch_vccz .LBB0_431
	s_barrier

; #define LAS __attribute__((address_space(3)))
; #define PG8_STAGE(bufoff, gbase, voff) do { _Pragma("unroll") for (int _i = 0; _i < 2; ++_i) \
;         __builtin_amdgcn_global_load_lds((const unsigned*)((const char*)(gbase) + (voff)[_i]), (LAS unsigned*)(lds + (bufoff) + ldsw + _i * 8192), 16, 0, 0); } while (0)
; #define PG8_STAGE_A(bufoff, h, abase) do { _Pragma("unroll") for (int _i = 0; _i < 2; ++_i) { \
;         const char* _src = GATHER ? ((const char*)(abase) + gA[h][_i]) : ((const char*)(abase) + (size_t)(h) * hstep + voffA[_i]); \
;         __builtin_amdgcn_global_load_lds((const unsigned*)_src, (LAS unsigned*)(lds + (bufoff) + ldsw + _i * 8192), 16, 0, 0); } } while (0)
; #define PG8_WAIT_V(n) asm volatile("s_waitcnt vmcnt(" #n ")" ::: "memory")
; template <int DT  , class Epi, class Sched, class Hook = NoHook>
; __device__ __forceinline__ void gemm_phase(LAS unsigned char* lds, const Sched& S, const Epi& E, int wave_s, LAS unsigned char* aux  ,
;                                            const Hook& H = Hook()  ) {
;     ...
;         const bool has_next = S.next(ui + 1, nxt);
;         const char* nA = has_next ? S.aptr(nxt) : cA; const char* nB = has_next ? S.bptr(nxt) : cB;
;         {
;             if constexpr (GATHER) { if (has_next && wid == 0) __builtin_amdgcn_global_load_lds((const unsigned*)(S.list_src(nxt) + 4 * lane), (LAS unsigned*)(aux + ((ui + 1) & 1) * 1024), 16, 0, 0); }
;             if constexpr (Epi::PREFETCH) E.prefetch(cur, aux + 2048 + (ui & 1) * 3072, wid, lane);
;         }
;         for (int t = 0; t < nt; t += 2) {
;             const bool last = (t == nt - 2);
;             const char* a1 = cA + (size_t)(t + 1) * kstep;
;             const char* a2 = last ? nA : cA + (size_t)(t + 2) * kstep; const char* b2 = last ? nB : cB + (size_t)(t + 2) * kstep;
;             const char* a3 = a2 + kstep; const char* b3 = b2 + kstep;
;             PG8_LDB(B0, 0, 0); PG8_LDB(B1, 0, 1); PG8_SCHED; PG8_LDA(At, 0, 0); PG8_STAGE_A(PG8_SA(1, 1), 1, a1);
;             if (GATHER) { if (last && has_next) S.gather_lds(nxt, gA, tid, aux + ((ui + 1) & 1) * 1024); }
;             PG8_WAIT_V(8); PG8_WAIT_L(0); PG8_BAR; PG8_MMA(0, 0, At, B0); PG8_MMA(0, 1, At, B1); PG8_BAR; PG8_SCHED;
;             PG8_LDA(At, 0, 1); PG8_STAGE(PG8_SB(0, 0), b2, voffB); PG8_STAGE(PG8_SB(0, 1), b2 + hstep, voffB); PG8_STAGE_A(PG8_SA(0, 0), 0, a2);
.LBB0_576:
	s_lshl_b32 s4, s74, 10
	s_and_b32 s4, s4, 0x400
	v_lshlrev_b32_e32 v0, 2, v208
	s_add_i32 s77, s4, 0
	v_add_u32_e32 v0, 0, v0
	v_readlane_b32 s24, v253, 36
	s_add_i32 s77, s77, 0x20240
	v_add_u32_e32 v209, 0x20040, v0
	v_lshl_add_u64 v[214:215], v[2:3], 0, s[54:55]
	s_mov_b32 s89, -2
	v_readlane_b32 s25, v253, 37
	ds_read_b128 v[130:133], v230
	ds_read_b128 v[134:137], v231
	ds_read_b128 v[154:157], v226
	ds_read_b128 v[42:45], v227
	ds_read_b128 v[158:161], v232
	ds_read_b128 v[50:53], v233
	ds_read_b128 v[122:125], v234
	ds_read_b128 v[126:129], v235
	s_cmp_eq_u32 s89, 4
	s_cselect_b64 s[4:5], -1, 0
	s_add_i32 m0, s28, 0xc000
	ds_read_b128 v[186:189], v242
	ds_read_b128 v[190:193], v242 offset:1024
	ds_read_b128 v[178:181], v242 offset:2048
	ds_read_b128 v[182:185], v242 offset:3072
	ds_read_b128 v[170:173], v242 offset:4096
	ds_read_b128 v[174:177], v242 offset:5120
	ds_read_b128 v[162:165], v242 offset:6144
	ds_read_b128 v[166:169], v242 offset:7168
	global_load_lds_dwordx4 v206, s[24:25]
	s_add_i32 m0, s28, 0xe000
	s_and_b64 s[18:19], s[22:23], s[4:5]
	global_load_lds_dwordx4 v204, s[24:25]
	s_andn2_b64 vcc, exec, s[18:19]
	v_mov_b32_e32 v207, v33
	v_mov_b32_e32 v205, v33
	v_mov_b64_e32 v[216:217], v[206:207]
	s_waitcnt vmcnt(8)
	s_add_u32 s42, s24, 0x80
	s_waitcnt lgkmcnt(0)
	s_addc_u32 s43, s25, 0
	s_and_b64 s[18:19], s[4:5], exec
	s_cselect_b32 s19, s37, s43
	s_cselect_b32 s18, s36, s42
	v_cndmask_b32_e64 v219, v215, v211, s[4:5]
	v_cndmask_b32_e64 v218, v214, v210, s[4:5]
	s_barrier
	s_setprio 1
	s_waitcnt lgkmcnt(0)
	v_mfma_i32_16x16x64_i8 v[150:153], v[154:157], v[186:189], 0
	v_mfma_i32_16x16x64_i8 v[146:149], v[134:137], v[186:189], 0
	v_mfma_i32_16x16x64_i8 v[142:145], v[154:157], v[178:181], 0
	v_mfma_i32_16x16x64_i8 v[138:141], v[134:137], v[178:181], 0
	v_mfma_i32_16x16x64_i8 v[118:121], v[154:157], v[170:173], 0
	v_mfma_i32_16x16x64_i8 v[114:117], v[134:137], v[170:173], 0
	v_mfma_i32_16x16x64_i8 v[110:113], v[154:157], v[162:165], 0
	v_mfma_i32_16x16x64_i8 v[106:109], v[134:137], v[162:165], 0
	v_mfma_i32_16x16x64_i8 v[150:153], v[130:133], v[190:193], v[150:153]
	v_mfma_i32_16x16x64_i8 v[146:149], v[158:161], v[190:193], v[146:149]
	v_mfma_i32_16x16x64_i8 v[142:145], v[130:133], v[182:185], v[142:145]
	v_mfma_i32_16x16x64_i8 v[138:141], v[158:161], v[182:185], v[138:141]
	v_mfma_i32_16x16x64_i8 v[118:121], v[130:133], v[174:177], v[118:121]
	v_mfma_i32_16x16x64_i8 v[114:117], v[158:161], v[174:177], v[114:117]
	v_mfma_i32_16x16x64_i8 v[110:113], v[130:133], v[166:169], v[110:113]
	v_mfma_i32_16x16x64_i8 v[106:109], v[158:161], v[166:169], v[106:109]
	v_mfma_i32_16x16x64_i8 v[66:69], v[42:45], v[186:189], 0
	v_mfma_i32_16x16x64_i8 v[70:73], v[122:125], v[186:189], 0
	v_mfma_i32_16x16x64_i8 v[58:61], v[42:45], v[178:181], 0
	v_mfma_i32_16x16x64_i8 v[62:65], v[122:125], v[178:181], 0
	v_mfma_i32_16x16x64_i8 v[46:49], v[42:45], v[170:173], 0
	v_mfma_i32_16x16x64_i8 v[54:57], v[122:125], v[170:173], 0
	v_mfma_i32_16x16x64_i8 v[34:37], v[42:45], v[162:165], 0
	v_mfma_i32_16x16x64_i8 v[38:41], v[122:125], v[162:165], 0
	v_mfma_i32_16x16x64_i8 v[66:69], v[50:53], v[190:193], v[66:69]
	v_mfma_i32_16x16x64_i8 v[70:73], v[126:129], v[190:193], v[70:73]
	v_mfma_i32_16x16x64_i8 v[58:61], v[50:53], v[182:185], v[58:61]
	v_mfma_i32_16x16x64_i8 v[62:65], v[126:129], v[182:185], v[62:65]
	v_mfma_i32_16x16x64_i8 v[46:49], v[50:53], v[174:177], v[46:49]
	v_mfma_i32_16x16x64_i8 v[54:57], v[126:129], v[174:177], v[54:57]
	v_mfma_i32_16x16x64_i8 v[34:37], v[50:53], v[166:169], v[34:37]
	v_mfma_i32_16x16x64_i8 v[38:41], v[126:129], v[166:169], v[38:41]
	s_setprio 0
	s_barrier
	s_mov_b32 m0, s29
	v_lshl_add_u64 v[244:245], v[218:219], 0, v[198:199]
	ds_read_b128 v[162:165], v242 offset:16384
	ds_read_b128 v[166:169], v242 offset:17408
	ds_read_b128 v[170:173], v242 offset:18432
	ds_read_b128 v[174:177], v242 offset:19456
	ds_read_b128 v[178:181], v242 offset:20480
	ds_read_b128 v[182:185], v242 offset:21504
	ds_read_b128 v[186:189], v242 offset:22528
	ds_read_b128 v[190:193], v242 offset:23552
	global_load_lds_dwordx4 v[244:245], off
	v_lshl_add_u64 v[246:247], v[218:219], 0, v[196:197]
	s_mov_b32 m0, s30
	v_lshl_add_u64 v[248:249], v[218:219], 0, s[70:71]
	global_load_lds_dwordx4 v[246:247], off
	v_lshl_add_u64 v[194:195], v[248:249], 0, v[198:199]
	s_mov_b32 m0, s31
	v_mov_b32_e32 v201, v33
	global_load_lds_dwordx4 v[194:195], off
	v_lshl_add_u64 v[194:195], v[248:249], 0, v[196:197]
	s_mov_b32 m0, s34
	v_lshl_add_u64 v[248:249], s[18:19], 0, v[200:201]
	global_load_lds_dwordx4 v[194:195], off
	s_mov_b32 m0, s28
	v_lshl_add_u64 v[194:195], s[18:19], 0, v[32:33]
	global_load_lds_dwordx4 v32, s[18:19]
	s_mov_b32 m0, s35
	s_nop 0
	global_load_lds_dwordx4 v200, s[18:19]
	s_waitcnt vmcnt(8)
	s_waitcnt lgkmcnt(0)
	s_barrier
; #define PG8_STAGE_A(bufoff, h, abase) do { _Pragma("unroll") for (int _i = 0; _i < 2; ++_i) { \
;         const char* _src = GATHER ? ((const char*)(abase) + gA[h][_i]) : ((const char*)(abase) + (size_t)(h) * hstep + voffA[_i]); \
;         __builtin_amdgcn_global_load_lds((const unsigned*)_src, (LAS unsigned*)(lds + (bufoff) + ldsw + _i * 8192), 16, 0, 0); } } while (0)
; #define PG8_LDA(dst, b, h) do { _Pragma("unroll") for (int m = 0; m < 4; ++m) PG8_LD2(dst[m], PG8_SA(b, h) + aoff + m * 2048); } while (0)
; #define PG8_LDB(dst, b, h) do { _Pragma("unroll") for (int n = 0; n < 2; ++n) PG8_LD2(dst[n], PG8_SB(b, h) + boff + n * 2048); } while (0)
; #define PG8_WAIT_V(n) asm volatile("s_waitcnt vmcnt(" #n ")" ::: "memory")
; #define PG8_WAIT_L(n) asm volatile("s_waitcnt lgkmcnt(" #n ")" ::: "memory")
; #define PG8_BAR __builtin_amdgcn_s_barrier()
; #define PG8_SCHED __builtin_amdgcn_sched_barrier(0)
; template <int DT  , class Epi, class Sched, class Hook = NoHook>
; __device__ __forceinline__ void gemm_phase(LAS unsigned char* lds, const Sched& S, const Epi& E, int wave_s, LAS unsigned char* aux  ,
;                                            const Hook& H = Hook()  ) {
;     ...
;             PG8_WAIT_V(8); PG8_WAIT_L(0); PG8_BAR; PG8_MMA(1, 0, At, B0); PG8_MMA(1, 1, At, B1); PG8_BAR; PG8_SCHED;
;             PG8_LDB(B0, 1, 0); PG8_LDB(B1, 1, 1); PG8_SCHED; PG8_LDA(At, 1, 0); PG8_STAGE_A(PG8_SA(0, 1), 1, a2);
;             PG8_WAIT_V(8); PG8_WAIT_L(0); PG8_BAR; PG8_MMA(0, 0, At, B0); PG8_MMA(0, 1, At, B1); PG8_BAR; PG8_SCHED;
	s_setprio 1
	s_waitcnt lgkmcnt(0)
	v_mfma_i32_16x16x64_i8 v[102:105], v[154:157], v[162:165], 0
	v_mfma_i32_16x16x64_i8 v[98:101], v[134:137], v[162:165], 0
	v_mfma_i32_16x16x64_i8 v[94:97], v[154:157], v[170:173], 0
	v_mfma_i32_16x16x64_i8 v[90:93], v[134:137], v[170:173], 0
	v_mfma_i32_16x16x64_i8 v[86:89], v[154:157], v[178:181], 0
	v_mfma_i32_16x16x64_i8 v[82:85], v[134:137], v[178:181], 0
	v_mfma_i32_16x16x64_i8 v[78:81], v[154:157], v[186:189], 0
	v_mfma_i32_16x16x64_i8 v[74:77], v[134:137], v[186:189], 0
	v_mfma_i32_16x16x64_i8 v[102:105], v[130:133], v[166:169], v[102:105]
	v_mfma_i32_16x16x64_i8 v[98:101], v[158:161], v[166:169], v[98:101]
	v_mfma_i32_16x16x64_i8 v[94:97], v[130:133], v[174:177], v[94:97]
	v_mfma_i32_16x16x64_i8 v[90:93], v[158:161], v[174:177], v[90:93]
	v_mfma_i32_16x16x64_i8 v[86:89], v[130:133], v[182:185], v[86:89]
	v_mfma_i32_16x16x64_i8 v[82:85], v[158:161], v[182:185], v[82:85]
	v_mfma_i32_16x16x64_i8 v[78:81], v[130:133], v[190:193], v[78:81]
	v_mfma_i32_16x16x64_i8 v[74:77], v[158:161], v[190:193], v[74:77]
	v_mfma_i32_16x16x64_i8 v[24:27], v[42:45], v[162:165], 0
	v_mfma_i32_16x16x64_i8 v[28:31], v[122:125], v[162:165], 0
	v_mfma_i32_16x16x64_i8 v[16:19], v[42:45], v[170:173], 0
	v_mfma_i32_16x16x64_i8 v[20:23], v[122:125], v[170:173], 0
	v_mfma_i32_16x16x64_i8 v[8:11], v[42:45], v[178:181], 0
	v_mfma_i32_16x16x64_i8 v[12:15], v[122:125], v[178:181], 0
	v_mfma_i32_16x16x64_i8 v[0:3], v[42:45], v[186:189], 0
	v_mfma_i32_16x16x64_i8 v[4:7], v[122:125], v[186:189], 0
	v_mfma_i32_16x16x64_i8 v[24:27], v[50:53], v[166:169], v[24:27]
	v_mfma_i32_16x16x64_i8 v[28:31], v[126:129], v[166:169], v[28:31]
	v_mfma_i32_16x16x64_i8 v[16:19], v[50:53], v[174:177], v[16:19]
	v_mfma_i32_16x16x64_i8 v[20:23], v[126:129], v[174:177], v[20:23]
	v_mfma_i32_16x16x64_i8 v[8:11], v[50:53], v[182:185], v[8:11]
	v_mfma_i32_16x16x64_i8 v[12:15], v[126:129], v[182:185], v[12:15]
	v_mfma_i32_16x16x64_i8 v[0:3], v[50:53], v[190:193], v[0:3]
	v_mfma_i32_16x16x64_i8 v[4:7], v[126:129], v[190:193], v[4:7]
	s_setprio 0
	s_barrier
	ds_read_b128 v[42:45], v236
	ds_read_b128 v[50:53], v237
	ds_read_b128 v[122:125], v228
	ds_read_b128 v[126:129], v229
	ds_read_b128 v[130:133], v238
	ds_read_b128 v[134:137], v239
	ds_read_b128 v[154:157], v240
	ds_read_b128 v[158:161], v241
	s_mov_b32 m0, s38
	v_lshl_add_u64 v[216:217], s[18:19], 0, v[216:217]
	ds_read_b128 v[162:165], v242 offset:32768
	ds_read_b128 v[166:169], v242 offset:33792
	ds_read_b128 v[170:173], v242 offset:34816
	ds_read_b128 v[174:177], v242 offset:35840
	ds_read_b128 v[178:181], v242 offset:36864
	ds_read_b128 v[182:185], v242 offset:37888
	ds_read_b128 v[186:189], v242 offset:38912
	ds_read_b128 v[190:193], v242 offset:39936
	global_load_lds_dwordx4 v[216:217], off
	v_lshl_add_u64 v[216:217], s[18:19], 0, v[204:205]
	s_mov_b32 m0, s44
	s_nop 0
	global_load_lds_dwordx4 v[216:217], off
	s_waitcnt vmcnt(8)
	s_waitcnt lgkmcnt(0)
	s_barrier
	s_setprio 1
	s_waitcnt lgkmcnt(0)
	v_mfma_i32_16x16x64_i8 v[150:153], v[122:125], v[162:165], v[150:153]
	v_mfma_i32_16x16x64_i8 v[146:149], v[50:53], v[162:165], v[146:149]
	v_mfma_i32_16x16x64_i8 v[142:145], v[122:125], v[170:173], v[142:145]
	v_mfma_i32_16x16x64_i8 v[138:141], v[50:53], v[170:173], v[138:141]
	v_mfma_i32_16x16x64_i8 v[118:121], v[122:125], v[178:181], v[118:121]
	v_mfma_i32_16x16x64_i8 v[114:117], v[50:53], v[178:181], v[114:117]
	v_mfma_i32_16x16x64_i8 v[110:113], v[122:125], v[186:189], v[110:113]
	v_mfma_i32_16x16x64_i8 v[106:109], v[50:53], v[186:189], v[106:109]
	v_mfma_i32_16x16x64_i8 v[150:153], v[42:45], v[166:169], v[150:153]
	v_mfma_i32_16x16x64_i8 v[146:149], v[130:133], v[166:169], v[146:149]
	v_mfma_i32_16x16x64_i8 v[142:145], v[42:45], v[174:177], v[142:145]
	v_mfma_i32_16x16x64_i8 v[138:141], v[130:133], v[174:177], v[138:141]
	v_mfma_i32_16x16x64_i8 v[118:121], v[42:45], v[182:185], v[118:121]
	v_mfma_i32_16x16x64_i8 v[114:117], v[130:133], v[182:185], v[114:117]
	v_mfma_i32_16x16x64_i8 v[110:113], v[42:45], v[190:193], v[110:113]
	v_mfma_i32_16x16x64_i8 v[106:109], v[130:133], v[190:193], v[106:109]
	v_mfma_i32_16x16x64_i8 v[66:69], v[126:129], v[162:165], v[66:69]
	v_mfma_i32_16x16x64_i8 v[70:73], v[154:157], v[162:165], v[70:73]
	v_mfma_i32_16x16x64_i8 v[58:61], v[126:129], v[170:173], v[58:61]
	v_mfma_i32_16x16x64_i8 v[62:65], v[154:157], v[170:173], v[62:65]
	v_mfma_i32_16x16x64_i8 v[46:49], v[126:129], v[178:181], v[46:49]
	v_mfma_i32_16x16x64_i8 v[54:57], v[154:157], v[178:181], v[54:57]
	v_mfma_i32_16x16x64_i8 v[34:37], v[126:129], v[186:189], v[34:37]
	v_mfma_i32_16x16x64_i8 v[38:41], v[154:157], v[186:189], v[38:41]
	v_mfma_i32_16x16x64_i8 v[66:69], v[134:137], v[166:169], v[66:69]
	v_mfma_i32_16x16x64_i8 v[70:73], v[158:161], v[166:169], v[70:73]
	v_mfma_i32_16x16x64_i8 v[58:61], v[134:137], v[174:177], v[58:61]
	v_mfma_i32_16x16x64_i8 v[62:65], v[158:161], v[174:177], v[62:65]
	v_mfma_i32_16x16x64_i8 v[46:49], v[134:137], v[182:185], v[46:49]
	v_mfma_i32_16x16x64_i8 v[54:57], v[158:161], v[182:185], v[54:57]
	v_mfma_i32_16x16x64_i8 v[34:37], v[134:137], v[190:193], v[34:37]
	v_mfma_i32_16x16x64_i8 v[38:41], v[158:161], v[190:193], v[38:41]
	s_setprio 0
	s_barrier
; #define PG8_STAGE(bufoff, gbase, voff) do { _Pragma("unroll") for (int _i = 0; _i < 2; ++_i) \
;         __builtin_amdgcn_global_load_lds((const unsigned*)((const char*)(gbase) + (voff)[_i]), (LAS unsigned*)(lds + (bufoff) + ldsw + _i * 8192), 16, 0, 0); } while (0)
; #define PG8_STAGE_A(bufoff, h, abase) do { _Pragma("unroll") for (int _i = 0; _i < 2; ++_i) { \
;         const char* _src = GATHER ? ((const char*)(abase) + gA[h][_i]) : ((const char*)(abase) + (size_t)(h) * hstep + voffA[_i]); \
;         __builtin_amdgcn_global_load_lds((const unsigned*)_src, (LAS unsigned*)(lds + (bufoff) + ldsw + _i * 8192), 16, 0, 0); } } while (0)
; #define PG8_LDA(dst, b, h) do { _Pragma("unroll") for (int m = 0; m < 4; ++m) PG8_LD2(dst[m], PG8_SA(b, h) + aoff + m * 2048); } while (0)
; #define PG8_WAIT_V(n) asm volatile("s_waitcnt vmcnt(" #n ")" ::: "memory")
; #define PG8_WAIT_L(n) asm volatile("s_waitcnt lgkmcnt(" #n ")" ::: "memory")
; #define PG8_BAR __builtin_amdgcn_s_barrier()
; #define PG8_SCHED __builtin_amdgcn_sched_barrier(0)
; template <int DT  , class Epi, class Sched, class Hook = NoHook>
; __device__ __forceinline__ void gemm_phase(LAS unsigned char* lds, const Sched& S, const Epi& E, int wave_s, LAS unsigned char* aux  ,
;                                            const Hook& H = Hook()  ) {
;     ...
;             PG8_LDA(At, 1, 1); PG8_STAGE(PG8_SB(1, 0), b3, voffB); PG8_STAGE(PG8_SB(1, 1), b3 + hstep, voffB); PG8_STAGE_A(PG8_SA(1, 0), 0, a3);
;             PG8_WAIT_V(8); PG8_WAIT_L(0); PG8_BAR; PG8_MMA(1, 0, At, B0); PG8_MMA(1, 1, At, B1); PG8_BAR; PG8_SCHED;
	s_mov_b32 m0, s45
	v_lshl_add_u64 v[216:217], v[244:245], 0, s[58:59]
	ds_read_b128 v[162:165], v242 offset:49152
	ds_read_b128 v[166:169], v242 offset:50176
	ds_read_b128 v[170:173], v242 offset:51200
	ds_read_b128 v[174:177], v242 offset:52224
	ds_read_b128 v[178:181], v242 offset:53248
	ds_read_b128 v[182:185], v242 offset:54272
	ds_read_b128 v[186:189], v242 offset:55296
	ds_read_b128 v[190:193], v242 offset:56320
	global_load_lds_dwordx4 v[216:217], off
	v_lshl_add_u64 v[216:217], v[246:247], 0, s[58:59]
	s_mov_b32 m0, s46
	v_lshl_add_u64 v[194:195], v[194:195], 0, s[58:59]
	global_load_lds_dwordx4 v[216:217], off
	v_lshl_add_u64 v[216:217], v[218:219], 0, s[62:63]
	v_lshl_add_u64 v[218:219], v[216:217], 0, v[198:199]
	s_mov_b32 m0, s51
	v_lshl_add_u64 v[216:217], v[216:217], 0, v[196:197]
	global_load_lds_dwordx4 v[218:219], off
	s_mov_b32 m0, s57
	s_nop 0
	global_load_lds_dwordx4 v[216:217], off
	s_mov_b32 m0, s47
	s_nop 0
	global_load_lds_dwordx4 v[194:195], off
	v_lshl_add_u64 v[194:195], v[248:249], 0, s[58:59]
	s_mov_b32 m0, s48
	s_nop 0
	global_load_lds_dwordx4 v[194:195], off
	s_waitcnt vmcnt(8)
	s_waitcnt lgkmcnt(0)
	s_barrier
	s_setprio 1
	s_waitcnt lgkmcnt(0)
	v_mfma_i32_16x16x64_i8 v[102:105], v[122:125], v[162:165], v[102:105]
	v_mfma_i32_16x16x64_i8 v[94:97], v[122:125], v[170:173], v[94:97]
	v_mfma_i32_16x16x64_i8 v[86:89], v[122:125], v[178:181], v[86:89]
	v_mfma_i32_16x16x64_i8 v[78:81], v[122:125], v[186:189], v[78:81]
	v_mfma_i32_16x16x64_i8 v[102:105], v[42:45], v[166:169], v[102:105]
	v_mfma_i32_16x16x64_i8 v[98:101], v[50:53], v[162:165], v[98:101]
	v_mfma_i32_16x16x64_i8 v[94:97], v[42:45], v[174:177], v[94:97]
	v_mfma_i32_16x16x64_i8 v[90:93], v[50:53], v[170:173], v[90:93]
	v_mfma_i32_16x16x64_i8 v[86:89], v[42:45], v[182:185], v[86:89]
	v_mfma_i32_16x16x64_i8 v[82:85], v[50:53], v[178:181], v[82:85]
	v_mfma_i32_16x16x64_i8 v[78:81], v[42:45], v[190:193], v[78:81]
	v_mfma_i32_16x16x64_i8 v[42:45], v[50:53], v[186:189], v[74:77]
	v_mfma_i32_16x16x64_i8 v[98:101], v[130:133], v[166:169], v[98:101]
	v_mfma_i32_16x16x64_i8 v[90:93], v[130:133], v[174:177], v[90:93]
	v_mfma_i32_16x16x64_i8 v[82:85], v[130:133], v[182:185], v[82:85]
	v_mfma_i32_16x16x64_i8 v[74:77], v[130:133], v[190:193], v[42:45]
	v_mfma_i32_16x16x64_i8 v[24:27], v[126:129], v[162:165], v[24:27]
	v_mfma_i32_16x16x64_i8 v[28:31], v[154:157], v[162:165], v[28:31]
	v_mfma_i32_16x16x64_i8 v[16:19], v[126:129], v[170:173], v[16:19]
	v_mfma_i32_16x16x64_i8 v[20:23], v[154:157], v[170:173], v[20:23]
	v_mfma_i32_16x16x64_i8 v[8:11], v[126:129], v[178:181], v[8:11]
	v_mfma_i32_16x16x64_i8 v[12:15], v[154:157], v[178:181], v[12:15]
	v_mfma_i32_16x16x64_i8 v[0:3], v[126:129], v[186:189], v[0:3]
	v_mfma_i32_16x16x64_i8 v[4:7], v[154:157], v[186:189], v[4:7]
	v_mfma_i32_16x16x64_i8 v[24:27], v[134:137], v[166:169], v[24:27]
	v_mfma_i32_16x16x64_i8 v[28:31], v[158:161], v[166:169], v[28:31]
	v_mfma_i32_16x16x64_i8 v[16:19], v[134:137], v[174:177], v[16:19]
	v_mfma_i32_16x16x64_i8 v[20:23], v[158:161], v[174:177], v[20:23]
	v_mfma_i32_16x16x64_i8 v[8:11], v[134:137], v[182:185], v[8:11]
	v_mfma_i32_16x16x64_i8 v[12:15], v[158:161], v[182:185], v[12:15]
	v_mfma_i32_16x16x64_i8 v[0:3], v[134:137], v[190:193], v[0:3]
	v_mfma_i32_16x16x64_i8 v[4:7], v[158:161], v[190:193], v[4:7]
	s_setprio 0
	s_barrier
	s_add_i32 s89, s89, 2
	s_add_u32 s24, s24, 0x100
	s_addc_u32 s25, s25, 0
	s_cmp_gt_u32 s89, 5
	v_lshl_add_u64 v[214:215], v[214:215], 0, s[54:55]
	s_branch .LBB0_579

; #define PG8_STAGE(bufoff, gbase, voff) do { _Pragma("unroll") for (int _i = 0; _i < 2; ++_i) \
;         __builtin_amdgcn_global_load_lds((const unsigned*)((const char*)(gbase) + (voff)[_i]), (LAS unsigned*)(lds + (bufoff) + ldsw + _i * 8192), 16, 0, 0); } while (0)
; #define PG8_STAGE_A(bufoff, h, abase) do { _Pragma("unroll") for (int _i = 0; _i < 2; ++_i) { \
;         const char* _src = GATHER ? ((const char*)(abase) + gA[h][_i]) : ((const char*)(abase) + (size_t)(h) * hstep + voffA[_i]); \
;         __builtin_amdgcn_global_load_lds((const unsigned*)_src, (LAS unsigned*)(lds + (bufoff) + ldsw + _i * 8192), 16, 0, 0); } } while (0)
; #define PG8_LDA(dst, b, h) do { _Pragma("unroll") for (int m = 0; m < 4; ++m) PG8_LD2(dst[m], PG8_SA(b, h) + aoff + m * 2048); } while (0)
; #define PG8_LDB(dst, b, h) do { _Pragma("unroll") for (int n = 0; n < 2; ++n) PG8_LD2(dst[n], PG8_SB(b, h) + boff + n * 2048); } while (0)
; #define PG8_WAIT_V(n) asm volatile("s_waitcnt vmcnt(" #n ")" ::: "memory")
; #define PG8_WAIT_L(n) asm volatile("s_waitcnt lgkmcnt(" #n ")" ::: "memory")
; #define PG8_BAR __builtin_amdgcn_s_barrier()
; #define PG8_SCHED __builtin_amdgcn_sched_barrier(0)
; template <int DT  , class Epi, class Sched, class Hook = NoHook>
; __device__ __forceinline__ void gemm_phase(LAS unsigned char* lds, const Sched& S, const Epi& E, int wave_s, LAS unsigned char* aux  ,
;                                            const Hook& H = Hook()  ) {
;     ...
;             PG8_WAIT_V(8); PG8_WAIT_L(0); PG8_BAR; PG8_MMA(0, 0, At, B0); PG8_MMA(0, 1, At, B1); PG8_BAR; PG8_SCHED;
;             PG8_LDA(At, 0, 1); PG8_STAGE(PG8_SB(0, 0), b2, voffB); PG8_STAGE(PG8_SB(0, 1), b2 + hstep, voffB); PG8_STAGE_A(PG8_SA(0, 0), 0, a2);
;             PG8_WAIT_V(8); PG8_WAIT_L(0); PG8_BAR; PG8_MMA(1, 0, At, B0); PG8_MMA(1, 1, At, B1); PG8_BAR; PG8_SCHED;
;             PG8_LDB(B0, 1, 0); PG8_LDB(B1, 1, 1); PG8_SCHED; PG8_LDA(At, 1, 0); PG8_STAGE_A(PG8_SA(0, 1), 1, a2);
;             PG8_WAIT_V(8); PG8_WAIT_L(0); PG8_BAR; PG8_MMA(0, 0, At, B0); PG8_MMA(0, 1, At, B1); PG8_BAR; PG8_SCHED;
.LBB0_578:
	s_waitcnt vmcnt(8)
	s_add_u32 s42, s24, 0x80
	s_waitcnt lgkmcnt(0)
	s_addc_u32 s43, s25, 0
	s_and_b64 s[18:19], s[4:5], exec
	s_cselect_b32 s19, s37, s43
	s_cselect_b32 s18, s36, s42
	v_cndmask_b32_e64 v219, v215, v211, s[4:5]
	v_cndmask_b32_e64 v218, v214, v210, s[4:5]
	s_barrier
	s_setprio 1
	s_waitcnt lgkmcnt(0)
	v_mfma_i32_16x16x64_i8 v[150:153], v[154:157], v[186:189], v[150:153]
	v_mfma_i32_16x16x64_i8 v[146:149], v[134:137], v[186:189], v[146:149]
	v_mfma_i32_16x16x64_i8 v[142:145], v[154:157], v[178:181], v[142:145]
	v_mfma_i32_16x16x64_i8 v[138:141], v[134:137], v[178:181], v[138:141]
	v_mfma_i32_16x16x64_i8 v[118:121], v[154:157], v[170:173], v[118:121]
	v_mfma_i32_16x16x64_i8 v[114:117], v[134:137], v[170:173], v[114:117]
	v_mfma_i32_16x16x64_i8 v[110:113], v[154:157], v[162:165], v[110:113]
	v_mfma_i32_16x16x64_i8 v[106:109], v[134:137], v[162:165], v[106:109]
	v_mfma_i32_16x16x64_i8 v[150:153], v[130:133], v[190:193], v[150:153]
	v_mfma_i32_16x16x64_i8 v[146:149], v[158:161], v[190:193], v[146:149]
	v_mfma_i32_16x16x64_i8 v[142:145], v[130:133], v[182:185], v[142:145]
	v_mfma_i32_16x16x64_i8 v[138:141], v[158:161], v[182:185], v[138:141]
	v_mfma_i32_16x16x64_i8 v[118:121], v[130:133], v[174:177], v[118:121]
	v_mfma_i32_16x16x64_i8 v[114:117], v[158:161], v[174:177], v[114:117]
	v_mfma_i32_16x16x64_i8 v[110:113], v[130:133], v[166:169], v[110:113]
	v_mfma_i32_16x16x64_i8 v[106:109], v[158:161], v[166:169], v[106:109]
	v_mfma_i32_16x16x64_i8 v[66:69], v[42:45], v[186:189], v[66:69]
	v_mfma_i32_16x16x64_i8 v[70:73], v[122:125], v[186:189], v[70:73]
	v_mfma_i32_16x16x64_i8 v[58:61], v[42:45], v[178:181], v[58:61]
	v_mfma_i32_16x16x64_i8 v[62:65], v[122:125], v[178:181], v[62:65]
	v_mfma_i32_16x16x64_i8 v[46:49], v[42:45], v[170:173], v[46:49]
	v_mfma_i32_16x16x64_i8 v[54:57], v[122:125], v[170:173], v[54:57]
	v_mfma_i32_16x16x64_i8 v[34:37], v[42:45], v[162:165], v[34:37]
	v_mfma_i32_16x16x64_i8 v[38:41], v[122:125], v[162:165], v[38:41]
	v_mfma_i32_16x16x64_i8 v[66:69], v[50:53], v[190:193], v[66:69]
	v_mfma_i32_16x16x64_i8 v[70:73], v[126:129], v[190:193], v[70:73]
	v_mfma_i32_16x16x64_i8 v[58:61], v[50:53], v[182:185], v[58:61]
	v_mfma_i32_16x16x64_i8 v[62:65], v[126:129], v[182:185], v[62:65]
	v_mfma_i32_16x16x64_i8 v[46:49], v[50:53], v[174:177], v[46:49]
	v_mfma_i32_16x16x64_i8 v[54:57], v[126:129], v[174:177], v[54:57]
	v_mfma_i32_16x16x64_i8 v[34:37], v[50:53], v[166:169], v[34:37]
	v_mfma_i32_16x16x64_i8 v[38:41], v[126:129], v[166:169], v[38:41]
	s_setprio 0
	s_barrier
	s_mov_b32 m0, s29
	v_lshl_add_u64 v[244:245], v[218:219], 0, v[198:199]
	ds_read_b128 v[162:165], v242 offset:16384
	ds_read_b128 v[166:169], v242 offset:17408
	ds_read_b128 v[170:173], v242 offset:18432
	ds_read_b128 v[174:177], v242 offset:19456
	ds_read_b128 v[178:181], v242 offset:20480
	ds_read_b128 v[182:185], v242 offset:21504
	ds_read_b128 v[186:189], v242 offset:22528
	ds_read_b128 v[190:193], v242 offset:23552
	global_load_lds_dwordx4 v[244:245], off
	v_lshl_add_u64 v[246:247], v[218:219], 0, v[196:197]
	s_mov_b32 m0, s30
	v_lshl_add_u64 v[248:249], v[218:219], 0, s[70:71]
	global_load_lds_dwordx4 v[246:247], off
	v_lshl_add_u64 v[194:195], v[248:249], 0, v[198:199]
	s_mov_b32 m0, s31
	v_mov_b32_e32 v201, v33
	global_load_lds_dwordx4 v[194:195], off
	v_lshl_add_u64 v[194:195], v[248:249], 0, v[196:197]
	s_mov_b32 m0, s34
	v_lshl_add_u64 v[248:249], s[18:19], 0, v[200:201]
	global_load_lds_dwordx4 v[194:195], off
	s_mov_b32 m0, s28
	v_lshl_add_u64 v[194:195], s[18:19], 0, v[32:33]
	global_load_lds_dwordx4 v32, s[18:19]
	s_mov_b32 m0, s35
	s_nop 0
	global_load_lds_dwordx4 v200, s[18:19]
	s_waitcnt vmcnt(8)
	s_waitcnt lgkmcnt(0)
	s_barrier
	s_setprio 1
	s_waitcnt lgkmcnt(0)
	v_mfma_i32_16x16x64_i8 v[102:105], v[154:157], v[162:165], v[102:105]
	v_mfma_i32_16x16x64_i8 v[98:101], v[134:137], v[162:165], v[98:101]
	v_mfma_i32_16x16x64_i8 v[94:97], v[154:157], v[170:173], v[94:97]
	v_mfma_i32_16x16x64_i8 v[90:93], v[134:137], v[170:173], v[90:93]
	v_mfma_i32_16x16x64_i8 v[86:89], v[154:157], v[178:181], v[86:89]
	v_mfma_i32_16x16x64_i8 v[82:85], v[134:137], v[178:181], v[82:85]
	v_mfma_i32_16x16x64_i8 v[78:81], v[154:157], v[186:189], v[78:81]
	v_mfma_i32_16x16x64_i8 v[74:77], v[134:137], v[186:189], v[74:77]
	v_mfma_i32_16x16x64_i8 v[102:105], v[130:133], v[166:169], v[102:105]
	v_mfma_i32_16x16x64_i8 v[98:101], v[158:161], v[166:169], v[98:101]
	v_mfma_i32_16x16x64_i8 v[94:97], v[130:133], v[174:177], v[94:97]
	v_mfma_i32_16x16x64_i8 v[90:93], v[158:161], v[174:177], v[90:93]
	v_mfma_i32_16x16x64_i8 v[86:89], v[130:133], v[182:185], v[86:89]
	v_mfma_i32_16x16x64_i8 v[82:85], v[158:161], v[182:185], v[82:85]
	v_mfma_i32_16x16x64_i8 v[78:81], v[130:133], v[190:193], v[78:81]
	v_mfma_i32_16x16x64_i8 v[74:77], v[158:161], v[190:193], v[74:77]
	v_mfma_i32_16x16x64_i8 v[24:27], v[42:45], v[162:165], v[24:27]
	v_mfma_i32_16x16x64_i8 v[28:31], v[122:125], v[162:165], v[28:31]
	v_mfma_i32_16x16x64_i8 v[16:19], v[42:45], v[170:173], v[16:19]
	v_mfma_i32_16x16x64_i8 v[20:23], v[122:125], v[170:173], v[20:23]
	v_mfma_i32_16x16x64_i8 v[8:11], v[42:45], v[178:181], v[8:11]
	v_mfma_i32_16x16x64_i8 v[12:15], v[122:125], v[178:181], v[12:15]
	v_mfma_i32_16x16x64_i8 v[0:3], v[42:45], v[186:189], v[0:3]
	v_mfma_i32_16x16x64_i8 v[4:7], v[122:125], v[186:189], v[4:7]
	v_mfma_i32_16x16x64_i8 v[24:27], v[50:53], v[166:169], v[24:27]
	v_mfma_i32_16x16x64_i8 v[28:31], v[126:129], v[166:169], v[28:31]
	v_mfma_i32_16x16x64_i8 v[16:19], v[50:53], v[174:177], v[16:19]
	v_mfma_i32_16x16x64_i8 v[20:23], v[126:129], v[174:177], v[20:23]
	v_mfma_i32_16x16x64_i8 v[8:11], v[50:53], v[182:185], v[8:11]
	v_mfma_i32_16x16x64_i8 v[12:15], v[126:129], v[182:185], v[12:15]
	v_mfma_i32_16x16x64_i8 v[0:3], v[50:53], v[190:193], v[0:3]
	v_mfma_i32_16x16x64_i8 v[4:7], v[126:129], v[190:193], v[4:7]
	s_setprio 0
	s_barrier
; #define PG8_STAGE(bufoff, gbase, voff) do { _Pragma("unroll") for (int _i = 0; _i < 2; ++_i) \
;         __builtin_amdgcn_global_load_lds((const unsigned*)((const char*)(gbase) + (voff)[_i]), (LAS unsigned*)(lds + (bufoff) + ldsw + _i * 8192), 16, 0, 0); } while (0)
; #define PG8_STAGE_A(bufoff, h, abase) do { _Pragma("unroll") for (int _i = 0; _i < 2; ++_i) { \
;         const char* _src = GATHER ? ((const char*)(abase) + gA[h][_i]) : ((const char*)(abase) + (size_t)(h) * hstep + voffA[_i]); \
;         __builtin_amdgcn_global_load_lds((const unsigned*)_src, (LAS unsigned*)(lds + (bufoff) + ldsw + _i * 8192), 16, 0, 0); } } while (0)
; #define PG8_LDA(dst, b, h) do { _Pragma("unroll") for (int m = 0; m < 4; ++m) PG8_LD2(dst[m], PG8_SA(b, h) + aoff + m * 2048); } while (0)
; #define PG8_LDB(dst, b, h) do { _Pragma("unroll") for (int n = 0; n < 2; ++n) PG8_LD2(dst[n], PG8_SB(b, h) + boff + n * 2048); } while (0)
; #define PG8_WAIT_V(n) asm volatile("s_waitcnt vmcnt(" #n ")" ::: "memory")
; #define PG8_WAIT_L(n) asm volatile("s_waitcnt lgkmcnt(" #n ")" ::: "memory")
; #define PG8_BAR __builtin_amdgcn_s_barrier()
; #define PG8_SCHED __builtin_amdgcn_sched_barrier(0)
; template <int DT  , class Epi, class Sched, class Hook = NoHook>
; __device__ __forceinline__ void gemm_phase(LAS unsigned char* lds, const Sched& S, const Epi& E, int wave_s, LAS unsigned char* aux  ,
;                                            const Hook& H = Hook()  ) {
;     ...
;             PG8_LDB(B0, 1, 0); PG8_LDB(B1, 1, 1); PG8_SCHED; PG8_LDA(At, 1, 0); PG8_STAGE_A(PG8_SA(0, 1), 1, a2);
;             PG8_WAIT_V(8); PG8_WAIT_L(0); PG8_BAR; PG8_MMA(0, 0, At, B0); PG8_MMA(0, 1, At, B1); PG8_BAR; PG8_SCHED;
;             PG8_LDA(At, 1, 1); PG8_STAGE(PG8_SB(1, 0), b3, voffB); PG8_STAGE(PG8_SB(1, 1), b3 + hstep, voffB); PG8_STAGE_A(PG8_SA(1, 0), 0, a3);
;             PG8_WAIT_V(8); PG8_WAIT_L(0); PG8_BAR; PG8_MMA(1, 0, At, B0); PG8_MMA(1, 1, At, B1); PG8_BAR; PG8_SCHED;
;         }
;         if (wr == 0) PG8_BAR;
	ds_read_b128 v[42:45], v236
	ds_read_b128 v[50:53], v237
	ds_read_b128 v[122:125], v228
	ds_read_b128 v[126:129], v229
	ds_read_b128 v[130:133], v238
	ds_read_b128 v[134:137], v239
	ds_read_b128 v[154:157], v240
	ds_read_b128 v[158:161], v241
	s_mov_b32 m0, s38
	v_lshl_add_u64 v[216:217], s[18:19], 0, v[216:217]
	ds_read_b128 v[162:165], v242 offset:32768
	ds_read_b128 v[166:169], v242 offset:33792
	ds_read_b128 v[170:173], v242 offset:34816
	ds_read_b128 v[174:177], v242 offset:35840
	ds_read_b128 v[178:181], v242 offset:36864
	ds_read_b128 v[182:185], v242 offset:37888
	ds_read_b128 v[186:189], v242 offset:38912
	ds_read_b128 v[190:193], v242 offset:39936
	global_load_lds_dwordx4 v[216:217], off
	v_lshl_add_u64 v[216:217], s[18:19], 0, v[204:205]
	s_mov_b32 m0, s44
	s_nop 0
	global_load_lds_dwordx4 v[216:217], off
	s_waitcnt vmcnt(8)
	s_waitcnt lgkmcnt(0)
	s_barrier
	s_setprio 1
	s_waitcnt lgkmcnt(0)
	v_mfma_i32_16x16x64_i8 v[150:153], v[122:125], v[162:165], v[150:153]
	v_mfma_i32_16x16x64_i8 v[146:149], v[50:53], v[162:165], v[146:149]
	v_mfma_i32_16x16x64_i8 v[142:145], v[122:125], v[170:173], v[142:145]
	v_mfma_i32_16x16x64_i8 v[138:141], v[50:53], v[170:173], v[138:141]
	v_mfma_i32_16x16x64_i8 v[118:121], v[122:125], v[178:181], v[118:121]
	v_mfma_i32_16x16x64_i8 v[114:117], v[50:53], v[178:181], v[114:117]
	v_mfma_i32_16x16x64_i8 v[110:113], v[122:125], v[186:189], v[110:113]
	v_mfma_i32_16x16x64_i8 v[106:109], v[50:53], v[186:189], v[106:109]
	v_mfma_i32_16x16x64_i8 v[150:153], v[42:45], v[166:169], v[150:153]
	v_mfma_i32_16x16x64_i8 v[146:149], v[130:133], v[166:169], v[146:149]
	v_mfma_i32_16x16x64_i8 v[142:145], v[42:45], v[174:177], v[142:145]
	v_mfma_i32_16x16x64_i8 v[138:141], v[130:133], v[174:177], v[138:141]
	v_mfma_i32_16x16x64_i8 v[118:121], v[42:45], v[182:185], v[118:121]
	v_mfma_i32_16x16x64_i8 v[114:117], v[130:133], v[182:185], v[114:117]
	v_mfma_i32_16x16x64_i8 v[110:113], v[42:45], v[190:193], v[110:113]
	v_mfma_i32_16x16x64_i8 v[106:109], v[130:133], v[190:193], v[106:109]
	v_mfma_i32_16x16x64_i8 v[66:69], v[126:129], v[162:165], v[66:69]
	v_mfma_i32_16x16x64_i8 v[70:73], v[154:157], v[162:165], v[70:73]
	v_mfma_i32_16x16x64_i8 v[58:61], v[126:129], v[170:173], v[58:61]
	v_mfma_i32_16x16x64_i8 v[62:65], v[154:157], v[170:173], v[62:65]
	v_mfma_i32_16x16x64_i8 v[46:49], v[126:129], v[178:181], v[46:49]
	v_mfma_i32_16x16x64_i8 v[54:57], v[154:157], v[178:181], v[54:57]
	v_mfma_i32_16x16x64_i8 v[34:37], v[126:129], v[186:189], v[34:37]
	v_mfma_i32_16x16x64_i8 v[38:41], v[154:157], v[186:189], v[38:41]
	v_mfma_i32_16x16x64_i8 v[66:69], v[134:137], v[166:169], v[66:69]
	v_mfma_i32_16x16x64_i8 v[70:73], v[158:161], v[166:169], v[70:73]
	v_mfma_i32_16x16x64_i8 v[58:61], v[134:137], v[174:177], v[58:61]
	v_mfma_i32_16x16x64_i8 v[62:65], v[158:161], v[174:177], v[62:65]
	v_mfma_i32_16x16x64_i8 v[46:49], v[134:137], v[182:185], v[46:49]
	v_mfma_i32_16x16x64_i8 v[54:57], v[158:161], v[182:185], v[54:57]
	v_mfma_i32_16x16x64_i8 v[34:37], v[134:137], v[190:193], v[34:37]
	v_mfma_i32_16x16x64_i8 v[38:41], v[158:161], v[190:193], v[38:41]
	s_setprio 0
	s_barrier
	s_mov_b32 m0, s45
	v_lshl_add_u64 v[216:217], v[244:245], 0, s[58:59]
	ds_read_b128 v[162:165], v242 offset:49152
	ds_read_b128 v[166:169], v242 offset:50176
	ds_read_b128 v[170:173], v242 offset:51200
	ds_read_b128 v[174:177], v242 offset:52224
	ds_read_b128 v[178:181], v242 offset:53248
	ds_read_b128 v[182:185], v242 offset:54272
	ds_read_b128 v[186:189], v242 offset:55296
	ds_read_b128 v[190:193], v242 offset:56320
	global_load_lds_dwordx4 v[216:217], off
	v_lshl_add_u64 v[216:217], v[246:247], 0, s[58:59]
	s_mov_b32 m0, s46
	v_lshl_add_u64 v[194:195], v[194:195], 0, s[58:59]
	global_load_lds_dwordx4 v[216:217], off
	v_lshl_add_u64 v[216:217], v[218:219], 0, s[62:63]
	v_lshl_add_u64 v[218:219], v[216:217], 0, v[198:199]
	s_mov_b32 m0, s51
	v_lshl_add_u64 v[216:217], v[216:217], 0, v[196:197]
	global_load_lds_dwordx4 v[218:219], off
	s_mov_b32 m0, s57
	s_nop 0
	global_load_lds_dwordx4 v[216:217], off
	s_mov_b32 m0, s47
	s_nop 0
	global_load_lds_dwordx4 v[194:195], off
	v_lshl_add_u64 v[194:195], v[248:249], 0, s[58:59]
	s_mov_b32 m0, s48
	s_nop 0
	global_load_lds_dwordx4 v[194:195], off
	s_waitcnt vmcnt(8)
	s_waitcnt lgkmcnt(0)
	s_barrier
	s_setprio 1
	s_waitcnt lgkmcnt(0)
	v_mfma_i32_16x16x64_i8 v[102:105], v[122:125], v[162:165], v[102:105]
	v_mfma_i32_16x16x64_i8 v[94:97], v[122:125], v[170:173], v[94:97]
	v_mfma_i32_16x16x64_i8 v[86:89], v[122:125], v[178:181], v[86:89]
	v_mfma_i32_16x16x64_i8 v[78:81], v[122:125], v[186:189], v[78:81]
	v_mfma_i32_16x16x64_i8 v[102:105], v[42:45], v[166:169], v[102:105]
	v_mfma_i32_16x16x64_i8 v[98:101], v[50:53], v[162:165], v[98:101]
	v_mfma_i32_16x16x64_i8 v[94:97], v[42:45], v[174:177], v[94:97]
	v_mfma_i32_16x16x64_i8 v[90:93], v[50:53], v[170:173], v[90:93]
	v_mfma_i32_16x16x64_i8 v[86:89], v[42:45], v[182:185], v[86:89]
	v_mfma_i32_16x16x64_i8 v[82:85], v[50:53], v[178:181], v[82:85]
	v_mfma_i32_16x16x64_i8 v[78:81], v[42:45], v[190:193], v[78:81]
	v_mfma_i32_16x16x64_i8 v[42:45], v[50:53], v[186:189], v[74:77]
	v_mfma_i32_16x16x64_i8 v[98:101], v[130:133], v[166:169], v[98:101]
	v_mfma_i32_16x16x64_i8 v[90:93], v[130:133], v[174:177], v[90:93]
	v_mfma_i32_16x16x64_i8 v[82:85], v[130:133], v[182:185], v[82:85]
	v_mfma_i32_16x16x64_i8 v[74:77], v[130:133], v[190:193], v[42:45]
	v_mfma_i32_16x16x64_i8 v[24:27], v[126:129], v[162:165], v[24:27]
	v_mfma_i32_16x16x64_i8 v[28:31], v[154:157], v[162:165], v[28:31]
	v_mfma_i32_16x16x64_i8 v[16:19], v[126:129], v[170:173], v[16:19]
	v_mfma_i32_16x16x64_i8 v[20:23], v[154:157], v[170:173], v[20:23]
	v_mfma_i32_16x16x64_i8 v[8:11], v[126:129], v[178:181], v[8:11]
	v_mfma_i32_16x16x64_i8 v[12:15], v[154:157], v[178:181], v[12:15]
	v_mfma_i32_16x16x64_i8 v[0:3], v[126:129], v[186:189], v[0:3]
	v_mfma_i32_16x16x64_i8 v[4:7], v[154:157], v[186:189], v[4:7]
	v_mfma_i32_16x16x64_i8 v[24:27], v[134:137], v[166:169], v[24:27]
	v_mfma_i32_16x16x64_i8 v[28:31], v[158:161], v[166:169], v[28:31]
	v_mfma_i32_16x16x64_i8 v[16:19], v[134:137], v[174:177], v[16:19]
	v_mfma_i32_16x16x64_i8 v[20:23], v[158:161], v[174:177], v[20:23]
	v_mfma_i32_16x16x64_i8 v[8:11], v[134:137], v[182:185], v[8:11]
	v_mfma_i32_16x16x64_i8 v[12:15], v[158:161], v[182:185], v[12:15]
	v_mfma_i32_16x16x64_i8 v[0:3], v[134:137], v[190:193], v[0:3]
	v_mfma_i32_16x16x64_i8 v[4:7], v[158:161], v[190:193], v[4:7]
	s_setprio 0
	s_barrier
	s_add_i32 s89, s89, 2
	s_add_u32 s24, s24, 0x100
	s_addc_u32 s25, s25, 0
	s_cmp_gt_u32 s89, 5
	v_lshl_add_u64 v[214:215], v[214:215], 0, s[54:55]
	s_cbranch_scc1 .LBB0_581

; #define LAS __attribute__((address_space(3)))
; #define PG8_STAGE(bufoff, gbase, voff) do { _Pragma("unroll") for (int _i = 0; _i < 2; ++_i) \
;         __builtin_amdgcn_global_load_lds((const unsigned*)((const char*)(gbase) + (voff)[_i]), (LAS unsigned*)(lds + (bufoff) + ldsw + _i * 8192), 16, 0, 0); } while (0)
; #define PG8_LDA(dst, b, h) do { _Pragma("unroll") for (int m = 0; m < 4; ++m) PG8_LD2(dst[m], PG8_SA(b, h) + aoff + m * 2048); } while (0)
; #define PG8_LDB(dst, b, h) do { _Pragma("unroll") for (int n = 0; n < 2; ++n) PG8_LD2(dst[n], PG8_SB(b, h) + boff + n * 2048); } while (0)
; #define PG8_BAR __builtin_amdgcn_s_barrier()
; template <int DT  , class Epi, class Sched, class Hook = NoHook>
; __device__ __forceinline__ void gemm_phase(LAS unsigned char* lds, const Sched& S, const Epi& E, int wave_s, LAS unsigned char* aux  ,
;                                            const Hook& H = Hook()  ) {
;     ...
;         const bool has_next = S.next(ui + 1, nxt);
;         const char* nA = has_next ? S.aptr(nxt) : cA; const char* nB = has_next ? S.bptr(nxt) : cB;
;         {
;             if constexpr (GATHER) { if (has_next && wid == 0) __builtin_amdgcn_global_load_lds((const unsigned*)(S.list_src(nxt) + 4 * lane), (LAS unsigned*)(aux + ((ui + 1) & 1) * 1024), 16, 0, 0); }
;             if constexpr (Epi::PREFETCH) E.prefetch(cur, aux + 2048 + (ui & 1) * 3072, wid, lane);
;         }
;         for (int t = 0; t < nt; t += 2) {
;             const bool last = (t == nt - 2);
;             const char* a1 = cA + (size_t)(t + 1) * kstep;
;             const char* a2 = last ? nA : cA + (size_t)(t + 2) * kstep; const char* b2 = last ? nB : cB + (size_t)(t + 2) * kstep;
;             const char* a3 = a2 + kstep; const char* b3 = b2 + kstep;
;             PG8_LDB(B0, 0, 0); PG8_LDB(B1, 0, 1); PG8_SCHED; PG8_LDA(At, 0, 0); PG8_STAGE_A(PG8_SA(1, 1), 1, a1);
;             if (GATHER) { if (last && has_next) S.gather_lds(nxt, gA, tid, aux + ((ui + 1) & 1) * 1024); }
;             PG8_WAIT_V(8); PG8_WAIT_L(0); PG8_BAR; PG8_MMA(0, 0, At, B0); PG8_MMA(0, 1, At, B1); PG8_BAR; PG8_SCHED;
;             PG8_LDA(At, 0, 1); PG8_STAGE(PG8_SB(0, 0), b2, voffB); PG8_STAGE(PG8_SB(0, 1), b2 + hstep, voffB); PG8_STAGE_A(PG8_SA(0, 0), 0, a2);
;             PG8_WAIT_V(8); PG8_WAIT_L(0); PG8_BAR; PG8_MMA(1, 0, At, B0); PG8_MMA(1, 1, At, B1); PG8_BAR; PG8_SCHED;
.LBB0_650:
	s_ashr_i32 s15, s14, 31
	s_lshl_b64 s[18:19], s[14:15], 18
	v_readlane_b32 s20, v253, 44
	v_readlane_b32 s21, v253, 45
	s_add_u32 s20, s20, s18
	s_addc_u32 s21, s21, s19
	s_and_b64 s[18:19], s[24:25], exec
	s_cselect_b32 s15, s21, s23
	s_cselect_b32 s24, s20, s22
	s_add_u32 s22, s22, 0x20080
	s_addc_u32 s23, s23, 0
	v_lshl_add_u64 v[180:181], v[0:1], 0, s[54:55]
	s_mov_b32 s25, -2
	ds_read_b128 v[28:31], v197
	ds_read_b128 v[16:19], v198
	ds_read_b128 v[24:27], v171
	ds_read_b128 v[0:3], v192
	ds_read_b128 v[20:23], v199
	ds_read_b128 v[4:7], v200
	ds_read_b128 v[8:11], v201
	ds_read_b128 v[12:15], v202
	s_add_u32 s18, s22, 0xfffe0080
	s_addc_u32 s19, s23, -1
	s_cmp_eq_u32 s25, 4
	s_cselect_b64 vcc, -1, 0
	s_cselect_b32 s19, s15, s19
	s_cselect_b32 s18, s24, s18
	v_cndmask_b32_e32 v183, v181, v179, vcc
	v_cndmask_b32_e32 v182, v180, v178, vcc
	v_lshl_add_u64 v[194:195], s[22:23], 0, v[172:173]
	s_add_i32 m0, s28, 0xc000
	ds_read_b128 v[184:187], v210
	ds_read_b128 v[188:191], v210 offset:1024
	ds_read_b128 v[226:229], v210 offset:2048
	ds_read_b128 v[230:233], v210 offset:3072
	ds_read_b128 v[234:237], v210 offset:4096
	ds_read_b128 v[238:241], v210 offset:5120
	ds_read_b128 v[242:245], v210 offset:6144
	ds_read_b128 v[246:249], v210 offset:7168
	global_load_lds_dwordx4 v[194:195], off
	v_lshl_add_u64 v[194:195], s[22:23], 0, v[174:175]
	s_add_i32 m0, s28, 0xe000
	s_nop 0
	global_load_lds_dwordx4 v[194:195], off
	s_waitcnt vmcnt(8)
	s_waitcnt lgkmcnt(0)
	s_barrier
	s_setprio 1
	s_waitcnt lgkmcnt(0)
	v_mfma_scale_f32_16x16x128_f8f6f4 v[154:157], v[24:31], v[184:191], 0, v220, v220 op_sel_hi:[0,0,0]
	v_mfma_scale_f32_16x16x128_f8f6f4 v[158:161], v[16:23], v[184:191], 0, v220, v220 op_sel_hi:[0,0,0]
	v_mfma_scale_f32_16x16x128_f8f6f4 v[138:141], v[24:31], v[226:233], 0, v220, v220 op_sel_hi:[0,0,0]
	v_mfma_scale_f32_16x16x128_f8f6f4 v[142:145], v[16:23], v[226:233], 0, v220, v220 op_sel_hi:[0,0,0]
	v_mfma_scale_f32_16x16x128_f8f6f4 v[122:125], v[24:31], v[234:241], 0, v220, v220 op_sel_hi:[0,0,0]
	v_mfma_scale_f32_16x16x128_f8f6f4 v[126:129], v[16:23], v[234:241], 0, v220, v220 op_sel_hi:[0,0,0]
	v_mfma_scale_f32_16x16x128_f8f6f4 v[106:109], v[24:31], v[242:249], 0, v220, v220 op_sel_hi:[0,0,0]
	v_mfma_scale_f32_16x16x128_f8f6f4 v[110:113], v[16:23], v[242:249], 0, v220, v220 op_sel_hi:[0,0,0]
	v_mfma_scale_f32_16x16x128_f8f6f4 v[146:149], v[0:7], v[184:191], 0, v220, v220 op_sel_hi:[0,0,0]
	v_mfma_scale_f32_16x16x128_f8f6f4 v[150:153], v[8:15], v[184:191], 0, v220, v220 op_sel_hi:[0,0,0]
	v_mfma_scale_f32_16x16x128_f8f6f4 v[130:133], v[0:7], v[226:233], 0, v220, v220 op_sel_hi:[0,0,0]
	v_mfma_scale_f32_16x16x128_f8f6f4 v[134:137], v[8:15], v[226:233], 0, v220, v220 op_sel_hi:[0,0,0]
	v_mfma_scale_f32_16x16x128_f8f6f4 v[114:117], v[0:7], v[234:241], 0, v220, v220 op_sel_hi:[0,0,0]
	v_mfma_scale_f32_16x16x128_f8f6f4 v[118:121], v[8:15], v[234:241], 0, v220, v220 op_sel_hi:[0,0,0]
	v_mfma_scale_f32_16x16x128_f8f6f4 v[98:101], v[0:7], v[242:249], 0, v220, v220 op_sel_hi:[0,0,0]
	v_mfma_scale_f32_16x16x128_f8f6f4 v[102:105], v[8:15], v[242:249], 0, v220, v220 op_sel_hi:[0,0,0]
	s_setprio 0
	s_barrier
	s_mov_b32 m0, s29
	v_lshl_add_u64 v[184:185], v[182:183], 0, v[166:167]
	ds_read_b128 v[226:229], v210 offset:16384
	ds_read_b128 v[230:233], v210 offset:17408
	ds_read_b128 v[234:237], v210 offset:18432
	ds_read_b128 v[238:241], v210 offset:19456
	ds_read_b128 v[242:245], v210 offset:20480
	ds_read_b128 v[246:249], v210 offset:21504
	ds_read_b128 v[212:215], v210 offset:22528
	ds_read_b128 v[216:219], v210 offset:23552
	global_load_lds_dwordx4 v[184:185], off
	v_lshl_add_u64 v[186:187], v[182:183], 0, v[162:163]
	s_mov_b32 m0, s30
	v_lshl_add_u64 v[188:189], v[182:183], 0, s[70:71]
	global_load_lds_dwordx4 v[186:187], off
	v_lshl_add_u64 v[190:191], v[188:189], 0, v[166:167]
	s_mov_b32 m0, s31
	v_lshl_add_u64 v[188:189], v[188:189], 0, v[162:163]
	global_load_lds_dwordx4 v[190:191], off
	s_mov_b32 m0, s33
	v_lshl_add_u64 v[190:191], s[18:19], 0, v[164:165]
	global_load_lds_dwordx4 v[188:189], off
	v_lshl_add_u64 v[188:189], s[18:19], 0, v[168:169]
	s_mov_b32 m0, s28
	s_nop 0
	global_load_lds_dwordx4 v[188:189], off
	s_mov_b32 m0, s34
	s_nop 0
	global_load_lds_dwordx4 v[190:191], off
	s_waitcnt vmcnt(8)
	s_waitcnt lgkmcnt(0)
	s_barrier
	s_setprio 1
	s_waitcnt lgkmcnt(0)
	v_mfma_scale_f32_16x16x128_f8f6f4 v[82:85], v[24:31], v[226:233], 0, v220, v220 op_sel_hi:[0,0,0]
	v_mfma_scale_f32_16x16x128_f8f6f4 v[86:89], v[16:23], v[226:233], 0, v220, v220 op_sel_hi:[0,0,0]
	v_mfma_scale_f32_16x16x128_f8f6f4 v[66:69], v[24:31], v[234:241], 0, v220, v220 op_sel_hi:[0,0,0]
	v_mfma_scale_f32_16x16x128_f8f6f4 v[70:73], v[16:23], v[234:241], 0, v220, v220 op_sel_hi:[0,0,0]
	v_mfma_scale_f32_16x16x128_f8f6f4 v[50:53], v[24:31], v[242:249], 0, v220, v220 op_sel_hi:[0,0,0]
	v_mfma_scale_f32_16x16x128_f8f6f4 v[54:57], v[16:23], v[242:249], 0, v220, v220 op_sel_hi:[0,0,0]
	v_mfma_scale_f32_16x16x128_f8f6f4 v[24:27], v[24:31], v[212:219], 0, v220, v220 op_sel_hi:[0,0,0]
	v_mfma_scale_f32_16x16x128_f8f6f4 v[16:19], v[16:23], v[212:219], 0, v220, v220 op_sel_hi:[0,0,0]
	v_mfma_scale_f32_16x16x128_f8f6f4 v[20:23], v[0:7], v[226:233], 0, v220, v220 op_sel_hi:[0,0,0]
	v_mfma_scale_f32_16x16x128_f8f6f4 v[28:31], v[8:15], v[226:233], 0, v220, v220 op_sel_hi:[0,0,0]
	v_mfma_scale_f32_16x16x128_f8f6f4 v[74:77], v[0:7], v[234:241], 0, v220, v220 op_sel_hi:[0,0,0]
	v_mfma_scale_f32_16x16x128_f8f6f4 v[78:81], v[8:15], v[234:241], 0, v220, v220 op_sel_hi:[0,0,0]
	v_mfma_scale_f32_16x16x128_f8f6f4 v[58:61], v[0:7], v[242:249], 0, v220, v220 op_sel_hi:[0,0,0]
	v_mfma_scale_f32_16x16x128_f8f6f4 v[62:65], v[8:15], v[242:249], 0, v220, v220 op_sel_hi:[0,0,0]
	v_mfma_scale_f32_16x16x128_f8f6f4 v[42:45], v[0:7], v[212:219], 0, v220, v220 op_sel_hi:[0,0,0]
	v_mfma_scale_f32_16x16x128_f8f6f4 v[46:49], v[8:15], v[212:219], 0, v220, v220 op_sel_hi:[0,0,0]
	s_setprio 0
	s_barrier
; #define PG8_STAGE(bufoff, gbase, voff) do { _Pragma("unroll") for (int _i = 0; _i < 2; ++_i) \
;         __builtin_amdgcn_global_load_lds((const unsigned*)((const char*)(gbase) + (voff)[_i]), (LAS unsigned*)(lds + (bufoff) + ldsw + _i * 8192), 16, 0, 0); } while (0)
; #define PG8_STAGE_A(bufoff, h, abase) do { _Pragma("unroll") for (int _i = 0; _i < 2; ++_i) { \
;         const char* _src = GATHER ? ((const char*)(abase) + gA[h][_i]) : ((const char*)(abase) + (size_t)(h) * hstep + voffA[_i]); \
;         __builtin_amdgcn_global_load_lds((const unsigned*)_src, (LAS unsigned*)(lds + (bufoff) + ldsw + _i * 8192), 16, 0, 0); } } while (0)
; #define PG8_LDA(dst, b, h) do { _Pragma("unroll") for (int m = 0; m < 4; ++m) PG8_LD2(dst[m], PG8_SA(b, h) + aoff + m * 2048); } while (0)
; #define PG8_LDB(dst, b, h) do { _Pragma("unroll") for (int n = 0; n < 2; ++n) PG8_LD2(dst[n], PG8_SB(b, h) + boff + n * 2048); } while (0)
; #define PG8_WAIT_V(n) asm volatile("s_waitcnt vmcnt(" #n ")" ::: "memory")
; #define PG8_WAIT_L(n) asm volatile("s_waitcnt lgkmcnt(" #n ")" ::: "memory")
; #define PG8_BAR __builtin_amdgcn_s_barrier()
; #define PG8_SCHED __builtin_amdgcn_sched_barrier(0)
; template <int DT  , class Epi, class Sched, class Hook = NoHook>
; __device__ __forceinline__ void gemm_phase(LAS unsigned char* lds, const Sched& S, const Epi& E, int wave_s, LAS unsigned char* aux  ,
;                                            const Hook& H = Hook()  ) {
;     ...
;             PG8_LDB(B0, 1, 0); PG8_LDB(B1, 1, 1); PG8_SCHED; PG8_LDA(At, 1, 0); PG8_STAGE_A(PG8_SA(0, 1), 1, a2);
;             PG8_WAIT_V(8); PG8_WAIT_L(0); PG8_BAR; PG8_MMA(0, 0, At, B0); PG8_MMA(0, 1, At, B1); PG8_BAR; PG8_SCHED;
;             PG8_LDA(At, 1, 1); PG8_STAGE(PG8_SB(1, 0), b3, voffB); PG8_STAGE(PG8_SB(1, 1), b3 + hstep, voffB); PG8_STAGE_A(PG8_SA(1, 0), 0, a3);
;             PG8_WAIT_V(8); PG8_WAIT_L(0); PG8_BAR; PG8_MMA(1, 0, At, B0); PG8_MMA(1, 1, At, B1); PG8_BAR; PG8_SCHED;
	ds_read_b128 v[38:41], v204
	ds_read_b128 v[90:93], v205
	ds_read_b128 v[34:37], v193
	ds_read_b128 v[0:3], v196
	ds_read_b128 v[94:97], v206
	ds_read_b128 v[4:7], v207
	ds_read_b128 v[8:11], v208
	ds_read_b128 v[12:15], v209
	s_add_u32 s18, s18, 0x20000
	s_addc_u32 s19, s19, 0
	s_mov_b32 m0, s35
	v_lshl_add_u64 v[194:195], s[18:19], 0, v[168:169]
	ds_read_b128 v[212:215], v210 offset:32768
	ds_read_b128 v[216:219], v210 offset:33792
	ds_read_b128 v[226:229], v210 offset:34816
	ds_read_b128 v[230:233], v210 offset:35840
	ds_read_b128 v[234:237], v210 offset:36864
	ds_read_b128 v[238:241], v210 offset:37888
	ds_read_b128 v[242:245], v210 offset:38912
	ds_read_b128 v[246:249], v210 offset:39936
	global_load_lds_dwordx4 v[194:195], off
	v_lshl_add_u64 v[194:195], s[18:19], 0, v[164:165]
	s_mov_b32 m0, s38
	s_nop 0
	global_load_lds_dwordx4 v[194:195], off
	s_waitcnt vmcnt(8)
	s_waitcnt lgkmcnt(0)
	s_barrier
	s_setprio 1
	s_waitcnt lgkmcnt(0)
	v_mfma_scale_f32_16x16x128_f8f6f4 v[154:157], v[34:41], v[212:219], v[154:157], v220, v220 op_sel_hi:[0,0,0]
	v_mfma_scale_f32_16x16x128_f8f6f4 v[158:161], v[90:97], v[212:219], v[158:161], v220, v220 op_sel_hi:[0,0,0]
	v_mfma_scale_f32_16x16x128_f8f6f4 v[138:141], v[34:41], v[226:233], v[138:141], v220, v220 op_sel_hi:[0,0,0]
	v_mfma_scale_f32_16x16x128_f8f6f4 v[142:145], v[90:97], v[226:233], v[142:145], v220, v220 op_sel_hi:[0,0,0]
	v_mfma_scale_f32_16x16x128_f8f6f4 v[122:125], v[34:41], v[234:241], v[122:125], v220, v220 op_sel_hi:[0,0,0]
	v_mfma_scale_f32_16x16x128_f8f6f4 v[126:129], v[90:97], v[234:241], v[126:129], v220, v220 op_sel_hi:[0,0,0]
	v_mfma_scale_f32_16x16x128_f8f6f4 v[106:109], v[34:41], v[242:249], v[106:109], v220, v220 op_sel_hi:[0,0,0]
	v_mfma_scale_f32_16x16x128_f8f6f4 v[110:113], v[90:97], v[242:249], v[110:113], v220, v220 op_sel_hi:[0,0,0]
	v_mfma_scale_f32_16x16x128_f8f6f4 v[146:149], v[0:7], v[212:219], v[146:149], v220, v220 op_sel_hi:[0,0,0]
	v_mfma_scale_f32_16x16x128_f8f6f4 v[150:153], v[8:15], v[212:219], v[150:153], v220, v220 op_sel_hi:[0,0,0]
	v_mfma_scale_f32_16x16x128_f8f6f4 v[130:133], v[0:7], v[226:233], v[130:133], v220, v220 op_sel_hi:[0,0,0]
	v_mfma_scale_f32_16x16x128_f8f6f4 v[134:137], v[8:15], v[226:233], v[134:137], v220, v220 op_sel_hi:[0,0,0]
	v_mfma_scale_f32_16x16x128_f8f6f4 v[114:117], v[0:7], v[234:241], v[114:117], v220, v220 op_sel_hi:[0,0,0]
	v_mfma_scale_f32_16x16x128_f8f6f4 v[118:121], v[8:15], v[234:241], v[118:121], v220, v220 op_sel_hi:[0,0,0]
	v_mfma_scale_f32_16x16x128_f8f6f4 v[98:101], v[0:7], v[242:249], v[98:101], v220, v220 op_sel_hi:[0,0,0]
	v_mfma_scale_f32_16x16x128_f8f6f4 v[102:105], v[8:15], v[242:249], v[102:105], v220, v220 op_sel_hi:[0,0,0]
	s_setprio 0
	s_barrier
	s_mov_b32 m0, s40
	v_lshl_add_u64 v[184:185], v[184:185], 0, s[58:59]
	ds_read_b128 v[212:215], v210 offset:49152
	ds_read_b128 v[216:219], v210 offset:50176
	ds_read_b128 v[226:229], v210 offset:51200
	ds_read_b128 v[230:233], v210 offset:52224
	ds_read_b128 v[234:237], v210 offset:53248
	ds_read_b128 v[238:241], v210 offset:54272
	ds_read_b128 v[242:245], v210 offset:55296
	ds_read_b128 v[246:249], v210 offset:56320
	global_load_lds_dwordx4 v[184:185], off
	v_lshl_add_u64 v[184:185], v[186:187], 0, s[58:59]
	s_mov_b32 m0, s41
	v_lshl_add_u64 v[182:183], v[182:183], 0, s[62:63]
	global_load_lds_dwordx4 v[184:185], off
	v_lshl_add_u64 v[184:185], v[182:183], 0, v[166:167]
	s_mov_b32 m0, s46
	v_lshl_add_u64 v[182:183], v[182:183], 0, v[162:163]
	global_load_lds_dwordx4 v[184:185], off
	s_mov_b32 m0, s47
	s_nop 0
	global_load_lds_dwordx4 v[182:183], off
	v_lshl_add_u64 v[182:183], v[188:189], 0, s[58:59]
	s_mov_b32 m0, s44
	s_nop 0
	global_load_lds_dwordx4 v[182:183], off
	v_lshl_add_u64 v[182:183], v[190:191], 0, s[58:59]
	s_mov_b32 m0, s45
	s_nop 0
	global_load_lds_dwordx4 v[182:183], off
	s_waitcnt vmcnt(8)
	s_waitcnt lgkmcnt(0)
	s_barrier
	s_setprio 1
	s_waitcnt lgkmcnt(0)
	v_mfma_scale_f32_16x16x128_f8f6f4 v[82:85], v[34:41], v[212:219], v[82:85], v220, v220 op_sel_hi:[0,0,0]
	v_mfma_scale_f32_16x16x128_f8f6f4 v[86:89], v[90:97], v[212:219], v[86:89], v220, v220 op_sel_hi:[0,0,0]
	v_mfma_scale_f32_16x16x128_f8f6f4 v[66:69], v[34:41], v[226:233], v[66:69], v220, v220 op_sel_hi:[0,0,0]
	v_mfma_scale_f32_16x16x128_f8f6f4 v[70:73], v[90:97], v[226:233], v[70:73], v220, v220 op_sel_hi:[0,0,0]
	v_mfma_scale_f32_16x16x128_f8f6f4 v[50:53], v[34:41], v[234:241], v[50:53], v220, v220 op_sel_hi:[0,0,0]
	v_mfma_scale_f32_16x16x128_f8f6f4 v[54:57], v[90:97], v[234:241], v[54:57], v220, v220 op_sel_hi:[0,0,0]
	v_mfma_scale_f32_16x16x128_f8f6f4 v[34:37], v[34:41], v[242:249], v[24:27], v220, v220 op_sel_hi:[0,0,0]
	v_mfma_scale_f32_16x16x128_f8f6f4 v[38:41], v[90:97], v[242:249], v[16:19], v220, v220 op_sel_hi:[0,0,0]
	v_mfma_scale_f32_16x16x128_f8f6f4 v[90:93], v[0:7], v[212:219], v[20:23], v220, v220 op_sel_hi:[0,0,0]
	v_mfma_scale_f32_16x16x128_f8f6f4 v[94:97], v[8:15], v[212:219], v[28:31], v220, v220 op_sel_hi:[0,0,0]
	v_mfma_scale_f32_16x16x128_f8f6f4 v[74:77], v[0:7], v[226:233], v[74:77], v220, v220 op_sel_hi:[0,0,0]
	v_mfma_scale_f32_16x16x128_f8f6f4 v[78:81], v[8:15], v[226:233], v[78:81], v220, v220 op_sel_hi:[0,0,0]
	v_mfma_scale_f32_16x16x128_f8f6f4 v[58:61], v[0:7], v[234:241], v[58:61], v220, v220 op_sel_hi:[0,0,0]
	v_mfma_scale_f32_16x16x128_f8f6f4 v[62:65], v[8:15], v[234:241], v[62:65], v220, v220 op_sel_hi:[0,0,0]
	v_mfma_scale_f32_16x16x128_f8f6f4 v[42:45], v[0:7], v[242:249], v[42:45], v220, v220 op_sel_hi:[0,0,0]
	v_mfma_scale_f32_16x16x128_f8f6f4 v[46:49], v[8:15], v[242:249], v[46:49], v220, v220 op_sel_hi:[0,0,0]
	s_setprio 0
	s_barrier
	s_add_i32 s25, s25, 2
	s_add_u32 s22, s22, 0x100
	s_addc_u32 s23, s23, 0
	s_cmp_gt_u32 s25, 5
	v_lshl_add_u64 v[180:181], v[180:181], 0, s[54:55]
; #define PG8_STAGE(bufoff, gbase, voff) do { _Pragma("unroll") for (int _i = 0; _i < 2; ++_i) \
;         __builtin_amdgcn_global_load_lds((const unsigned*)((const char*)(gbase) + (voff)[_i]), (LAS unsigned*)(lds + (bufoff) + ldsw + _i * 8192), 16, 0, 0); } while (0)
; #define PG8_STAGE_A(bufoff, h, abase) do { _Pragma("unroll") for (int _i = 0; _i < 2; ++_i) { \
;         const char* _src = GATHER ? ((const char*)(abase) + gA[h][_i]) : ((const char*)(abase) + (size_t)(h) * hstep + voffA[_i]); \
;         __builtin_amdgcn_global_load_lds((const unsigned*)_src, (LAS unsigned*)(lds + (bufoff) + ldsw + _i * 8192), 16, 0, 0); } } while (0)
; #define PG8_LDA(dst, b, h) do { _Pragma("unroll") for (int m = 0; m < 4; ++m) PG8_LD2(dst[m], PG8_SA(b, h) + aoff + m * 2048); } while (0)
; #define PG8_WAIT_V(n) asm volatile("s_waitcnt vmcnt(" #n ")" ::: "memory")
; #define PG8_BAR __builtin_amdgcn_s_barrier()
; template <int DT  , class Epi, class Sched, class Hook = NoHook>
; __device__ __forceinline__ void gemm_phase(LAS unsigned char* lds, const Sched& S, const Epi& E, int wave_s, LAS unsigned char* aux  ,
;                                            const Hook& H = Hook()  ) {
;     ...
;         for (int t = 0; t < nt; t += 2) {
;             const bool last = (t == nt - 2);
;             const char* a1 = cA + (size_t)(t + 1) * kstep;
;             const char* a2 = last ? nA : cA + (size_t)(t + 2) * kstep; const char* b2 = last ? nB : cB + (size_t)(t + 2) * kstep;
;             const char* a3 = a2 + kstep; const char* b3 = b2 + kstep;
;             PG8_LDB(B0, 0, 0); PG8_LDB(B1, 0, 1); PG8_SCHED; PG8_LDA(At, 0, 0); PG8_STAGE_A(PG8_SA(1, 1), 1, a1);
;             if (GATHER) { if (last && has_next) S.gather_lds(nxt, gA, tid, aux + ((ui + 1) & 1) * 1024); }
;             PG8_WAIT_V(8); PG8_WAIT_L(0); PG8_BAR; PG8_MMA(0, 0, At, B0); PG8_MMA(0, 1, At, B1); PG8_BAR; PG8_SCHED;
;             PG8_LDA(At, 0, 1); PG8_STAGE(PG8_SB(0, 0), b2, voffB); PG8_STAGE(PG8_SB(0, 1), b2 + hstep, voffB); PG8_STAGE_A(PG8_SA(0, 0), 0, a2);
;             PG8_WAIT_V(8); PG8_WAIT_L(0); PG8_BAR; PG8_MMA(1, 0, At, B0); PG8_MMA(1, 1, At, B1); PG8_BAR; PG8_SCHED;
;             PG8_LDB(B0, 1, 0); PG8_LDB(B1, 1, 1); PG8_SCHED; PG8_LDA(At, 1, 0); PG8_STAGE_A(PG8_SA(0, 1), 1, a2);
;             PG8_WAIT_V(8); PG8_WAIT_L(0); PG8_BAR; PG8_MMA(0, 0, At, B0); PG8_MMA(0, 1, At, B1); PG8_BAR; PG8_SCHED;
.LBB0_651:
	ds_read_b128 v[28:31], v197
	ds_read_b128 v[16:19], v198
	ds_read_b128 v[24:27], v171
	ds_read_b128 v[0:3], v192
	ds_read_b128 v[20:23], v199
	ds_read_b128 v[4:7], v200
	ds_read_b128 v[8:11], v201
	ds_read_b128 v[12:15], v202
	s_add_u32 s18, s22, 0xfffe0080
	s_addc_u32 s19, s23, -1
	s_cmp_eq_u32 s25, 4
	s_cselect_b64 vcc, -1, 0
	s_cselect_b32 s19, s15, s19
	s_cselect_b32 s18, s24, s18
	v_cndmask_b32_e32 v183, v181, v179, vcc
	v_cndmask_b32_e32 v182, v180, v178, vcc
	v_lshl_add_u64 v[194:195], s[22:23], 0, v[172:173]
	s_add_i32 m0, s28, 0xc000
	ds_read_b128 v[184:187], v210
	ds_read_b128 v[188:191], v210 offset:1024
	ds_read_b128 v[226:229], v210 offset:2048
	ds_read_b128 v[230:233], v210 offset:3072
	ds_read_b128 v[234:237], v210 offset:4096
	ds_read_b128 v[238:241], v210 offset:5120
	ds_read_b128 v[242:245], v210 offset:6144
	ds_read_b128 v[246:249], v210 offset:7168
	global_load_lds_dwordx4 v[194:195], off
	v_lshl_add_u64 v[194:195], s[22:23], 0, v[174:175]
	s_add_i32 m0, s28, 0xe000
	s_nop 0
	global_load_lds_dwordx4 v[194:195], off
	s_waitcnt vmcnt(8)
	s_waitcnt lgkmcnt(0)
	s_barrier
	s_setprio 1
	s_waitcnt lgkmcnt(0)
	v_mfma_scale_f32_16x16x128_f8f6f4 v[154:157], v[24:31], v[184:191], v[154:157], v220, v220 op_sel_hi:[0,0,0]
	v_mfma_scale_f32_16x16x128_f8f6f4 v[158:161], v[16:23], v[184:191], v[158:161], v220, v220 op_sel_hi:[0,0,0]
	v_mfma_scale_f32_16x16x128_f8f6f4 v[138:141], v[24:31], v[226:233], v[138:141], v220, v220 op_sel_hi:[0,0,0]
	v_mfma_scale_f32_16x16x128_f8f6f4 v[142:145], v[16:23], v[226:233], v[142:145], v220, v220 op_sel_hi:[0,0,0]
	v_mfma_scale_f32_16x16x128_f8f6f4 v[122:125], v[24:31], v[234:241], v[122:125], v220, v220 op_sel_hi:[0,0,0]
	v_mfma_scale_f32_16x16x128_f8f6f4 v[126:129], v[16:23], v[234:241], v[126:129], v220, v220 op_sel_hi:[0,0,0]
	v_mfma_scale_f32_16x16x128_f8f6f4 v[106:109], v[24:31], v[242:249], v[106:109], v220, v220 op_sel_hi:[0,0,0]
	v_mfma_scale_f32_16x16x128_f8f6f4 v[110:113], v[16:23], v[242:249], v[110:113], v220, v220 op_sel_hi:[0,0,0]
	v_mfma_scale_f32_16x16x128_f8f6f4 v[146:149], v[0:7], v[184:191], v[146:149], v220, v220 op_sel_hi:[0,0,0]
	v_mfma_scale_f32_16x16x128_f8f6f4 v[150:153], v[8:15], v[184:191], v[150:153], v220, v220 op_sel_hi:[0,0,0]
	v_mfma_scale_f32_16x16x128_f8f6f4 v[130:133], v[0:7], v[226:233], v[130:133], v220, v220 op_sel_hi:[0,0,0]
	v_mfma_scale_f32_16x16x128_f8f6f4 v[134:137], v[8:15], v[226:233], v[134:137], v220, v220 op_sel_hi:[0,0,0]
	v_mfma_scale_f32_16x16x128_f8f6f4 v[114:117], v[0:7], v[234:241], v[114:117], v220, v220 op_sel_hi:[0,0,0]
	v_mfma_scale_f32_16x16x128_f8f6f4 v[118:121], v[8:15], v[234:241], v[118:121], v220, v220 op_sel_hi:[0,0,0]
	v_mfma_scale_f32_16x16x128_f8f6f4 v[98:101], v[0:7], v[242:249], v[98:101], v220, v220 op_sel_hi:[0,0,0]
	v_mfma_scale_f32_16x16x128_f8f6f4 v[102:105], v[8:15], v[242:249], v[102:105], v220, v220 op_sel_hi:[0,0,0]
	s_setprio 0
	s_barrier
	s_mov_b32 m0, s29
	v_lshl_add_u64 v[184:185], v[182:183], 0, v[166:167]
	ds_read_b128 v[226:229], v210 offset:16384
	ds_read_b128 v[230:233], v210 offset:17408
	ds_read_b128 v[234:237], v210 offset:18432
	ds_read_b128 v[238:241], v210 offset:19456
	ds_read_b128 v[242:245], v210 offset:20480
	ds_read_b128 v[246:249], v210 offset:21504
	ds_read_b128 v[212:215], v210 offset:22528
	ds_read_b128 v[216:219], v210 offset:23552
	global_load_lds_dwordx4 v[184:185], off
	v_lshl_add_u64 v[186:187], v[182:183], 0, v[162:163]
	s_mov_b32 m0, s30
	v_lshl_add_u64 v[188:189], v[182:183], 0, s[70:71]
	global_load_lds_dwordx4 v[186:187], off
	v_lshl_add_u64 v[190:191], v[188:189], 0, v[166:167]
	s_mov_b32 m0, s31
	v_lshl_add_u64 v[188:189], v[188:189], 0, v[162:163]
	global_load_lds_dwordx4 v[190:191], off
	s_mov_b32 m0, s33
	v_lshl_add_u64 v[190:191], s[18:19], 0, v[164:165]
	global_load_lds_dwordx4 v[188:189], off
	v_lshl_add_u64 v[188:189], s[18:19], 0, v[168:169]
	s_mov_b32 m0, s28
	s_nop 0
	global_load_lds_dwordx4 v[188:189], off
	s_mov_b32 m0, s34
	s_nop 0
	global_load_lds_dwordx4 v[190:191], off
	s_waitcnt vmcnt(8)
	s_waitcnt lgkmcnt(0)
	s_barrier
	s_setprio 1
	s_waitcnt lgkmcnt(0)
	v_mfma_scale_f32_16x16x128_f8f6f4 v[82:85], v[24:31], v[226:233], v[82:85], v220, v220 op_sel_hi:[0,0,0]
	v_mfma_scale_f32_16x16x128_f8f6f4 v[86:89], v[16:23], v[226:233], v[86:89], v220, v220 op_sel_hi:[0,0,0]
	v_mfma_scale_f32_16x16x128_f8f6f4 v[66:69], v[24:31], v[234:241], v[66:69], v220, v220 op_sel_hi:[0,0,0]
	v_mfma_scale_f32_16x16x128_f8f6f4 v[70:73], v[16:23], v[234:241], v[70:73], v220, v220 op_sel_hi:[0,0,0]
	v_mfma_scale_f32_16x16x128_f8f6f4 v[50:53], v[24:31], v[242:249], v[50:53], v220, v220 op_sel_hi:[0,0,0]
	v_mfma_scale_f32_16x16x128_f8f6f4 v[54:57], v[16:23], v[242:249], v[54:57], v220, v220 op_sel_hi:[0,0,0]
	v_mfma_scale_f32_16x16x128_f8f6f4 v[24:27], v[24:31], v[212:219], v[34:37], v220, v220 op_sel_hi:[0,0,0]
	v_mfma_scale_f32_16x16x128_f8f6f4 v[16:19], v[16:23], v[212:219], v[38:41], v220, v220 op_sel_hi:[0,0,0]
	v_mfma_scale_f32_16x16x128_f8f6f4 v[20:23], v[0:7], v[226:233], v[90:93], v220, v220 op_sel_hi:[0,0,0]
	v_mfma_scale_f32_16x16x128_f8f6f4 v[28:31], v[8:15], v[226:233], v[94:97], v220, v220 op_sel_hi:[0,0,0]
	v_mfma_scale_f32_16x16x128_f8f6f4 v[74:77], v[0:7], v[234:241], v[74:77], v220, v220 op_sel_hi:[0,0,0]
	v_mfma_scale_f32_16x16x128_f8f6f4 v[78:81], v[8:15], v[234:241], v[78:81], v220, v220 op_sel_hi:[0,0,0]
	v_mfma_scale_f32_16x16x128_f8f6f4 v[58:61], v[0:7], v[242:249], v[58:61], v220, v220 op_sel_hi:[0,0,0]
	v_mfma_scale_f32_16x16x128_f8f6f4 v[62:65], v[8:15], v[242:249], v[62:65], v220, v220 op_sel_hi:[0,0,0]
	v_mfma_scale_f32_16x16x128_f8f6f4 v[42:45], v[0:7], v[212:219], v[42:45], v220, v220 op_sel_hi:[0,0,0]
	v_mfma_scale_f32_16x16x128_f8f6f4 v[46:49], v[8:15], v[212:219], v[46:49], v220, v220 op_sel_hi:[0,0,0]
	s_setprio 0
	s_barrier
; #define PG8_STAGE(bufoff, gbase, voff) do { _Pragma("unroll") for (int _i = 0; _i < 2; ++_i) \
;         __builtin_amdgcn_global_load_lds((const unsigned*)((const char*)(gbase) + (voff)[_i]), (LAS unsigned*)(lds + (bufoff) + ldsw + _i * 8192), 16, 0, 0); } while (0)
; #define PG8_LDA(dst, b, h) do { _Pragma("unroll") for (int m = 0; m < 4; ++m) PG8_LD2(dst[m], PG8_SA(b, h) + aoff + m * 2048); } while (0)
; #define PG8_LDB(dst, b, h) do { _Pragma("unroll") for (int n = 0; n < 2; ++n) PG8_LD2(dst[n], PG8_SB(b, h) + boff + n * 2048); } while (0)
; #define PG8_WAIT_V(n) asm volatile("s_waitcnt vmcnt(" #n ")" ::: "memory")
; template <int DT  , class Epi, class Sched, class Hook = NoHook>
; __device__ __forceinline__ void gemm_phase(LAS unsigned char* lds, const Sched& S, const Epi& E, int wave_s, LAS unsigned char* aux  ,
;                                            const Hook& H = Hook()  ) {
;     ...
;         for (int t = 0; t < nt; t += 2) {
;             const bool last = (t == nt - 2);
;             const char* a1 = cA + (size_t)(t + 1) * kstep;
;             const char* a2 = last ? nA : cA + (size_t)(t + 2) * kstep; const char* b2 = last ? nB : cB + (size_t)(t + 2) * kstep;
;             const char* a3 = a2 + kstep; const char* b3 = b2 + kstep;
;             PG8_LDB(B0, 0, 0); PG8_LDB(B1, 0, 1); PG8_SCHED; PG8_LDA(At, 0, 0); PG8_STAGE_A(PG8_SA(1, 1), 1, a1);
;             if (GATHER) { if (last && has_next) S.gather_lds(nxt, gA, tid, aux + ((ui + 1) & 1) * 1024); }
;             PG8_WAIT_V(8); PG8_WAIT_L(0); PG8_BAR; PG8_MMA(0, 0, At, B0); PG8_MMA(0, 1, At, B1); PG8_BAR; PG8_SCHED;
;             PG8_LDA(At, 0, 1); PG8_STAGE(PG8_SB(0, 0), b2, voffB); PG8_STAGE(PG8_SB(0, 1), b2 + hstep, voffB); PG8_STAGE_A(PG8_SA(0, 0), 0, a2);
;             PG8_WAIT_V(8); PG8_WAIT_L(0); PG8_BAR; PG8_MMA(1, 0, At, B0); PG8_MMA(1, 1, At, B1); PG8_BAR; PG8_SCHED;
;             PG8_LDB(B0, 1, 0); PG8_LDB(B1, 1, 1); PG8_SCHED; PG8_LDA(At, 1, 0); PG8_STAGE_A(PG8_SA(0, 1), 1, a2);
;             PG8_WAIT_V(8); PG8_WAIT_L(0); PG8_BAR; PG8_MMA(0, 0, At, B0); PG8_MMA(0, 1, At, B1); PG8_BAR; PG8_SCHED;
;             PG8_LDA(At, 1, 1); PG8_STAGE(PG8_SB(1, 0), b3, voffB); PG8_STAGE(PG8_SB(1, 1), b3 + hstep, voffB); PG8_STAGE_A(PG8_SA(1, 0), 0, a3);
;             PG8_WAIT_V(8); PG8_WAIT_L(0); PG8_BAR; PG8_MMA(1, 0, At, B0); PG8_MMA(1, 1, At, B1); PG8_BAR; PG8_SCHED;
;         }
	ds_read_b128 v[38:41], v204
	ds_read_b128 v[90:93], v205
	ds_read_b128 v[34:37], v193
	ds_read_b128 v[0:3], v196
	ds_read_b128 v[94:97], v206
	ds_read_b128 v[4:7], v207
	ds_read_b128 v[8:11], v208
	ds_read_b128 v[12:15], v209
	s_add_u32 s18, s18, 0x20000
	s_addc_u32 s19, s19, 0
	s_mov_b32 m0, s35
	v_lshl_add_u64 v[194:195], s[18:19], 0, v[168:169]
	ds_read_b128 v[212:215], v210 offset:32768
	ds_read_b128 v[216:219], v210 offset:33792
	ds_read_b128 v[226:229], v210 offset:34816
	ds_read_b128 v[230:233], v210 offset:35840
	ds_read_b128 v[234:237], v210 offset:36864
	ds_read_b128 v[238:241], v210 offset:37888
	ds_read_b128 v[242:245], v210 offset:38912
	ds_read_b128 v[246:249], v210 offset:39936
	global_load_lds_dwordx4 v[194:195], off
	v_lshl_add_u64 v[194:195], s[18:19], 0, v[164:165]
	s_mov_b32 m0, s38
	s_nop 0
	global_load_lds_dwordx4 v[194:195], off
	s_waitcnt vmcnt(8)
	s_waitcnt lgkmcnt(0)
	s_barrier
	s_setprio 1
	s_waitcnt lgkmcnt(0)
	v_mfma_scale_f32_16x16x128_f8f6f4 v[154:157], v[34:41], v[212:219], v[154:157], v220, v220 op_sel_hi:[0,0,0]
	v_mfma_scale_f32_16x16x128_f8f6f4 v[158:161], v[90:97], v[212:219], v[158:161], v220, v220 op_sel_hi:[0,0,0]
	v_mfma_scale_f32_16x16x128_f8f6f4 v[138:141], v[34:41], v[226:233], v[138:141], v220, v220 op_sel_hi:[0,0,0]
	v_mfma_scale_f32_16x16x128_f8f6f4 v[142:145], v[90:97], v[226:233], v[142:145], v220, v220 op_sel_hi:[0,0,0]
	v_mfma_scale_f32_16x16x128_f8f6f4 v[122:125], v[34:41], v[234:241], v[122:125], v220, v220 op_sel_hi:[0,0,0]
	v_mfma_scale_f32_16x16x128_f8f6f4 v[126:129], v[90:97], v[234:241], v[126:129], v220, v220 op_sel_hi:[0,0,0]
	v_mfma_scale_f32_16x16x128_f8f6f4 v[106:109], v[34:41], v[242:249], v[106:109], v220, v220 op_sel_hi:[0,0,0]
	v_mfma_scale_f32_16x16x128_f8f6f4 v[110:113], v[90:97], v[242:249], v[110:113], v220, v220 op_sel_hi:[0,0,0]
	v_mfma_scale_f32_16x16x128_f8f6f4 v[146:149], v[0:7], v[212:219], v[146:149], v220, v220 op_sel_hi:[0,0,0]
	v_mfma_scale_f32_16x16x128_f8f6f4 v[150:153], v[8:15], v[212:219], v[150:153], v220, v220 op_sel_hi:[0,0,0]
	v_mfma_scale_f32_16x16x128_f8f6f4 v[130:133], v[0:7], v[226:233], v[130:133], v220, v220 op_sel_hi:[0,0,0]
	v_mfma_scale_f32_16x16x128_f8f6f4 v[134:137], v[8:15], v[226:233], v[134:137], v220, v220 op_sel_hi:[0,0,0]
	v_mfma_scale_f32_16x16x128_f8f6f4 v[114:117], v[0:7], v[234:241], v[114:117], v220, v220 op_sel_hi:[0,0,0]
	v_mfma_scale_f32_16x16x128_f8f6f4 v[118:121], v[8:15], v[234:241], v[118:121], v220, v220 op_sel_hi:[0,0,0]
	v_mfma_scale_f32_16x16x128_f8f6f4 v[98:101], v[0:7], v[242:249], v[98:101], v220, v220 op_sel_hi:[0,0,0]
	v_mfma_scale_f32_16x16x128_f8f6f4 v[102:105], v[8:15], v[242:249], v[102:105], v220, v220 op_sel_hi:[0,0,0]
	s_setprio 0
	s_barrier
	s_mov_b32 m0, s40
	v_lshl_add_u64 v[184:185], v[184:185], 0, s[58:59]
	ds_read_b128 v[212:215], v210 offset:49152
	ds_read_b128 v[216:219], v210 offset:50176
	ds_read_b128 v[226:229], v210 offset:51200
	ds_read_b128 v[230:233], v210 offset:52224
	ds_read_b128 v[234:237], v210 offset:53248
	ds_read_b128 v[238:241], v210 offset:54272
	ds_read_b128 v[242:245], v210 offset:55296
	ds_read_b128 v[246:249], v210 offset:56320
	global_load_lds_dwordx4 v[184:185], off
	v_lshl_add_u64 v[184:185], v[186:187], 0, s[58:59]
	s_mov_b32 m0, s41
	v_lshl_add_u64 v[182:183], v[182:183], 0, s[62:63]
	global_load_lds_dwordx4 v[184:185], off
	v_lshl_add_u64 v[184:185], v[182:183], 0, v[166:167]
	s_mov_b32 m0, s46
	v_lshl_add_u64 v[182:183], v[182:183], 0, v[162:163]
	global_load_lds_dwordx4 v[184:185], off
	s_mov_b32 m0, s47
	s_nop 0
	global_load_lds_dwordx4 v[182:183], off
	v_lshl_add_u64 v[182:183], v[188:189], 0, s[58:59]
	s_mov_b32 m0, s44
	s_nop 0
	global_load_lds_dwordx4 v[182:183], off
	v_lshl_add_u64 v[182:183], v[190:191], 0, s[58:59]
	s_mov_b32 m0, s45
	s_nop 0
	global_load_lds_dwordx4 v[182:183], off
	s_waitcnt vmcnt(8)
	s_waitcnt lgkmcnt(0)
	s_barrier
	s_setprio 1
	s_waitcnt lgkmcnt(0)
	v_mfma_scale_f32_16x16x128_f8f6f4 v[82:85], v[34:41], v[212:219], v[82:85], v220, v220 op_sel_hi:[0,0,0]
	v_mfma_scale_f32_16x16x128_f8f6f4 v[86:89], v[90:97], v[212:219], v[86:89], v220, v220 op_sel_hi:[0,0,0]
	v_mfma_scale_f32_16x16x128_f8f6f4 v[66:69], v[34:41], v[226:233], v[66:69], v220, v220 op_sel_hi:[0,0,0]
	v_mfma_scale_f32_16x16x128_f8f6f4 v[70:73], v[90:97], v[226:233], v[70:73], v220, v220 op_sel_hi:[0,0,0]
	v_mfma_scale_f32_16x16x128_f8f6f4 v[50:53], v[34:41], v[234:241], v[50:53], v220, v220 op_sel_hi:[0,0,0]
	v_mfma_scale_f32_16x16x128_f8f6f4 v[54:57], v[90:97], v[234:241], v[54:57], v220, v220 op_sel_hi:[0,0,0]
	v_mfma_scale_f32_16x16x128_f8f6f4 v[34:37], v[34:41], v[242:249], v[24:27], v220, v220 op_sel_hi:[0,0,0]
	v_mfma_scale_f32_16x16x128_f8f6f4 v[38:41], v[90:97], v[242:249], v[16:19], v220, v220 op_sel_hi:[0,0,0]
	v_mfma_scale_f32_16x16x128_f8f6f4 v[90:93], v[0:7], v[212:219], v[20:23], v220, v220 op_sel_hi:[0,0,0]
	v_mfma_scale_f32_16x16x128_f8f6f4 v[94:97], v[8:15], v[212:219], v[28:31], v220, v220 op_sel_hi:[0,0,0]
	v_mfma_scale_f32_16x16x128_f8f6f4 v[74:77], v[0:7], v[226:233], v[74:77], v220, v220 op_sel_hi:[0,0,0]
	v_mfma_scale_f32_16x16x128_f8f6f4 v[78:81], v[8:15], v[226:233], v[78:81], v220, v220 op_sel_hi:[0,0,0]
	v_mfma_scale_f32_16x16x128_f8f6f4 v[58:61], v[0:7], v[234:241], v[58:61], v220, v220 op_sel_hi:[0,0,0]
	v_mfma_scale_f32_16x16x128_f8f6f4 v[62:65], v[8:15], v[234:241], v[62:65], v220, v220 op_sel_hi:[0,0,0]
	v_mfma_scale_f32_16x16x128_f8f6f4 v[42:45], v[0:7], v[242:249], v[42:45], v220, v220 op_sel_hi:[0,0,0]
	v_mfma_scale_f32_16x16x128_f8f6f4 v[46:49], v[8:15], v[242:249], v[46:49], v220, v220 op_sel_hi:[0,0,0]
	s_setprio 0
	s_barrier
	s_add_i32 s25, s25, 2
	s_add_u32 s22, s22, 0x100
	s_addc_u32 s23, s23, 0
	s_cmp_gt_u32 s25, 5
	v_lshl_add_u64 v[180:181], v[180:181], 0, s[54:55]
	s_cbranch_scc0 .LBB0_651
	s_and_b64 vcc, exec, s[12:13]
	s_cbranch_vccz .LBB0_654
	s_barrier
